# speedup vs baseline: 1.1288x; 1.0132x over previous
.LBB1_26:
	s_waitcnt vmcnt(35)
	v_and_b32_e32 v113, 3, v0
	s_and_b32 s18, s2, 15
	v_cmp_eq_u32_e32 vcc, 0, v113
	v_cmp_gt_u32_e64 s[4:5], 12, v92
	s_and_b64 s[12:13], vcc, s[4:5]
	s_lshl_b32 s4, s3, 12
	s_lshl_b32 s5, s18, 8
	s_or_b32 s4, s4, s5
	s_mul_hi_i32 s5, s4, 0x6000
	s_mulk_i32 s4, 0x6000
	s_lshl_b32 s3, s3, 8
	s_add_u32 s16, s24, s4
	s_addc_u32 s17, s25, s5
	s_ashr_i32 s4, s21, 31
	s_lshr_b32 s4, s4, 29
	s_add_i32 s4, s21, s4
	s_ashr_i32 s19, s4, 3
	v_and_b32_e32 v101, 1, v74
	v_lshl_or_b32 v74, v91, 1, v95
	s_min_i32 s4, s19, 0xff
	v_mul_u32_u24_e32 v74, 0x60, v74
	v_lshlrev_b32_e32 v75, 1, v92
	s_mul_hi_i32 s5, s4, 0x6000
	s_mulk_i32 s4, 0x6000
	v_or3_b32 v88, v74, v75, v101
	s_add_u32 s4, s16, s4
	s_addc_u32 s5, s17, s5
	v_lshlrev_b64 v[102:103], 4, v[88:89]
	v_lshl_add_u64 v[104:105], s[4:5], 0, v[102:103]
	global_load_dwordx4 v[82:85], v[104:105], off
	global_load_dwordx4 v[74:77], v[104:105], off offset:512
	global_load_dwordx4 v[78:81], v[104:105], off offset:1024
	s_waitcnt vmcnt(5)
	v_mul_f32_e32 v88, 0xbfb8aa3b, v97
	v_mul_f32_e32 v99, 0x3c91a2b4, v88
	s_waitcnt vmcnt(4)
	v_mul_f32_e32 v88, 0x4038aa3b, v96
	v_mul_f32_e32 v104, 0x3c91a2b4, v88
	v_lshrrev_b32_e32 v88, 2, v92
	v_and_b32_e32 v92, 4, v92
	v_cmp_lt_u32_e64 s[4:5], 1, v93
	v_mov_b32_e32 v93, 0xd0
	v_cmp_ne_u32_e32 vcc, 0, v92
	v_lshlrev_b32_e32 v107, 3, v88
	v_sub_u32_e32 v88, 0, v107
	v_cndmask_b32_e32 v92, 0, v93, vcc
	v_add_u32_e32 v106, v92, v86
	v_and_b32_e32 v92, 12, v0
	v_mul_u32_u24_e32 v86, 0xd0, v101
	v_mad_u32_u24 v91, v91, 24, v92
	v_mul_u32_u24_e32 v93, 12, v95
	v_lshlrev_b32_e32 v92, 20, v101
	v_add3_u32 v112, v91, v86, v93
	v_lshl_or_b32 v86, s18, 21, v90
	v_add3_u32 v86, v86, s3, v92
	v_mul_f32_e32 v1, 0xbfb8aa3b, v1
	v_and_b32_e32 v114, 24, v88
	v_or_b32_e32 v88, v86, v94
	s_min_i32 s3, s19, 0xfe
	v_mul_f32_e32 v1, 0x3c91a2b4, v1
	s_waitcnt vmcnt(3)
	v_mul_f32_e32 v105, 0x4038aa3b, v100
	v_add_u32_e32 v108, 16, v106
	v_add_u32_e32 v109, 0x70, v106
	v_add_u32_e32 v110, 0x1b0, v106
	v_add_u32_e32 v111, 0x210, v106
	v_mul_u32_u24_e32 v113, 6, v113
	s_add_i32 s19, s3, 1
	v_lshl_add_u64 v[100:101], s[16:17], 0, v[102:103]
	v_lshl_add_u64 v[102:103], v[88:89], 1, s[14:15]
	s_sub_i32 s3, 0x7ff, s21
	v_mov_b32_e32 v115, 0x7f7f7f7f
	s_mov_b32 s16, 0x42700000
	s_mov_b32 s17, 0x41f00000
	s_mov_b32 s18, 0x41700000
	v_mov_b32_e32 v116, 0x6000
	v_mov_b32_e32 v117, 0x4b400000
	v_mov_b32_e32 v118, 0x4b400008
	v_mov_b32_e32 v119, 0x4b400010
	v_mbcnt_lo_u32_b32 v200, -1, 0
	v_mbcnt_hi_u32_b32 v200, -1, v200
	v_and_b32_e32 v201, 3, v200
	v_and_b32_e32 v202, 15, v200
	v_cmp_gt_u32_e32 vcc, 8, v202
	s_nop 1
	v_cndmask_b32_e64 v178, 0, v115, vcc
	v_cndmask_b32_e64 v179, v115, 0, vcc
	v_lshlrev_b32_e32 v181, 1, v201
	v_sub_u32_e32 v202, 22, v181
	v_lshlrev_b32_e64 v180, v202, 1
	v_sub_u32_e32 v202, 16, v181
	v_lshlrev_b32_e64 v181, v202, 1
	v_lshrrev_b32_e32 v202, 3, v107
	v_sub_u32_e32 v184, v112, v202
	v_add_u32_e32 v184, v184, v201
	v_add_u32_e32 v202, 0xc0, v202
	v_cmp_eq_u32_e32 vcc, 3, v201
	s_nop 1
	v_cndmask_b32_e32 v184, v184, v202, vcc
	v_subrev_u32_e32 v185, s14, v102
	s_mov_b32 s44, s21
	s_mov_b32 s45, s22
	s_lshr_b32 s46, s44, 3
	s_add_i32 s46, s46, 1
	s_mul_i32 s46, s46, 0x6000
	s_mov_b32 s47, 0
	v_lshl_add_u64 v[196:197], v[100:101], 0, s[46:47]
	s_mov_b32 s42, 0x6000
	s_mov_b32 s43, 0
	s_sub_i32 s46, s44, 1
	s_sub_i32 s47, 0x800, s44
	s_and_b64 s[40:41], s[6:7], exec
	s_cselect_b32 s46, s46, s47
	s_cselect_b32 s41, 0, -1
	s_xor_b32 s40, s41, 0x400
	s_sub_i32 s40, s40, s41
	s_ashr_i32 s47, s46, 31
	s_lshl_b64 s[46:47], s[46:47], 10
	s_add_u32 s48, s14, s46
	s_addc_u32 s49, s15, s47
	v_readfirstlane_b32 s51, v112
	s_waitcnt vmcnt(0) lgkmcnt(0)
	v_mov_b32_e32 v176, v87
	v_rcp_f32_e32 v186, v104
	s_nop 1
	v_mul_f32_e32 v188, v105, v186
	v_mov_b32_e32 v189, 0
	v_mov_b32_e32 v190, 0
	v_mov_b32_e32 v191, 0
	s_nop 1
	s_cmp_lt_i32 s44, s45
	s_cbranch_scc0 .Lscan_exit_st
	ds_read_b64 v[122:123], v106 offset:0
	ds_read_b64 v[124:125], v106 offset:8
	ds_read_b64 v[126:127], v106 offset:16
	s_waitcnt lgkmcnt(0)
	s_cmp_lt_u32 s51, 96
	s_cbranch_scc0 .Lscan_loop_b_st
.Lscan_loop_a_st:
	ds_read_b64 v[128:129], v106 offset:96
	ds_read_b64 v[130:131], v106 offset:104
	ds_read_b64 v[132:133], v106 offset:112
	s_waitcnt vmcnt(8)
	global_load_dwordx4 v[146:149], v[196:197], off
	global_load_dwordx4 v[150:153], v[196:197], off offset:512
	global_load_dwordx4 v[154:157], v[196:197], off offset:1024
	v_lshl_add_u64 v[196:197], v[196:197], 0, s[42:43]
	s_waitcnt lgkmcnt(3)
	v_mfma_f32_16x16x128_f8f6f4 v[134:137], v[122:127], v[2:7], 0 cbsz:2 blgp:2
	v_mfma_f32_16x16x128_f8f6f4 v[138:141], v[122:127], v[14:19], 0 cbsz:2 blgp:2
	v_mfma_f32_16x16x128_f8f6f4 v[142:145], v[122:127], v[26:31], v[188:191] cbsz:2 blgp:2
	v_mfma_f32_16x16x128_f8f6f4 v[204:207], v[122:127], v[38:43], 0 cbsz:2 blgp:2
	v_mfma_f32_16x16x128_f8f6f4 v[208:211], v[122:127], v[50:55], 0 cbsz:2 blgp:2
	v_mfma_f32_16x16x128_f8f6f4 v[212:215], v[122:127], v[62:67], v[188:191] cbsz:2 blgp:2
	s_waitcnt lgkmcnt(0)
	v_mfma_f32_16x16x128_f8f6f4 v[134:137], v[128:133], v[8:13], v[134:137] cbsz:2 blgp:2
	v_mfma_f32_16x16x128_f8f6f4 v[204:207], v[128:133], v[44:49], v[204:207] cbsz:2 blgp:2
	v_mfma_f32_16x16x128_f8f6f4 v[138:141], v[128:133], v[20:25], v[138:141] cbsz:2 blgp:2
	v_mfma_f32_16x16x128_f8f6f4 v[208:211], v[128:133], v[56:61], v[208:211] cbsz:2 blgp:2
	v_mfma_f32_16x16x128_f8f6f4 v[142:145], v[128:133], v[32:37], v[142:145] cbsz:2 blgp:2
	v_mfma_f32_16x16x128_f8f6f4 v[212:215], v[128:133], v[68:73], v[212:215] cbsz:2 blgp:2
	v_cndmask_b32_e64 v158, v134, v204, s[4:5]
	v_fma_mix_f32 v158, v158, v1, v82 op_sel_hi:[0,0,1]
	v_exp_f32_e32 v158, v158
	v_cndmask_b32_e64 v159, v138, v208, s[4:5]
	v_fma_mix_f32 v159, v159, v99, v74 op_sel_hi:[0,0,1]
	v_exp_f32_e32 v159, v159
	v_fma_f32 v158, v158, v186, v186
	v_rcp_f32_e32 v158, v158
	v_add_f32_e32 v159, 1.0, v159
	v_rcp_f32_e32 v159, v159
	v_cndmask_b32_e64 v160, v142, v212, s[4:5]
	v_fma_mix_f32 v161, v158, v160, v78 op_sel_hi:[0,0,1]
	v_exp_f32_e32 v161, v161
	s_add_u32 s48, s48, s40
	v_add_f32_e32 v161, 1.0, v161
	v_rcp_f32_e32 v161, v161
	s_addc_u32 s49, s49, s41
	v_fma_f32 v162, v161, -2.0, 1.0
	v_sub_f32_e32 v163, v176, v162
	v_fma_f32 v176, v159, v163, v162
	v_fma_f32 v164, |v176|, s16, v117
	v_fma_f32 v165, |v176|, s17, v118
	v_fma_f32 v166, |v176|, s18, v119
	v_lshrrev_b32_e32 v167, 26, v176
	v_min3_u32 v164, v164, v165, v166
	v_bfi_b32 v168, 31, v164, v167
	global_store_short_d16_hi v185, v176, s[48:49]
	s_nop 0
	v_mul_u32_u24_dpp v170, v168, v180 quad_perm:[1,2,3,3] row_mask:0xf bank_mask:0xf bound_ctrl:1
	v_mad_u32_u24 v171, v168, v181, v170
	ds_write_b8_d16_hi v184, v171 offset:416
	s_waitcnt lgkmcnt(0)
	s_barrier
	ds_read_b64 v[122:123], v106 offset:416
	ds_read_b64 v[124:125], v106 offset:424
	ds_read_b64 v[126:127], v106 offset:432
	s_barrier
	ds_read_b64 v[128:129], v106 offset:512
	ds_read_b64 v[130:131], v106 offset:520
	ds_read_b64 v[132:133], v106 offset:528
	s_waitcnt lgkmcnt(3)
	v_mfma_f32_16x16x128_f8f6f4 v[134:137], v[122:127], v[2:7], 0 cbsz:2 blgp:2
	v_mfma_f32_16x16x128_f8f6f4 v[138:141], v[122:127], v[14:19], 0 cbsz:2 blgp:2
	v_mfma_f32_16x16x128_f8f6f4 v[142:145], v[122:127], v[26:31], v[188:191] cbsz:2 blgp:2
	v_mfma_f32_16x16x128_f8f6f4 v[204:207], v[122:127], v[38:43], 0 cbsz:2 blgp:2
	v_mfma_f32_16x16x128_f8f6f4 v[208:211], v[122:127], v[50:55], 0 cbsz:2 blgp:2
	v_mfma_f32_16x16x128_f8f6f4 v[212:215], v[122:127], v[62:67], v[188:191] cbsz:2 blgp:2
	s_waitcnt lgkmcnt(0)
	v_mfma_f32_16x16x128_f8f6f4 v[134:137], v[128:133], v[8:13], v[134:137] cbsz:2 blgp:2
	v_mfma_f32_16x16x128_f8f6f4 v[204:207], v[128:133], v[44:49], v[204:207] cbsz:2 blgp:2
	v_mfma_f32_16x16x128_f8f6f4 v[138:141], v[128:133], v[20:25], v[138:141] cbsz:2 blgp:2
	v_mfma_f32_16x16x128_f8f6f4 v[208:211], v[128:133], v[56:61], v[208:211] cbsz:2 blgp:2
	v_mfma_f32_16x16x128_f8f6f4 v[142:145], v[128:133], v[32:37], v[142:145] cbsz:2 blgp:2
	v_mfma_f32_16x16x128_f8f6f4 v[212:215], v[128:133], v[68:73], v[212:215] cbsz:2 blgp:2
	v_cndmask_b32_e64 v158, v134, v204, s[4:5]
	v_fma_mix_f32 v158, v158, v1, v82 op_sel:[0,0,1] op_sel_hi:[0,0,1]
	v_exp_f32_e32 v158, v158
	v_cndmask_b32_e64 v159, v138, v208, s[4:5]
	v_fma_mix_f32 v159, v159, v99, v74 op_sel:[0,0,1] op_sel_hi:[0,0,1]
	v_exp_f32_e32 v159, v159
	v_fma_f32 v158, v158, v186, v186
	v_rcp_f32_e32 v158, v158
	v_add_f32_e32 v159, 1.0, v159
	v_rcp_f32_e32 v159, v159
	v_cndmask_b32_e64 v160, v142, v212, s[4:5]
	v_fma_mix_f32 v161, v158, v160, v78 op_sel:[0,0,1] op_sel_hi:[0,0,1]
	v_exp_f32_e32 v161, v161
	s_add_u32 s48, s48, s40
	v_add_f32_e32 v161, 1.0, v161
	v_rcp_f32_e32 v161, v161
	s_addc_u32 s49, s49, s41
	v_fma_f32 v162, v161, -2.0, 1.0
	v_sub_f32_e32 v163, v176, v162
	v_fma_f32 v176, v159, v163, v162
	v_fma_f32 v164, |v176|, s16, v117
	v_fma_f32 v165, |v176|, s17, v118
	v_fma_f32 v166, |v176|, s18, v119
	v_lshrrev_b32_e32 v167, 26, v176
	v_min3_u32 v164, v164, v165, v166
	v_bfi_b32 v168, 31, v164, v167
	global_store_short_d16_hi v185, v176, s[48:49]
	s_nop 0
	v_mul_u32_u24_dpp v170, v168, v180 quad_perm:[1,2,3,3] row_mask:0xf bank_mask:0xf bound_ctrl:1
	v_mad_u32_u24 v171, v168, v181, v170
	ds_write_b8_d16_hi v184, v171
	s_waitcnt lgkmcnt(0)
	s_barrier
	ds_read_b64 v[122:123], v106 offset:0
	ds_read_b64 v[124:125], v106 offset:8
	ds_read_b64 v[126:127], v106 offset:16
	s_barrier
	ds_read_b64 v[128:129], v106 offset:96
	ds_read_b64 v[130:131], v106 offset:104
	ds_read_b64 v[132:133], v106 offset:112
	s_waitcnt lgkmcnt(3)
	v_mfma_f32_16x16x128_f8f6f4 v[134:137], v[122:127], v[2:7], 0 cbsz:2 blgp:2
	v_mfma_f32_16x16x128_f8f6f4 v[138:141], v[122:127], v[14:19], 0 cbsz:2 blgp:2
	v_mfma_f32_16x16x128_f8f6f4 v[142:145], v[122:127], v[26:31], v[188:191] cbsz:2 blgp:2
	v_mfma_f32_16x16x128_f8f6f4 v[204:207], v[122:127], v[38:43], 0 cbsz:2 blgp:2
	v_mfma_f32_16x16x128_f8f6f4 v[208:211], v[122:127], v[50:55], 0 cbsz:2 blgp:2
	v_mfma_f32_16x16x128_f8f6f4 v[212:215], v[122:127], v[62:67], v[188:191] cbsz:2 blgp:2
	s_waitcnt lgkmcnt(0)
	v_mfma_f32_16x16x128_f8f6f4 v[134:137], v[128:133], v[8:13], v[134:137] cbsz:2 blgp:2
	v_mfma_f32_16x16x128_f8f6f4 v[204:207], v[128:133], v[44:49], v[204:207] cbsz:2 blgp:2
	v_mfma_f32_16x16x128_f8f6f4 v[138:141], v[128:133], v[20:25], v[138:141] cbsz:2 blgp:2
	v_mfma_f32_16x16x128_f8f6f4 v[208:211], v[128:133], v[56:61], v[208:211] cbsz:2 blgp:2
	v_mfma_f32_16x16x128_f8f6f4 v[142:145], v[128:133], v[32:37], v[142:145] cbsz:2 blgp:2
	v_mfma_f32_16x16x128_f8f6f4 v[212:215], v[128:133], v[68:73], v[212:215] cbsz:2 blgp:2
	v_cndmask_b32_e64 v158, v134, v204, s[4:5]
	v_fma_mix_f32 v158, v158, v1, v83 op_sel_hi:[0,0,1]
	v_exp_f32_e32 v158, v158
	v_cndmask_b32_e64 v159, v138, v208, s[4:5]
	v_fma_mix_f32 v159, v159, v99, v75 op_sel_hi:[0,0,1]
	v_exp_f32_e32 v159, v159
	v_fma_f32 v158, v158, v186, v186
	v_rcp_f32_e32 v158, v158
	v_add_f32_e32 v159, 1.0, v159
	v_rcp_f32_e32 v159, v159
	v_cndmask_b32_e64 v160, v142, v212, s[4:5]
	v_fma_mix_f32 v161, v158, v160, v79 op_sel_hi:[0,0,1]
	v_exp_f32_e32 v161, v161
	s_add_u32 s48, s48, s40
	v_add_f32_e32 v161, 1.0, v161
	v_rcp_f32_e32 v161, v161
	s_addc_u32 s49, s49, s41
	v_fma_f32 v162, v161, -2.0, 1.0
	v_sub_f32_e32 v163, v176, v162
	v_fma_f32 v176, v159, v163, v162
	v_fma_f32 v164, |v176|, s16, v117
	v_fma_f32 v165, |v176|, s17, v118
	v_fma_f32 v166, |v176|, s18, v119
	v_lshrrev_b32_e32 v167, 26, v176
	v_min3_u32 v164, v164, v165, v166
	v_bfi_b32 v168, 31, v164, v167
	global_store_short_d16_hi v185, v176, s[48:49]
	s_nop 0
	v_mul_u32_u24_dpp v170, v168, v180 quad_perm:[1,2,3,3] row_mask:0xf bank_mask:0xf bound_ctrl:1
	v_mad_u32_u24 v171, v168, v181, v170
	ds_write_b8_d16_hi v184, v171 offset:416
	s_waitcnt lgkmcnt(0)
	s_barrier
	ds_read_b64 v[122:123], v106 offset:416
	ds_read_b64 v[124:125], v106 offset:424
	ds_read_b64 v[126:127], v106 offset:432
	s_barrier
	ds_read_b64 v[128:129], v106 offset:512
	ds_read_b64 v[130:131], v106 offset:520
	ds_read_b64 v[132:133], v106 offset:528
	s_waitcnt lgkmcnt(3)
	v_mfma_f32_16x16x128_f8f6f4 v[134:137], v[122:127], v[2:7], 0 cbsz:2 blgp:2
	v_mfma_f32_16x16x128_f8f6f4 v[138:141], v[122:127], v[14:19], 0 cbsz:2 blgp:2
	v_mfma_f32_16x16x128_f8f6f4 v[142:145], v[122:127], v[26:31], v[188:191] cbsz:2 blgp:2
	v_mfma_f32_16x16x128_f8f6f4 v[204:207], v[122:127], v[38:43], 0 cbsz:2 blgp:2
	v_mfma_f32_16x16x128_f8f6f4 v[208:211], v[122:127], v[50:55], 0 cbsz:2 blgp:2
	v_mfma_f32_16x16x128_f8f6f4 v[212:215], v[122:127], v[62:67], v[188:191] cbsz:2 blgp:2
	s_waitcnt lgkmcnt(0)
	v_mfma_f32_16x16x128_f8f6f4 v[134:137], v[128:133], v[8:13], v[134:137] cbsz:2 blgp:2
	v_mfma_f32_16x16x128_f8f6f4 v[204:207], v[128:133], v[44:49], v[204:207] cbsz:2 blgp:2
	v_mfma_f32_16x16x128_f8f6f4 v[138:141], v[128:133], v[20:25], v[138:141] cbsz:2 blgp:2
	v_mfma_f32_16x16x128_f8f6f4 v[208:211], v[128:133], v[56:61], v[208:211] cbsz:2 blgp:2
	v_mfma_f32_16x16x128_f8f6f4 v[142:145], v[128:133], v[32:37], v[142:145] cbsz:2 blgp:2
	v_mfma_f32_16x16x128_f8f6f4 v[212:215], v[128:133], v[68:73], v[212:215] cbsz:2 blgp:2
	v_cndmask_b32_e64 v158, v134, v204, s[4:5]
	v_fma_mix_f32 v158, v158, v1, v83 op_sel:[0,0,1] op_sel_hi:[0,0,1]
	v_exp_f32_e32 v158, v158
	v_cndmask_b32_e64 v159, v138, v208, s[4:5]
	v_fma_mix_f32 v159, v159, v99, v75 op_sel:[0,0,1] op_sel_hi:[0,0,1]
	v_exp_f32_e32 v159, v159
	v_fma_f32 v158, v158, v186, v186
	v_rcp_f32_e32 v158, v158
	v_add_f32_e32 v159, 1.0, v159
	v_rcp_f32_e32 v159, v159
	v_cndmask_b32_e64 v160, v142, v212, s[4:5]
	v_fma_mix_f32 v161, v158, v160, v79 op_sel:[0,0,1] op_sel_hi:[0,0,1]
	v_exp_f32_e32 v161, v161
	s_add_u32 s48, s48, s40
	v_add_f32_e32 v161, 1.0, v161
	v_rcp_f32_e32 v161, v161
	s_addc_u32 s49, s49, s41
	v_fma_f32 v162, v161, -2.0, 1.0
	v_sub_f32_e32 v163, v176, v162
	v_fma_f32 v176, v159, v163, v162
	v_fma_f32 v164, |v176|, s16, v117
	v_fma_f32 v165, |v176|, s17, v118
	v_fma_f32 v166, |v176|, s18, v119
	v_lshrrev_b32_e32 v167, 26, v176
	v_min3_u32 v164, v164, v165, v166
	v_bfi_b32 v168, 31, v164, v167
	global_store_short_d16_hi v185, v176, s[48:49]
	s_nop 0
	v_mul_u32_u24_dpp v170, v168, v180 quad_perm:[1,2,3,3] row_mask:0xf bank_mask:0xf bound_ctrl:1
	v_mad_u32_u24 v171, v168, v181, v170
	ds_write_b8_d16_hi v184, v171
	s_waitcnt lgkmcnt(0)
	s_barrier
	ds_read_b64 v[122:123], v106 offset:0
	ds_read_b64 v[124:125], v106 offset:8
	ds_read_b64 v[126:127], v106 offset:16
	s_barrier
	ds_read_b64 v[128:129], v106 offset:96
	ds_read_b64 v[130:131], v106 offset:104
	ds_read_b64 v[132:133], v106 offset:112
	s_waitcnt lgkmcnt(3)
	v_mfma_f32_16x16x128_f8f6f4 v[134:137], v[122:127], v[2:7], 0 cbsz:2 blgp:2
	v_mfma_f32_16x16x128_f8f6f4 v[138:141], v[122:127], v[14:19], 0 cbsz:2 blgp:2
	v_mfma_f32_16x16x128_f8f6f4 v[142:145], v[122:127], v[26:31], v[188:191] cbsz:2 blgp:2
	v_mfma_f32_16x16x128_f8f6f4 v[204:207], v[122:127], v[38:43], 0 cbsz:2 blgp:2
	v_mfma_f32_16x16x128_f8f6f4 v[208:211], v[122:127], v[50:55], 0 cbsz:2 blgp:2
	v_mfma_f32_16x16x128_f8f6f4 v[212:215], v[122:127], v[62:67], v[188:191] cbsz:2 blgp:2
	s_waitcnt lgkmcnt(0)
	v_mfma_f32_16x16x128_f8f6f4 v[134:137], v[128:133], v[8:13], v[134:137] cbsz:2 blgp:2
	v_mfma_f32_16x16x128_f8f6f4 v[204:207], v[128:133], v[44:49], v[204:207] cbsz:2 blgp:2
	v_mfma_f32_16x16x128_f8f6f4 v[138:141], v[128:133], v[20:25], v[138:141] cbsz:2 blgp:2
	v_mfma_f32_16x16x128_f8f6f4 v[208:211], v[128:133], v[56:61], v[208:211] cbsz:2 blgp:2
	v_mfma_f32_16x16x128_f8f6f4 v[142:145], v[128:133], v[32:37], v[142:145] cbsz:2 blgp:2
	v_mfma_f32_16x16x128_f8f6f4 v[212:215], v[128:133], v[68:73], v[212:215] cbsz:2 blgp:2
	v_cndmask_b32_e64 v158, v134, v204, s[4:5]
	v_fma_mix_f32 v158, v158, v1, v84 op_sel_hi:[0,0,1]
	v_exp_f32_e32 v158, v158
	v_cndmask_b32_e64 v159, v138, v208, s[4:5]
	v_fma_mix_f32 v159, v159, v99, v76 op_sel_hi:[0,0,1]
	v_exp_f32_e32 v159, v159
	v_fma_f32 v158, v158, v186, v186
	v_rcp_f32_e32 v158, v158
	v_add_f32_e32 v159, 1.0, v159
	v_rcp_f32_e32 v159, v159
	v_cndmask_b32_e64 v160, v142, v212, s[4:5]
	v_fma_mix_f32 v161, v158, v160, v80 op_sel_hi:[0,0,1]
	v_exp_f32_e32 v161, v161
	s_add_u32 s48, s48, s40
	v_add_f32_e32 v161, 1.0, v161
	v_rcp_f32_e32 v161, v161
	s_addc_u32 s49, s49, s41
	v_fma_f32 v162, v161, -2.0, 1.0
	v_sub_f32_e32 v163, v176, v162
	v_fma_f32 v176, v159, v163, v162
	v_fma_f32 v164, |v176|, s16, v117
	v_fma_f32 v165, |v176|, s17, v118
	v_fma_f32 v166, |v176|, s18, v119
	v_lshrrev_b32_e32 v167, 26, v176
	v_min3_u32 v164, v164, v165, v166
	v_bfi_b32 v168, 31, v164, v167
	global_store_short_d16_hi v185, v176, s[48:49]
	s_nop 0
	v_mul_u32_u24_dpp v170, v168, v180 quad_perm:[1,2,3,3] row_mask:0xf bank_mask:0xf bound_ctrl:1
	v_mad_u32_u24 v171, v168, v181, v170
	ds_write_b8_d16_hi v184, v171 offset:416
	s_waitcnt lgkmcnt(0)
	s_barrier
	ds_read_b64 v[122:123], v106 offset:416
	ds_read_b64 v[124:125], v106 offset:424
	ds_read_b64 v[126:127], v106 offset:432
	s_barrier
	ds_read_b64 v[128:129], v106 offset:512
	ds_read_b64 v[130:131], v106 offset:520
	ds_read_b64 v[132:133], v106 offset:528
	s_waitcnt lgkmcnt(3)
	v_mfma_f32_16x16x128_f8f6f4 v[134:137], v[122:127], v[2:7], 0 cbsz:2 blgp:2
	v_mfma_f32_16x16x128_f8f6f4 v[138:141], v[122:127], v[14:19], 0 cbsz:2 blgp:2
	v_mfma_f32_16x16x128_f8f6f4 v[142:145], v[122:127], v[26:31], v[188:191] cbsz:2 blgp:2
	v_mfma_f32_16x16x128_f8f6f4 v[204:207], v[122:127], v[38:43], 0 cbsz:2 blgp:2
	v_mfma_f32_16x16x128_f8f6f4 v[208:211], v[122:127], v[50:55], 0 cbsz:2 blgp:2
	v_mfma_f32_16x16x128_f8f6f4 v[212:215], v[122:127], v[62:67], v[188:191] cbsz:2 blgp:2
	s_waitcnt lgkmcnt(0)
	v_mfma_f32_16x16x128_f8f6f4 v[134:137], v[128:133], v[8:13], v[134:137] cbsz:2 blgp:2
	v_mfma_f32_16x16x128_f8f6f4 v[204:207], v[128:133], v[44:49], v[204:207] cbsz:2 blgp:2
	v_mfma_f32_16x16x128_f8f6f4 v[138:141], v[128:133], v[20:25], v[138:141] cbsz:2 blgp:2
	v_mfma_f32_16x16x128_f8f6f4 v[208:211], v[128:133], v[56:61], v[208:211] cbsz:2 blgp:2
	v_mfma_f32_16x16x128_f8f6f4 v[142:145], v[128:133], v[32:37], v[142:145] cbsz:2 blgp:2
	v_mfma_f32_16x16x128_f8f6f4 v[212:215], v[128:133], v[68:73], v[212:215] cbsz:2 blgp:2
	v_cndmask_b32_e64 v158, v134, v204, s[4:5]
	v_fma_mix_f32 v158, v158, v1, v84 op_sel:[0,0,1] op_sel_hi:[0,0,1]
	v_exp_f32_e32 v158, v158
	v_cndmask_b32_e64 v159, v138, v208, s[4:5]
	v_fma_mix_f32 v159, v159, v99, v76 op_sel:[0,0,1] op_sel_hi:[0,0,1]
	v_exp_f32_e32 v159, v159
	v_fma_f32 v158, v158, v186, v186
	v_rcp_f32_e32 v158, v158
	v_add_f32_e32 v159, 1.0, v159
	v_rcp_f32_e32 v159, v159
	v_cndmask_b32_e64 v160, v142, v212, s[4:5]
	v_fma_mix_f32 v161, v158, v160, v80 op_sel:[0,0,1] op_sel_hi:[0,0,1]
	v_exp_f32_e32 v161, v161
	s_add_u32 s48, s48, s40
	v_add_f32_e32 v161, 1.0, v161
	v_rcp_f32_e32 v161, v161
	s_addc_u32 s49, s49, s41
	v_fma_f32 v162, v161, -2.0, 1.0
	v_sub_f32_e32 v163, v176, v162
	v_fma_f32 v176, v159, v163, v162
	v_fma_f32 v164, |v176|, s16, v117
	v_fma_f32 v165, |v176|, s17, v118
	v_fma_f32 v166, |v176|, s18, v119
	v_lshrrev_b32_e32 v167, 26, v176
	v_min3_u32 v164, v164, v165, v166
	v_bfi_b32 v168, 31, v164, v167
	global_store_short_d16_hi v185, v176, s[48:49]
	s_nop 0
	v_mul_u32_u24_dpp v170, v168, v180 quad_perm:[1,2,3,3] row_mask:0xf bank_mask:0xf bound_ctrl:1
	v_mad_u32_u24 v171, v168, v181, v170
	ds_write_b8_d16_hi v184, v171
	s_waitcnt lgkmcnt(0)
	s_barrier
	ds_read_b64 v[122:123], v106 offset:0
	ds_read_b64 v[124:125], v106 offset:8
	ds_read_b64 v[126:127], v106 offset:16
	s_barrier
	ds_read_b64 v[128:129], v106 offset:96
	ds_read_b64 v[130:131], v106 offset:104
	ds_read_b64 v[132:133], v106 offset:112
	s_waitcnt lgkmcnt(3)
	v_mfma_f32_16x16x128_f8f6f4 v[134:137], v[122:127], v[2:7], 0 cbsz:2 blgp:2
	v_mfma_f32_16x16x128_f8f6f4 v[138:141], v[122:127], v[14:19], 0 cbsz:2 blgp:2
	v_mfma_f32_16x16x128_f8f6f4 v[142:145], v[122:127], v[26:31], v[188:191] cbsz:2 blgp:2
	v_mfma_f32_16x16x128_f8f6f4 v[204:207], v[122:127], v[38:43], 0 cbsz:2 blgp:2
	v_mfma_f32_16x16x128_f8f6f4 v[208:211], v[122:127], v[50:55], 0 cbsz:2 blgp:2
	v_mfma_f32_16x16x128_f8f6f4 v[212:215], v[122:127], v[62:67], v[188:191] cbsz:2 blgp:2
	s_waitcnt lgkmcnt(0)
	v_mfma_f32_16x16x128_f8f6f4 v[134:137], v[128:133], v[8:13], v[134:137] cbsz:2 blgp:2
	v_mfma_f32_16x16x128_f8f6f4 v[204:207], v[128:133], v[44:49], v[204:207] cbsz:2 blgp:2
	v_mfma_f32_16x16x128_f8f6f4 v[138:141], v[128:133], v[20:25], v[138:141] cbsz:2 blgp:2
	v_mfma_f32_16x16x128_f8f6f4 v[208:211], v[128:133], v[56:61], v[208:211] cbsz:2 blgp:2
	v_mfma_f32_16x16x128_f8f6f4 v[142:145], v[128:133], v[32:37], v[142:145] cbsz:2 blgp:2
	v_mfma_f32_16x16x128_f8f6f4 v[212:215], v[128:133], v[68:73], v[212:215] cbsz:2 blgp:2
	v_cndmask_b32_e64 v158, v134, v204, s[4:5]
	v_fma_mix_f32 v158, v158, v1, v85 op_sel_hi:[0,0,1]
	v_exp_f32_e32 v158, v158
	v_cndmask_b32_e64 v159, v138, v208, s[4:5]
	v_fma_mix_f32 v159, v159, v99, v77 op_sel_hi:[0,0,1]
	v_exp_f32_e32 v159, v159
	v_fma_f32 v158, v158, v186, v186
	v_rcp_f32_e32 v158, v158
	v_add_f32_e32 v159, 1.0, v159
	v_rcp_f32_e32 v159, v159
	v_cndmask_b32_e64 v160, v142, v212, s[4:5]
	v_fma_mix_f32 v161, v158, v160, v81 op_sel_hi:[0,0,1]
	v_exp_f32_e32 v161, v161
	s_add_u32 s48, s48, s40
	v_add_f32_e32 v161, 1.0, v161
	v_rcp_f32_e32 v161, v161
	s_addc_u32 s49, s49, s41
	v_fma_f32 v162, v161, -2.0, 1.0
	v_sub_f32_e32 v163, v176, v162
	v_fma_f32 v176, v159, v163, v162
	v_fma_f32 v164, |v176|, s16, v117
	v_fma_f32 v165, |v176|, s17, v118
	v_fma_f32 v166, |v176|, s18, v119
	v_lshrrev_b32_e32 v167, 26, v176
	v_min3_u32 v164, v164, v165, v166
	v_bfi_b32 v168, 31, v164, v167
	global_store_short_d16_hi v185, v176, s[48:49]
	s_nop 0
	v_mul_u32_u24_dpp v170, v168, v180 quad_perm:[1,2,3,3] row_mask:0xf bank_mask:0xf bound_ctrl:1
	v_mad_u32_u24 v171, v168, v181, v170
	ds_write_b8_d16_hi v184, v171 offset:416
	s_waitcnt lgkmcnt(0)
	s_barrier
	ds_read_b64 v[122:123], v106 offset:416
	ds_read_b64 v[124:125], v106 offset:424
	ds_read_b64 v[126:127], v106 offset:432
	s_barrier
	ds_read_b64 v[128:129], v106 offset:512
	ds_read_b64 v[130:131], v106 offset:520
	ds_read_b64 v[132:133], v106 offset:528
	s_waitcnt lgkmcnt(3)
	v_mfma_f32_16x16x128_f8f6f4 v[134:137], v[122:127], v[2:7], 0 cbsz:2 blgp:2
	v_mfma_f32_16x16x128_f8f6f4 v[138:141], v[122:127], v[14:19], 0 cbsz:2 blgp:2
	v_mfma_f32_16x16x128_f8f6f4 v[142:145], v[122:127], v[26:31], v[188:191] cbsz:2 blgp:2
	v_mfma_f32_16x16x128_f8f6f4 v[204:207], v[122:127], v[38:43], 0 cbsz:2 blgp:2
	v_mfma_f32_16x16x128_f8f6f4 v[208:211], v[122:127], v[50:55], 0 cbsz:2 blgp:2
	v_mfma_f32_16x16x128_f8f6f4 v[212:215], v[122:127], v[62:67], v[188:191] cbsz:2 blgp:2
	s_waitcnt lgkmcnt(0)
	v_mfma_f32_16x16x128_f8f6f4 v[134:137], v[128:133], v[8:13], v[134:137] cbsz:2 blgp:2
	v_mfma_f32_16x16x128_f8f6f4 v[204:207], v[128:133], v[44:49], v[204:207] cbsz:2 blgp:2
	v_mfma_f32_16x16x128_f8f6f4 v[138:141], v[128:133], v[20:25], v[138:141] cbsz:2 blgp:2
	v_mfma_f32_16x16x128_f8f6f4 v[208:211], v[128:133], v[56:61], v[208:211] cbsz:2 blgp:2
	v_mfma_f32_16x16x128_f8f6f4 v[142:145], v[128:133], v[32:37], v[142:145] cbsz:2 blgp:2
	v_mfma_f32_16x16x128_f8f6f4 v[212:215], v[128:133], v[68:73], v[212:215] cbsz:2 blgp:2
	v_cndmask_b32_e64 v158, v134, v204, s[4:5]
	v_fma_mix_f32 v158, v158, v1, v85 op_sel:[0,0,1] op_sel_hi:[0,0,1]
	v_exp_f32_e32 v158, v158
	v_cndmask_b32_e64 v159, v138, v208, s[4:5]
	v_fma_mix_f32 v159, v159, v99, v77 op_sel:[0,0,1] op_sel_hi:[0,0,1]
	v_exp_f32_e32 v159, v159
	v_fma_f32 v158, v158, v186, v186
	v_rcp_f32_e32 v158, v158
	v_add_f32_e32 v159, 1.0, v159
	v_rcp_f32_e32 v159, v159
	v_cndmask_b32_e64 v160, v142, v212, s[4:5]
	v_fma_mix_f32 v161, v158, v160, v81 op_sel:[0,0,1] op_sel_hi:[0,0,1]
	v_exp_f32_e32 v161, v161
	s_add_u32 s48, s48, s40
	v_add_f32_e32 v161, 1.0, v161
	v_rcp_f32_e32 v161, v161
	s_addc_u32 s49, s49, s41
	v_fma_f32 v162, v161, -2.0, 1.0
	v_sub_f32_e32 v163, v176, v162
	v_fma_f32 v176, v159, v163, v162
	v_fma_f32 v164, |v176|, s16, v117
	v_fma_f32 v165, |v176|, s17, v118
	v_fma_f32 v166, |v176|, s18, v119
	v_lshrrev_b32_e32 v167, 26, v176
	v_min3_u32 v164, v164, v165, v166
	v_bfi_b32 v168, 31, v164, v167
	global_store_short_d16_hi v185, v176, s[48:49]
	s_nop 0
	v_mul_u32_u24_dpp v170, v168, v180 quad_perm:[1,2,3,3] row_mask:0xf bank_mask:0xf bound_ctrl:1
	v_mad_u32_u24 v171, v168, v181, v170
	ds_write_b8_d16_hi v184, v171
	s_waitcnt lgkmcnt(0)
	s_barrier
	ds_read_b64 v[122:123], v106 offset:0
	ds_read_b64 v[124:125], v106 offset:8
	ds_read_b64 v[126:127], v106 offset:16
	s_barrier
	ds_read_b64 v[128:129], v106 offset:96
	ds_read_b64 v[130:131], v106 offset:104
	ds_read_b64 v[132:133], v106 offset:112
	s_waitcnt vmcnt(8)
	global_load_dwordx4 v[82:85], v[196:197], off
	global_load_dwordx4 v[74:77], v[196:197], off offset:512
	global_load_dwordx4 v[78:81], v[196:197], off offset:1024
	v_lshl_add_u64 v[196:197], v[196:197], 0, s[42:43]
	s_waitcnt lgkmcnt(3)
	v_mfma_f32_16x16x128_f8f6f4 v[134:137], v[122:127], v[2:7], 0 cbsz:2 blgp:2
	v_mfma_f32_16x16x128_f8f6f4 v[138:141], v[122:127], v[14:19], 0 cbsz:2 blgp:2
	v_mfma_f32_16x16x128_f8f6f4 v[142:145], v[122:127], v[26:31], v[188:191] cbsz:2 blgp:2
	v_mfma_f32_16x16x128_f8f6f4 v[204:207], v[122:127], v[38:43], 0 cbsz:2 blgp:2
	v_mfma_f32_16x16x128_f8f6f4 v[208:211], v[122:127], v[50:55], 0 cbsz:2 blgp:2
	v_mfma_f32_16x16x128_f8f6f4 v[212:215], v[122:127], v[62:67], v[188:191] cbsz:2 blgp:2
	s_waitcnt lgkmcnt(0)
	v_mfma_f32_16x16x128_f8f6f4 v[134:137], v[128:133], v[8:13], v[134:137] cbsz:2 blgp:2
	v_mfma_f32_16x16x128_f8f6f4 v[204:207], v[128:133], v[44:49], v[204:207] cbsz:2 blgp:2
	v_mfma_f32_16x16x128_f8f6f4 v[138:141], v[128:133], v[20:25], v[138:141] cbsz:2 blgp:2
	v_mfma_f32_16x16x128_f8f6f4 v[208:211], v[128:133], v[56:61], v[208:211] cbsz:2 blgp:2
	v_mfma_f32_16x16x128_f8f6f4 v[142:145], v[128:133], v[32:37], v[142:145] cbsz:2 blgp:2
	v_mfma_f32_16x16x128_f8f6f4 v[212:215], v[128:133], v[68:73], v[212:215] cbsz:2 blgp:2
	v_cndmask_b32_e64 v158, v134, v204, s[4:5]
	v_fma_mix_f32 v158, v158, v1, v146 op_sel_hi:[0,0,1]
	v_exp_f32_e32 v158, v158
	v_cndmask_b32_e64 v159, v138, v208, s[4:5]
	v_fma_mix_f32 v159, v159, v99, v150 op_sel_hi:[0,0,1]
	v_exp_f32_e32 v159, v159
	v_fma_f32 v158, v158, v186, v186
	v_rcp_f32_e32 v158, v158
	v_add_f32_e32 v159, 1.0, v159
	v_rcp_f32_e32 v159, v159
	v_cndmask_b32_e64 v160, v142, v212, s[4:5]
	v_fma_mix_f32 v161, v158, v160, v154 op_sel_hi:[0,0,1]
	v_exp_f32_e32 v161, v161
	s_add_u32 s48, s48, s40
	v_add_f32_e32 v161, 1.0, v161
	v_rcp_f32_e32 v161, v161
	s_addc_u32 s49, s49, s41
	v_fma_f32 v162, v161, -2.0, 1.0
	v_sub_f32_e32 v163, v176, v162
	v_fma_f32 v176, v159, v163, v162
	v_fma_f32 v164, |v176|, s16, v117
	v_fma_f32 v165, |v176|, s17, v118
	v_fma_f32 v166, |v176|, s18, v119
	v_lshrrev_b32_e32 v167, 26, v176
	v_min3_u32 v164, v164, v165, v166
	v_bfi_b32 v168, 31, v164, v167
	global_store_short_d16_hi v185, v176, s[48:49]
	s_nop 0
	v_mul_u32_u24_dpp v170, v168, v180 quad_perm:[1,2,3,3] row_mask:0xf bank_mask:0xf bound_ctrl:1
	v_mad_u32_u24 v171, v168, v181, v170
	ds_write_b8_d16_hi v184, v171 offset:416
	s_waitcnt lgkmcnt(0)
	s_barrier
	ds_read_b64 v[122:123], v106 offset:416
	ds_read_b64 v[124:125], v106 offset:424
	ds_read_b64 v[126:127], v106 offset:432
	s_barrier
	ds_read_b64 v[128:129], v106 offset:512
	ds_read_b64 v[130:131], v106 offset:520
	ds_read_b64 v[132:133], v106 offset:528
	s_waitcnt lgkmcnt(3)
	v_mfma_f32_16x16x128_f8f6f4 v[134:137], v[122:127], v[2:7], 0 cbsz:2 blgp:2
	v_mfma_f32_16x16x128_f8f6f4 v[138:141], v[122:127], v[14:19], 0 cbsz:2 blgp:2
	v_mfma_f32_16x16x128_f8f6f4 v[142:145], v[122:127], v[26:31], v[188:191] cbsz:2 blgp:2
	v_mfma_f32_16x16x128_f8f6f4 v[204:207], v[122:127], v[38:43], 0 cbsz:2 blgp:2
	v_mfma_f32_16x16x128_f8f6f4 v[208:211], v[122:127], v[50:55], 0 cbsz:2 blgp:2
	v_mfma_f32_16x16x128_f8f6f4 v[212:215], v[122:127], v[62:67], v[188:191] cbsz:2 blgp:2
	s_waitcnt lgkmcnt(0)
	v_mfma_f32_16x16x128_f8f6f4 v[134:137], v[128:133], v[8:13], v[134:137] cbsz:2 blgp:2
	v_mfma_f32_16x16x128_f8f6f4 v[204:207], v[128:133], v[44:49], v[204:207] cbsz:2 blgp:2
	v_mfma_f32_16x16x128_f8f6f4 v[138:141], v[128:133], v[20:25], v[138:141] cbsz:2 blgp:2
	v_mfma_f32_16x16x128_f8f6f4 v[208:211], v[128:133], v[56:61], v[208:211] cbsz:2 blgp:2
	v_mfma_f32_16x16x128_f8f6f4 v[142:145], v[128:133], v[32:37], v[142:145] cbsz:2 blgp:2
	v_mfma_f32_16x16x128_f8f6f4 v[212:215], v[128:133], v[68:73], v[212:215] cbsz:2 blgp:2
	v_cndmask_b32_e64 v158, v134, v204, s[4:5]
	v_fma_mix_f32 v158, v158, v1, v146 op_sel:[0,0,1] op_sel_hi:[0,0,1]
	v_exp_f32_e32 v158, v158
	v_cndmask_b32_e64 v159, v138, v208, s[4:5]
	v_fma_mix_f32 v159, v159, v99, v150 op_sel:[0,0,1] op_sel_hi:[0,0,1]
	v_exp_f32_e32 v159, v159
	v_fma_f32 v158, v158, v186, v186
	v_rcp_f32_e32 v158, v158
	v_add_f32_e32 v159, 1.0, v159
	v_rcp_f32_e32 v159, v159
	v_cndmask_b32_e64 v160, v142, v212, s[4:5]
	v_fma_mix_f32 v161, v158, v160, v154 op_sel:[0,0,1] op_sel_hi:[0,0,1]
	v_exp_f32_e32 v161, v161
	s_add_u32 s48, s48, s40
	v_add_f32_e32 v161, 1.0, v161
	v_rcp_f32_e32 v161, v161
	s_addc_u32 s49, s49, s41
	v_fma_f32 v162, v161, -2.0, 1.0
	v_sub_f32_e32 v163, v176, v162
	v_fma_f32 v176, v159, v163, v162
	v_fma_f32 v164, |v176|, s16, v117
	v_fma_f32 v165, |v176|, s17, v118
	v_fma_f32 v166, |v176|, s18, v119
	v_lshrrev_b32_e32 v167, 26, v176
	v_min3_u32 v164, v164, v165, v166
	v_bfi_b32 v168, 31, v164, v167
	global_store_short_d16_hi v185, v176, s[48:49]
	s_nop 0
	v_mul_u32_u24_dpp v170, v168, v180 quad_perm:[1,2,3,3] row_mask:0xf bank_mask:0xf bound_ctrl:1
	v_mad_u32_u24 v171, v168, v181, v170
	ds_write_b8_d16_hi v184, v171
	s_waitcnt lgkmcnt(0)
	s_barrier
	ds_read_b64 v[122:123], v106 offset:0
	ds_read_b64 v[124:125], v106 offset:8
	ds_read_b64 v[126:127], v106 offset:16
	s_barrier
	ds_read_b64 v[128:129], v106 offset:96
	ds_read_b64 v[130:131], v106 offset:104
	ds_read_b64 v[132:133], v106 offset:112
	s_waitcnt lgkmcnt(3)
	v_mfma_f32_16x16x128_f8f6f4 v[134:137], v[122:127], v[2:7], 0 cbsz:2 blgp:2
	v_mfma_f32_16x16x128_f8f6f4 v[138:141], v[122:127], v[14:19], 0 cbsz:2 blgp:2
	v_mfma_f32_16x16x128_f8f6f4 v[142:145], v[122:127], v[26:31], v[188:191] cbsz:2 blgp:2
	v_mfma_f32_16x16x128_f8f6f4 v[204:207], v[122:127], v[38:43], 0 cbsz:2 blgp:2
	v_mfma_f32_16x16x128_f8f6f4 v[208:211], v[122:127], v[50:55], 0 cbsz:2 blgp:2
	v_mfma_f32_16x16x128_f8f6f4 v[212:215], v[122:127], v[62:67], v[188:191] cbsz:2 blgp:2
	s_waitcnt lgkmcnt(0)
	v_mfma_f32_16x16x128_f8f6f4 v[134:137], v[128:133], v[8:13], v[134:137] cbsz:2 blgp:2
	v_mfma_f32_16x16x128_f8f6f4 v[204:207], v[128:133], v[44:49], v[204:207] cbsz:2 blgp:2
	v_mfma_f32_16x16x128_f8f6f4 v[138:141], v[128:133], v[20:25], v[138:141] cbsz:2 blgp:2
	v_mfma_f32_16x16x128_f8f6f4 v[208:211], v[128:133], v[56:61], v[208:211] cbsz:2 blgp:2
	v_mfma_f32_16x16x128_f8f6f4 v[142:145], v[128:133], v[32:37], v[142:145] cbsz:2 blgp:2
	v_mfma_f32_16x16x128_f8f6f4 v[212:215], v[128:133], v[68:73], v[212:215] cbsz:2 blgp:2
	v_cndmask_b32_e64 v158, v134, v204, s[4:5]
	v_fma_mix_f32 v158, v158, v1, v147 op_sel_hi:[0,0,1]
	v_exp_f32_e32 v158, v158
	v_cndmask_b32_e64 v159, v138, v208, s[4:5]
	v_fma_mix_f32 v159, v159, v99, v151 op_sel_hi:[0,0,1]
	v_exp_f32_e32 v159, v159
	v_fma_f32 v158, v158, v186, v186
	v_rcp_f32_e32 v158, v158
	v_add_f32_e32 v159, 1.0, v159
	v_rcp_f32_e32 v159, v159
	v_cndmask_b32_e64 v160, v142, v212, s[4:5]
	v_fma_mix_f32 v161, v158, v160, v155 op_sel_hi:[0,0,1]
	v_exp_f32_e32 v161, v161
	s_add_u32 s48, s48, s40
	v_add_f32_e32 v161, 1.0, v161
	v_rcp_f32_e32 v161, v161
	s_addc_u32 s49, s49, s41
	v_fma_f32 v162, v161, -2.0, 1.0
	v_sub_f32_e32 v163, v176, v162
	v_fma_f32 v176, v159, v163, v162
	v_fma_f32 v164, |v176|, s16, v117
	v_fma_f32 v165, |v176|, s17, v118
	v_fma_f32 v166, |v176|, s18, v119
	v_lshrrev_b32_e32 v167, 26, v176
	v_min3_u32 v164, v164, v165, v166
	v_bfi_b32 v168, 31, v164, v167
	global_store_short_d16_hi v185, v176, s[48:49]
	s_nop 0
	v_mul_u32_u24_dpp v170, v168, v180 quad_perm:[1,2,3,3] row_mask:0xf bank_mask:0xf bound_ctrl:1
	v_mad_u32_u24 v171, v168, v181, v170
	ds_write_b8_d16_hi v184, v171 offset:416
	s_waitcnt lgkmcnt(0)
	s_barrier
	ds_read_b64 v[122:123], v106 offset:416
	ds_read_b64 v[124:125], v106 offset:424
	ds_read_b64 v[126:127], v106 offset:432
	s_barrier
	ds_read_b64 v[128:129], v106 offset:512
	ds_read_b64 v[130:131], v106 offset:520
	ds_read_b64 v[132:133], v106 offset:528
	s_waitcnt lgkmcnt(3)
	v_mfma_f32_16x16x128_f8f6f4 v[134:137], v[122:127], v[2:7], 0 cbsz:2 blgp:2
	v_mfma_f32_16x16x128_f8f6f4 v[138:141], v[122:127], v[14:19], 0 cbsz:2 blgp:2
	v_mfma_f32_16x16x128_f8f6f4 v[142:145], v[122:127], v[26:31], v[188:191] cbsz:2 blgp:2
	v_mfma_f32_16x16x128_f8f6f4 v[204:207], v[122:127], v[38:43], 0 cbsz:2 blgp:2
	v_mfma_f32_16x16x128_f8f6f4 v[208:211], v[122:127], v[50:55], 0 cbsz:2 blgp:2
	v_mfma_f32_16x16x128_f8f6f4 v[212:215], v[122:127], v[62:67], v[188:191] cbsz:2 blgp:2
	s_waitcnt lgkmcnt(0)
	v_mfma_f32_16x16x128_f8f6f4 v[134:137], v[128:133], v[8:13], v[134:137] cbsz:2 blgp:2
	v_mfma_f32_16x16x128_f8f6f4 v[204:207], v[128:133], v[44:49], v[204:207] cbsz:2 blgp:2
	v_mfma_f32_16x16x128_f8f6f4 v[138:141], v[128:133], v[20:25], v[138:141] cbsz:2 blgp:2
	v_mfma_f32_16x16x128_f8f6f4 v[208:211], v[128:133], v[56:61], v[208:211] cbsz:2 blgp:2
	v_mfma_f32_16x16x128_f8f6f4 v[142:145], v[128:133], v[32:37], v[142:145] cbsz:2 blgp:2
	v_mfma_f32_16x16x128_f8f6f4 v[212:215], v[128:133], v[68:73], v[212:215] cbsz:2 blgp:2
	v_cndmask_b32_e64 v158, v134, v204, s[4:5]
	v_fma_mix_f32 v158, v158, v1, v147 op_sel:[0,0,1] op_sel_hi:[0,0,1]
	v_exp_f32_e32 v158, v158
	v_cndmask_b32_e64 v159, v138, v208, s[4:5]
	v_fma_mix_f32 v159, v159, v99, v151 op_sel:[0,0,1] op_sel_hi:[0,0,1]
	v_exp_f32_e32 v159, v159
	v_fma_f32 v158, v158, v186, v186
	v_rcp_f32_e32 v158, v158
	v_add_f32_e32 v159, 1.0, v159
	v_rcp_f32_e32 v159, v159
	v_cndmask_b32_e64 v160, v142, v212, s[4:5]
	v_fma_mix_f32 v161, v158, v160, v155 op_sel:[0,0,1] op_sel_hi:[0,0,1]
	v_exp_f32_e32 v161, v161
	s_add_u32 s48, s48, s40
	v_add_f32_e32 v161, 1.0, v161
	v_rcp_f32_e32 v161, v161
	s_addc_u32 s49, s49, s41
	v_fma_f32 v162, v161, -2.0, 1.0
	v_sub_f32_e32 v163, v176, v162
	v_fma_f32 v176, v159, v163, v162
	v_fma_f32 v164, |v176|, s16, v117
	v_fma_f32 v165, |v176|, s17, v118
	v_fma_f32 v166, |v176|, s18, v119
	v_lshrrev_b32_e32 v167, 26, v176
	v_min3_u32 v164, v164, v165, v166
	v_bfi_b32 v168, 31, v164, v167
	global_store_short_d16_hi v185, v176, s[48:49]
	s_nop 0
	v_mul_u32_u24_dpp v170, v168, v180 quad_perm:[1,2,3,3] row_mask:0xf bank_mask:0xf bound_ctrl:1
	v_mad_u32_u24 v171, v168, v181, v170
	ds_write_b8_d16_hi v184, v171
	s_waitcnt lgkmcnt(0)
	s_barrier
	ds_read_b64 v[122:123], v106 offset:0
	ds_read_b64 v[124:125], v106 offset:8
	ds_read_b64 v[126:127], v106 offset:16
	s_barrier
	ds_read_b64 v[128:129], v106 offset:96
	ds_read_b64 v[130:131], v106 offset:104
	ds_read_b64 v[132:133], v106 offset:112
	s_waitcnt lgkmcnt(3)
	v_mfma_f32_16x16x128_f8f6f4 v[134:137], v[122:127], v[2:7], 0 cbsz:2 blgp:2
	v_mfma_f32_16x16x128_f8f6f4 v[138:141], v[122:127], v[14:19], 0 cbsz:2 blgp:2
	v_mfma_f32_16x16x128_f8f6f4 v[142:145], v[122:127], v[26:31], v[188:191] cbsz:2 blgp:2
	v_mfma_f32_16x16x128_f8f6f4 v[204:207], v[122:127], v[38:43], 0 cbsz:2 blgp:2
	v_mfma_f32_16x16x128_f8f6f4 v[208:211], v[122:127], v[50:55], 0 cbsz:2 blgp:2
	v_mfma_f32_16x16x128_f8f6f4 v[212:215], v[122:127], v[62:67], v[188:191] cbsz:2 blgp:2
	s_waitcnt lgkmcnt(0)
	v_mfma_f32_16x16x128_f8f6f4 v[134:137], v[128:133], v[8:13], v[134:137] cbsz:2 blgp:2
	v_mfma_f32_16x16x128_f8f6f4 v[204:207], v[128:133], v[44:49], v[204:207] cbsz:2 blgp:2
	v_mfma_f32_16x16x128_f8f6f4 v[138:141], v[128:133], v[20:25], v[138:141] cbsz:2 blgp:2
	v_mfma_f32_16x16x128_f8f6f4 v[208:211], v[128:133], v[56:61], v[208:211] cbsz:2 blgp:2
	v_mfma_f32_16x16x128_f8f6f4 v[142:145], v[128:133], v[32:37], v[142:145] cbsz:2 blgp:2
	v_mfma_f32_16x16x128_f8f6f4 v[212:215], v[128:133], v[68:73], v[212:215] cbsz:2 blgp:2
	v_cndmask_b32_e64 v158, v134, v204, s[4:5]
	v_fma_mix_f32 v158, v158, v1, v148 op_sel_hi:[0,0,1]
	v_exp_f32_e32 v158, v158
	v_cndmask_b32_e64 v159, v138, v208, s[4:5]
	v_fma_mix_f32 v159, v159, v99, v152 op_sel_hi:[0,0,1]
	v_exp_f32_e32 v159, v159
	v_fma_f32 v158, v158, v186, v186
	v_rcp_f32_e32 v158, v158
	v_add_f32_e32 v159, 1.0, v159
	v_rcp_f32_e32 v159, v159
	v_cndmask_b32_e64 v160, v142, v212, s[4:5]
	v_fma_mix_f32 v161, v158, v160, v156 op_sel_hi:[0,0,1]
	v_exp_f32_e32 v161, v161
	s_add_u32 s48, s48, s40
	v_add_f32_e32 v161, 1.0, v161
	v_rcp_f32_e32 v161, v161
	s_addc_u32 s49, s49, s41
	v_fma_f32 v162, v161, -2.0, 1.0
	v_sub_f32_e32 v163, v176, v162
	v_fma_f32 v176, v159, v163, v162
	v_fma_f32 v164, |v176|, s16, v117
	v_fma_f32 v165, |v176|, s17, v118
	v_fma_f32 v166, |v176|, s18, v119
	v_lshrrev_b32_e32 v167, 26, v176
	v_min3_u32 v164, v164, v165, v166
	v_bfi_b32 v168, 31, v164, v167
	global_store_short_d16_hi v185, v176, s[48:49]
	s_nop 0
	v_mul_u32_u24_dpp v170, v168, v180 quad_perm:[1,2,3,3] row_mask:0xf bank_mask:0xf bound_ctrl:1
	v_mad_u32_u24 v171, v168, v181, v170
	ds_write_b8_d16_hi v184, v171 offset:416
	s_waitcnt lgkmcnt(0)
	s_barrier
	ds_read_b64 v[122:123], v106 offset:416
	ds_read_b64 v[124:125], v106 offset:424
	ds_read_b64 v[126:127], v106 offset:432
	s_barrier
	ds_read_b64 v[128:129], v106 offset:512
	ds_read_b64 v[130:131], v106 offset:520
	ds_read_b64 v[132:133], v106 offset:528
	s_waitcnt lgkmcnt(3)
	v_mfma_f32_16x16x128_f8f6f4 v[134:137], v[122:127], v[2:7], 0 cbsz:2 blgp:2
	v_mfma_f32_16x16x128_f8f6f4 v[138:141], v[122:127], v[14:19], 0 cbsz:2 blgp:2
	v_mfma_f32_16x16x128_f8f6f4 v[142:145], v[122:127], v[26:31], v[188:191] cbsz:2 blgp:2
	v_mfma_f32_16x16x128_f8f6f4 v[204:207], v[122:127], v[38:43], 0 cbsz:2 blgp:2
	v_mfma_f32_16x16x128_f8f6f4 v[208:211], v[122:127], v[50:55], 0 cbsz:2 blgp:2
	v_mfma_f32_16x16x128_f8f6f4 v[212:215], v[122:127], v[62:67], v[188:191] cbsz:2 blgp:2
	s_waitcnt lgkmcnt(0)
	v_mfma_f32_16x16x128_f8f6f4 v[134:137], v[128:133], v[8:13], v[134:137] cbsz:2 blgp:2
	v_mfma_f32_16x16x128_f8f6f4 v[204:207], v[128:133], v[44:49], v[204:207] cbsz:2 blgp:2
	v_mfma_f32_16x16x128_f8f6f4 v[138:141], v[128:133], v[20:25], v[138:141] cbsz:2 blgp:2
	v_mfma_f32_16x16x128_f8f6f4 v[208:211], v[128:133], v[56:61], v[208:211] cbsz:2 blgp:2
	v_mfma_f32_16x16x128_f8f6f4 v[142:145], v[128:133], v[32:37], v[142:145] cbsz:2 blgp:2
	v_mfma_f32_16x16x128_f8f6f4 v[212:215], v[128:133], v[68:73], v[212:215] cbsz:2 blgp:2
	v_cndmask_b32_e64 v158, v134, v204, s[4:5]
	v_fma_mix_f32 v158, v158, v1, v148 op_sel:[0,0,1] op_sel_hi:[0,0,1]
	v_exp_f32_e32 v158, v158
	v_cndmask_b32_e64 v159, v138, v208, s[4:5]
	v_fma_mix_f32 v159, v159, v99, v152 op_sel:[0,0,1] op_sel_hi:[0,0,1]
	v_exp_f32_e32 v159, v159
	v_fma_f32 v158, v158, v186, v186
	v_rcp_f32_e32 v158, v158
	v_add_f32_e32 v159, 1.0, v159
	v_rcp_f32_e32 v159, v159
	v_cndmask_b32_e64 v160, v142, v212, s[4:5]
	v_fma_mix_f32 v161, v158, v160, v156 op_sel:[0,0,1] op_sel_hi:[0,0,1]
	v_exp_f32_e32 v161, v161
	s_add_u32 s48, s48, s40
	v_add_f32_e32 v161, 1.0, v161
	v_rcp_f32_e32 v161, v161
	s_addc_u32 s49, s49, s41
	v_fma_f32 v162, v161, -2.0, 1.0
	v_sub_f32_e32 v163, v176, v162
	v_fma_f32 v176, v159, v163, v162
	v_fma_f32 v164, |v176|, s16, v117
	v_fma_f32 v165, |v176|, s17, v118
	v_fma_f32 v166, |v176|, s18, v119
	v_lshrrev_b32_e32 v167, 26, v176
	v_min3_u32 v164, v164, v165, v166
	v_bfi_b32 v168, 31, v164, v167
	global_store_short_d16_hi v185, v176, s[48:49]
	s_nop 0
	v_mul_u32_u24_dpp v170, v168, v180 quad_perm:[1,2,3,3] row_mask:0xf bank_mask:0xf bound_ctrl:1
	v_mad_u32_u24 v171, v168, v181, v170
	ds_write_b8_d16_hi v184, v171
	s_waitcnt lgkmcnt(0)
	s_barrier
	ds_read_b64 v[122:123], v106 offset:0
	ds_read_b64 v[124:125], v106 offset:8
	ds_read_b64 v[126:127], v106 offset:16
	s_barrier
	ds_read_b64 v[128:129], v106 offset:96
	ds_read_b64 v[130:131], v106 offset:104
	ds_read_b64 v[132:133], v106 offset:112
	s_waitcnt lgkmcnt(3)
	v_mfma_f32_16x16x128_f8f6f4 v[134:137], v[122:127], v[2:7], 0 cbsz:2 blgp:2
	v_mfma_f32_16x16x128_f8f6f4 v[138:141], v[122:127], v[14:19], 0 cbsz:2 blgp:2
	v_mfma_f32_16x16x128_f8f6f4 v[142:145], v[122:127], v[26:31], v[188:191] cbsz:2 blgp:2
	v_mfma_f32_16x16x128_f8f6f4 v[204:207], v[122:127], v[38:43], 0 cbsz:2 blgp:2
	v_mfma_f32_16x16x128_f8f6f4 v[208:211], v[122:127], v[50:55], 0 cbsz:2 blgp:2
	v_mfma_f32_16x16x128_f8f6f4 v[212:215], v[122:127], v[62:67], v[188:191] cbsz:2 blgp:2
	s_waitcnt lgkmcnt(0)
	v_mfma_f32_16x16x128_f8f6f4 v[134:137], v[128:133], v[8:13], v[134:137] cbsz:2 blgp:2
	v_mfma_f32_16x16x128_f8f6f4 v[204:207], v[128:133], v[44:49], v[204:207] cbsz:2 blgp:2
	v_mfma_f32_16x16x128_f8f6f4 v[138:141], v[128:133], v[20:25], v[138:141] cbsz:2 blgp:2
	v_mfma_f32_16x16x128_f8f6f4 v[208:211], v[128:133], v[56:61], v[208:211] cbsz:2 blgp:2
	v_mfma_f32_16x16x128_f8f6f4 v[142:145], v[128:133], v[32:37], v[142:145] cbsz:2 blgp:2
	v_mfma_f32_16x16x128_f8f6f4 v[212:215], v[128:133], v[68:73], v[212:215] cbsz:2 blgp:2
	v_cndmask_b32_e64 v158, v134, v204, s[4:5]
	v_fma_mix_f32 v158, v158, v1, v149 op_sel_hi:[0,0,1]
	v_exp_f32_e32 v158, v158
	v_cndmask_b32_e64 v159, v138, v208, s[4:5]
	v_fma_mix_f32 v159, v159, v99, v153 op_sel_hi:[0,0,1]
	v_exp_f32_e32 v159, v159
	v_fma_f32 v158, v158, v186, v186
	v_rcp_f32_e32 v158, v158
	v_add_f32_e32 v159, 1.0, v159
	v_rcp_f32_e32 v159, v159
	v_cndmask_b32_e64 v160, v142, v212, s[4:5]
	v_fma_mix_f32 v161, v158, v160, v157 op_sel_hi:[0,0,1]
	v_exp_f32_e32 v161, v161
	s_add_u32 s48, s48, s40
	v_add_f32_e32 v161, 1.0, v161
	v_rcp_f32_e32 v161, v161
	s_addc_u32 s49, s49, s41
	v_fma_f32 v162, v161, -2.0, 1.0
	v_sub_f32_e32 v163, v176, v162
	v_fma_f32 v176, v159, v163, v162
	v_fma_f32 v164, |v176|, s16, v117
	v_fma_f32 v165, |v176|, s17, v118
	v_fma_f32 v166, |v176|, s18, v119
	v_lshrrev_b32_e32 v167, 26, v176
	v_min3_u32 v164, v164, v165, v166
	v_bfi_b32 v168, 31, v164, v167
	global_store_short_d16_hi v185, v176, s[48:49]
	s_nop 0
	v_mul_u32_u24_dpp v170, v168, v180 quad_perm:[1,2,3,3] row_mask:0xf bank_mask:0xf bound_ctrl:1
	v_mad_u32_u24 v171, v168, v181, v170
	ds_write_b8_d16_hi v184, v171 offset:416
	s_waitcnt lgkmcnt(0)
	s_barrier
	ds_read_b64 v[122:123], v106 offset:416
	ds_read_b64 v[124:125], v106 offset:424
	ds_read_b64 v[126:127], v106 offset:432
	s_barrier
	ds_read_b64 v[128:129], v106 offset:512
	ds_read_b64 v[130:131], v106 offset:520
	ds_read_b64 v[132:133], v106 offset:528
	s_add_i32 s44, s44, 16
	s_waitcnt lgkmcnt(3)
	v_mfma_f32_16x16x128_f8f6f4 v[134:137], v[122:127], v[2:7], 0 cbsz:2 blgp:2
	v_mfma_f32_16x16x128_f8f6f4 v[138:141], v[122:127], v[14:19], 0 cbsz:2 blgp:2
	v_mfma_f32_16x16x128_f8f6f4 v[142:145], v[122:127], v[26:31], v[188:191] cbsz:2 blgp:2
	v_mfma_f32_16x16x128_f8f6f4 v[204:207], v[122:127], v[38:43], 0 cbsz:2 blgp:2
	v_mfma_f32_16x16x128_f8f6f4 v[208:211], v[122:127], v[50:55], 0 cbsz:2 blgp:2
	v_mfma_f32_16x16x128_f8f6f4 v[212:215], v[122:127], v[62:67], v[188:191] cbsz:2 blgp:2
	s_waitcnt lgkmcnt(0)
	v_mfma_f32_16x16x128_f8f6f4 v[134:137], v[128:133], v[8:13], v[134:137] cbsz:2 blgp:2
	v_mfma_f32_16x16x128_f8f6f4 v[204:207], v[128:133], v[44:49], v[204:207] cbsz:2 blgp:2
	v_mfma_f32_16x16x128_f8f6f4 v[138:141], v[128:133], v[20:25], v[138:141] cbsz:2 blgp:2
	v_mfma_f32_16x16x128_f8f6f4 v[208:211], v[128:133], v[56:61], v[208:211] cbsz:2 blgp:2
	v_mfma_f32_16x16x128_f8f6f4 v[142:145], v[128:133], v[32:37], v[142:145] cbsz:2 blgp:2
	v_mfma_f32_16x16x128_f8f6f4 v[212:215], v[128:133], v[68:73], v[212:215] cbsz:2 blgp:2
	v_cndmask_b32_e64 v158, v134, v204, s[4:5]
	v_fma_mix_f32 v158, v158, v1, v149 op_sel:[0,0,1] op_sel_hi:[0,0,1]
	v_exp_f32_e32 v158, v158
	v_cndmask_b32_e64 v159, v138, v208, s[4:5]
	v_fma_mix_f32 v159, v159, v99, v153 op_sel:[0,0,1] op_sel_hi:[0,0,1]
	v_exp_f32_e32 v159, v159
	v_fma_f32 v158, v158, v186, v186
	v_rcp_f32_e32 v158, v158
	v_add_f32_e32 v159, 1.0, v159
	v_rcp_f32_e32 v159, v159
	v_cndmask_b32_e64 v160, v142, v212, s[4:5]
	v_fma_mix_f32 v161, v158, v160, v157 op_sel:[0,0,1] op_sel_hi:[0,0,1]
	v_exp_f32_e32 v161, v161
	s_add_u32 s48, s48, s40
	v_add_f32_e32 v161, 1.0, v161
	v_rcp_f32_e32 v161, v161
	s_addc_u32 s49, s49, s41
	v_fma_f32 v162, v161, -2.0, 1.0
	v_sub_f32_e32 v163, v176, v162
	v_fma_f32 v176, v159, v163, v162
	v_fma_f32 v164, |v176|, s16, v117
	v_fma_f32 v165, |v176|, s17, v118
	v_fma_f32 v166, |v176|, s18, v119
	v_lshrrev_b32_e32 v167, 26, v176
	v_min3_u32 v164, v164, v165, v166
	v_bfi_b32 v168, 31, v164, v167
	global_store_short_d16_hi v185, v176, s[48:49]
	s_nop 0
	v_mul_u32_u24_dpp v170, v168, v180 quad_perm:[1,2,3,3] row_mask:0xf bank_mask:0xf bound_ctrl:1
	v_mad_u32_u24 v171, v168, v181, v170
	ds_write_b8_d16_hi v184, v171
	s_waitcnt lgkmcnt(0)
	s_barrier
	ds_read_b64 v[122:123], v106 offset:0
	ds_read_b64 v[124:125], v106 offset:8
	ds_read_b64 v[126:127], v106 offset:16
	s_cmp_lt_i32 s44, s45
	s_barrier
	s_cbranch_scc1 .Lscan_loop_a_st
	s_branch .Lscan_exit_st
.Lscan_loop_b_st:
	ds_read_b64 v[122:123], v106 offset:0
	ds_read_b64 v[124:125], v106 offset:8
	ds_read_b64 v[126:127], v106 offset:16
	ds_read_b64 v[128:129], v106 offset:96
	ds_read_b64 v[130:131], v106 offset:104
	ds_read_b64 v[132:133], v106 offset:112
	s_waitcnt vmcnt(8)
	global_load_dwordx4 v[146:149], v[196:197], off
	global_load_dwordx4 v[150:153], v[196:197], off offset:512
	global_load_dwordx4 v[154:157], v[196:197], off offset:1024
	v_lshl_add_u64 v[196:197], v[196:197], 0, s[42:43]
	s_waitcnt lgkmcnt(3)
	v_mfma_f32_16x16x128_f8f6f4 v[134:137], v[122:127], v[2:7], 0 cbsz:2 blgp:2
	v_mfma_f32_16x16x128_f8f6f4 v[138:141], v[122:127], v[14:19], 0 cbsz:2 blgp:2
	v_mfma_f32_16x16x128_f8f6f4 v[142:145], v[122:127], v[26:31], v[188:191] cbsz:2 blgp:2
	v_mfma_f32_16x16x128_f8f6f4 v[204:207], v[122:127], v[38:43], 0 cbsz:2 blgp:2
	v_mfma_f32_16x16x128_f8f6f4 v[208:211], v[122:127], v[50:55], 0 cbsz:2 blgp:2
	v_mfma_f32_16x16x128_f8f6f4 v[212:215], v[122:127], v[62:67], v[188:191] cbsz:2 blgp:2
	s_waitcnt lgkmcnt(0)
	v_mfma_f32_16x16x128_f8f6f4 v[134:137], v[128:133], v[8:13], v[134:137] cbsz:2 blgp:2
	v_mfma_f32_16x16x128_f8f6f4 v[204:207], v[128:133], v[44:49], v[204:207] cbsz:2 blgp:2
	v_mfma_f32_16x16x128_f8f6f4 v[138:141], v[128:133], v[20:25], v[138:141] cbsz:2 blgp:2
	v_mfma_f32_16x16x128_f8f6f4 v[208:211], v[128:133], v[56:61], v[208:211] cbsz:2 blgp:2
	v_mfma_f32_16x16x128_f8f6f4 v[142:145], v[128:133], v[32:37], v[142:145] cbsz:2 blgp:2
	v_mfma_f32_16x16x128_f8f6f4 v[212:215], v[128:133], v[68:73], v[212:215] cbsz:2 blgp:2
	v_cndmask_b32_e64 v158, v134, v204, s[4:5]
	v_fma_mix_f32 v158, v158, v1, v82 op_sel_hi:[0,0,1]
	v_exp_f32_e32 v158, v158
	v_cndmask_b32_e64 v159, v138, v208, s[4:5]
	v_fma_mix_f32 v159, v159, v99, v74 op_sel_hi:[0,0,1]
	v_exp_f32_e32 v159, v159
	v_fma_f32 v158, v158, v186, v186
	v_rcp_f32_e32 v158, v158
	v_add_f32_e32 v159, 1.0, v159
	v_rcp_f32_e32 v159, v159
	v_cndmask_b32_e64 v160, v142, v212, s[4:5]
	v_fma_mix_f32 v161, v158, v160, v78 op_sel_hi:[0,0,1]
	v_exp_f32_e32 v161, v161
	s_add_u32 s48, s48, s40
	v_add_f32_e32 v161, 1.0, v161
	v_rcp_f32_e32 v161, v161
	s_addc_u32 s49, s49, s41
	v_fma_f32 v162, v161, -2.0, 1.0
	v_sub_f32_e32 v163, v176, v162
	v_fma_f32 v176, v159, v163, v162
	v_fma_f32 v164, |v176|, s16, v117
	v_fma_f32 v165, |v176|, s17, v118
	v_fma_f32 v166, |v176|, s18, v119
	v_lshrrev_b32_e32 v167, 26, v176
	v_min3_u32 v164, v164, v165, v166
	v_bfi_b32 v168, 31, v164, v167
	global_store_short_d16_hi v185, v176, s[48:49]
	s_nop 0
	v_mul_u32_u24_dpp v170, v168, v180 quad_perm:[1,2,3,3] row_mask:0xf bank_mask:0xf bound_ctrl:1
	v_mad_u32_u24 v171, v168, v181, v170
	ds_write_b8_d16_hi v184, v171 offset:416
	s_barrier
	s_waitcnt lgkmcnt(0)
	s_barrier
	ds_read_b64 v[122:123], v106 offset:416
	ds_read_b64 v[124:125], v106 offset:424
	ds_read_b64 v[126:127], v106 offset:432
	ds_read_b64 v[128:129], v106 offset:512
	ds_read_b64 v[130:131], v106 offset:520
	ds_read_b64 v[132:133], v106 offset:528
	s_waitcnt lgkmcnt(3)
	v_mfma_f32_16x16x128_f8f6f4 v[134:137], v[122:127], v[2:7], 0 cbsz:2 blgp:2
	v_mfma_f32_16x16x128_f8f6f4 v[138:141], v[122:127], v[14:19], 0 cbsz:2 blgp:2
	v_mfma_f32_16x16x128_f8f6f4 v[142:145], v[122:127], v[26:31], v[188:191] cbsz:2 blgp:2
	v_mfma_f32_16x16x128_f8f6f4 v[204:207], v[122:127], v[38:43], 0 cbsz:2 blgp:2
	v_mfma_f32_16x16x128_f8f6f4 v[208:211], v[122:127], v[50:55], 0 cbsz:2 blgp:2
	v_mfma_f32_16x16x128_f8f6f4 v[212:215], v[122:127], v[62:67], v[188:191] cbsz:2 blgp:2
	s_waitcnt lgkmcnt(0)
	v_mfma_f32_16x16x128_f8f6f4 v[134:137], v[128:133], v[8:13], v[134:137] cbsz:2 blgp:2
	v_mfma_f32_16x16x128_f8f6f4 v[204:207], v[128:133], v[44:49], v[204:207] cbsz:2 blgp:2
	v_mfma_f32_16x16x128_f8f6f4 v[138:141], v[128:133], v[20:25], v[138:141] cbsz:2 blgp:2
	v_mfma_f32_16x16x128_f8f6f4 v[208:211], v[128:133], v[56:61], v[208:211] cbsz:2 blgp:2
	v_mfma_f32_16x16x128_f8f6f4 v[142:145], v[128:133], v[32:37], v[142:145] cbsz:2 blgp:2
	v_mfma_f32_16x16x128_f8f6f4 v[212:215], v[128:133], v[68:73], v[212:215] cbsz:2 blgp:2
	v_cndmask_b32_e64 v158, v134, v204, s[4:5]
	v_fma_mix_f32 v158, v158, v1, v82 op_sel:[0,0,1] op_sel_hi:[0,0,1]
	v_exp_f32_e32 v158, v158
	v_cndmask_b32_e64 v159, v138, v208, s[4:5]
	v_fma_mix_f32 v159, v159, v99, v74 op_sel:[0,0,1] op_sel_hi:[0,0,1]
	v_exp_f32_e32 v159, v159
	v_fma_f32 v158, v158, v186, v186
	v_rcp_f32_e32 v158, v158
	v_add_f32_e32 v159, 1.0, v159
	v_rcp_f32_e32 v159, v159
	v_cndmask_b32_e64 v160, v142, v212, s[4:5]
	v_fma_mix_f32 v161, v158, v160, v78 op_sel:[0,0,1] op_sel_hi:[0,0,1]
	v_exp_f32_e32 v161, v161
	s_add_u32 s48, s48, s40
	v_add_f32_e32 v161, 1.0, v161
	v_rcp_f32_e32 v161, v161
	s_addc_u32 s49, s49, s41
	v_fma_f32 v162, v161, -2.0, 1.0
	v_sub_f32_e32 v163, v176, v162
	v_fma_f32 v176, v159, v163, v162
	v_fma_f32 v164, |v176|, s16, v117
	v_fma_f32 v165, |v176|, s17, v118
	v_fma_f32 v166, |v176|, s18, v119
	v_lshrrev_b32_e32 v167, 26, v176
	v_min3_u32 v164, v164, v165, v166
	v_bfi_b32 v168, 31, v164, v167
	global_store_short_d16_hi v185, v176, s[48:49]
	s_nop 0
	v_mul_u32_u24_dpp v170, v168, v180 quad_perm:[1,2,3,3] row_mask:0xf bank_mask:0xf bound_ctrl:1
	v_mad_u32_u24 v171, v168, v181, v170
	ds_write_b8_d16_hi v184, v171
	s_barrier
	s_waitcnt lgkmcnt(0)
	s_barrier
	ds_read_b64 v[122:123], v106 offset:0
	ds_read_b64 v[124:125], v106 offset:8
	ds_read_b64 v[126:127], v106 offset:16
	ds_read_b64 v[128:129], v106 offset:96
	ds_read_b64 v[130:131], v106 offset:104
	ds_read_b64 v[132:133], v106 offset:112
	s_waitcnt lgkmcnt(3)
	v_mfma_f32_16x16x128_f8f6f4 v[134:137], v[122:127], v[2:7], 0 cbsz:2 blgp:2
	v_mfma_f32_16x16x128_f8f6f4 v[138:141], v[122:127], v[14:19], 0 cbsz:2 blgp:2
	v_mfma_f32_16x16x128_f8f6f4 v[142:145], v[122:127], v[26:31], v[188:191] cbsz:2 blgp:2
	v_mfma_f32_16x16x128_f8f6f4 v[204:207], v[122:127], v[38:43], 0 cbsz:2 blgp:2
	v_mfma_f32_16x16x128_f8f6f4 v[208:211], v[122:127], v[50:55], 0 cbsz:2 blgp:2
	v_mfma_f32_16x16x128_f8f6f4 v[212:215], v[122:127], v[62:67], v[188:191] cbsz:2 blgp:2
	s_waitcnt lgkmcnt(0)
	v_mfma_f32_16x16x128_f8f6f4 v[134:137], v[128:133], v[8:13], v[134:137] cbsz:2 blgp:2
	v_mfma_f32_16x16x128_f8f6f4 v[204:207], v[128:133], v[44:49], v[204:207] cbsz:2 blgp:2
	v_mfma_f32_16x16x128_f8f6f4 v[138:141], v[128:133], v[20:25], v[138:141] cbsz:2 blgp:2
	v_mfma_f32_16x16x128_f8f6f4 v[208:211], v[128:133], v[56:61], v[208:211] cbsz:2 blgp:2
	v_mfma_f32_16x16x128_f8f6f4 v[142:145], v[128:133], v[32:37], v[142:145] cbsz:2 blgp:2
	v_mfma_f32_16x16x128_f8f6f4 v[212:215], v[128:133], v[68:73], v[212:215] cbsz:2 blgp:2
	v_cndmask_b32_e64 v158, v134, v204, s[4:5]
	v_fma_mix_f32 v158, v158, v1, v83 op_sel_hi:[0,0,1]
	v_exp_f32_e32 v158, v158
	v_cndmask_b32_e64 v159, v138, v208, s[4:5]
	v_fma_mix_f32 v159, v159, v99, v75 op_sel_hi:[0,0,1]
	v_exp_f32_e32 v159, v159
	v_fma_f32 v158, v158, v186, v186
	v_rcp_f32_e32 v158, v158
	v_add_f32_e32 v159, 1.0, v159
	v_rcp_f32_e32 v159, v159
	v_cndmask_b32_e64 v160, v142, v212, s[4:5]
	v_fma_mix_f32 v161, v158, v160, v79 op_sel_hi:[0,0,1]
	v_exp_f32_e32 v161, v161
	s_add_u32 s48, s48, s40
	v_add_f32_e32 v161, 1.0, v161
	v_rcp_f32_e32 v161, v161
	s_addc_u32 s49, s49, s41
	v_fma_f32 v162, v161, -2.0, 1.0
	v_sub_f32_e32 v163, v176, v162
	v_fma_f32 v176, v159, v163, v162
	v_fma_f32 v164, |v176|, s16, v117
	v_fma_f32 v165, |v176|, s17, v118
	v_fma_f32 v166, |v176|, s18, v119
	v_lshrrev_b32_e32 v167, 26, v176
	v_min3_u32 v164, v164, v165, v166
	v_bfi_b32 v168, 31, v164, v167
	global_store_short_d16_hi v185, v176, s[48:49]
	s_nop 0
	v_mul_u32_u24_dpp v170, v168, v180 quad_perm:[1,2,3,3] row_mask:0xf bank_mask:0xf bound_ctrl:1
	v_mad_u32_u24 v171, v168, v181, v170
	ds_write_b8_d16_hi v184, v171 offset:416
	s_barrier
	s_waitcnt lgkmcnt(0)
	s_barrier
	ds_read_b64 v[122:123], v106 offset:416
	ds_read_b64 v[124:125], v106 offset:424
	ds_read_b64 v[126:127], v106 offset:432
	ds_read_b64 v[128:129], v106 offset:512
	ds_read_b64 v[130:131], v106 offset:520
	ds_read_b64 v[132:133], v106 offset:528
	s_waitcnt lgkmcnt(3)
	v_mfma_f32_16x16x128_f8f6f4 v[134:137], v[122:127], v[2:7], 0 cbsz:2 blgp:2
	v_mfma_f32_16x16x128_f8f6f4 v[138:141], v[122:127], v[14:19], 0 cbsz:2 blgp:2
	v_mfma_f32_16x16x128_f8f6f4 v[142:145], v[122:127], v[26:31], v[188:191] cbsz:2 blgp:2
	v_mfma_f32_16x16x128_f8f6f4 v[204:207], v[122:127], v[38:43], 0 cbsz:2 blgp:2
	v_mfma_f32_16x16x128_f8f6f4 v[208:211], v[122:127], v[50:55], 0 cbsz:2 blgp:2
	v_mfma_f32_16x16x128_f8f6f4 v[212:215], v[122:127], v[62:67], v[188:191] cbsz:2 blgp:2
	s_waitcnt lgkmcnt(0)
	v_mfma_f32_16x16x128_f8f6f4 v[134:137], v[128:133], v[8:13], v[134:137] cbsz:2 blgp:2
	v_mfma_f32_16x16x128_f8f6f4 v[204:207], v[128:133], v[44:49], v[204:207] cbsz:2 blgp:2
	v_mfma_f32_16x16x128_f8f6f4 v[138:141], v[128:133], v[20:25], v[138:141] cbsz:2 blgp:2
	v_mfma_f32_16x16x128_f8f6f4 v[208:211], v[128:133], v[56:61], v[208:211] cbsz:2 blgp:2
	v_mfma_f32_16x16x128_f8f6f4 v[142:145], v[128:133], v[32:37], v[142:145] cbsz:2 blgp:2
	v_mfma_f32_16x16x128_f8f6f4 v[212:215], v[128:133], v[68:73], v[212:215] cbsz:2 blgp:2
	v_cndmask_b32_e64 v158, v134, v204, s[4:5]
	v_fma_mix_f32 v158, v158, v1, v83 op_sel:[0,0,1] op_sel_hi:[0,0,1]
	v_exp_f32_e32 v158, v158
	v_cndmask_b32_e64 v159, v138, v208, s[4:5]
	v_fma_mix_f32 v159, v159, v99, v75 op_sel:[0,0,1] op_sel_hi:[0,0,1]
	v_exp_f32_e32 v159, v159
	v_fma_f32 v158, v158, v186, v186
	v_rcp_f32_e32 v158, v158
	v_add_f32_e32 v159, 1.0, v159
	v_rcp_f32_e32 v159, v159
	v_cndmask_b32_e64 v160, v142, v212, s[4:5]
	v_fma_mix_f32 v161, v158, v160, v79 op_sel:[0,0,1] op_sel_hi:[0,0,1]
	v_exp_f32_e32 v161, v161
	s_add_u32 s48, s48, s40
	v_add_f32_e32 v161, 1.0, v161
	v_rcp_f32_e32 v161, v161
	s_addc_u32 s49, s49, s41
	v_fma_f32 v162, v161, -2.0, 1.0
	v_sub_f32_e32 v163, v176, v162
	v_fma_f32 v176, v159, v163, v162
	v_fma_f32 v164, |v176|, s16, v117
	v_fma_f32 v165, |v176|, s17, v118
	v_fma_f32 v166, |v176|, s18, v119
	v_lshrrev_b32_e32 v167, 26, v176
	v_min3_u32 v164, v164, v165, v166
	v_bfi_b32 v168, 31, v164, v167
	global_store_short_d16_hi v185, v176, s[48:49]
	s_nop 0
	v_mul_u32_u24_dpp v170, v168, v180 quad_perm:[1,2,3,3] row_mask:0xf bank_mask:0xf bound_ctrl:1
	v_mad_u32_u24 v171, v168, v181, v170
	ds_write_b8_d16_hi v184, v171
	s_barrier
	s_waitcnt lgkmcnt(0)
	s_barrier
	ds_read_b64 v[122:123], v106 offset:0
	ds_read_b64 v[124:125], v106 offset:8
	ds_read_b64 v[126:127], v106 offset:16
	ds_read_b64 v[128:129], v106 offset:96
	ds_read_b64 v[130:131], v106 offset:104
	ds_read_b64 v[132:133], v106 offset:112
	s_waitcnt lgkmcnt(3)
	v_mfma_f32_16x16x128_f8f6f4 v[134:137], v[122:127], v[2:7], 0 cbsz:2 blgp:2
	v_mfma_f32_16x16x128_f8f6f4 v[138:141], v[122:127], v[14:19], 0 cbsz:2 blgp:2
	v_mfma_f32_16x16x128_f8f6f4 v[142:145], v[122:127], v[26:31], v[188:191] cbsz:2 blgp:2
	v_mfma_f32_16x16x128_f8f6f4 v[204:207], v[122:127], v[38:43], 0 cbsz:2 blgp:2
	v_mfma_f32_16x16x128_f8f6f4 v[208:211], v[122:127], v[50:55], 0 cbsz:2 blgp:2
	v_mfma_f32_16x16x128_f8f6f4 v[212:215], v[122:127], v[62:67], v[188:191] cbsz:2 blgp:2
	s_waitcnt lgkmcnt(0)
	v_mfma_f32_16x16x128_f8f6f4 v[134:137], v[128:133], v[8:13], v[134:137] cbsz:2 blgp:2
	v_mfma_f32_16x16x128_f8f6f4 v[204:207], v[128:133], v[44:49], v[204:207] cbsz:2 blgp:2
	v_mfma_f32_16x16x128_f8f6f4 v[138:141], v[128:133], v[20:25], v[138:141] cbsz:2 blgp:2
	v_mfma_f32_16x16x128_f8f6f4 v[208:211], v[128:133], v[56:61], v[208:211] cbsz:2 blgp:2
	v_mfma_f32_16x16x128_f8f6f4 v[142:145], v[128:133], v[32:37], v[142:145] cbsz:2 blgp:2
	v_mfma_f32_16x16x128_f8f6f4 v[212:215], v[128:133], v[68:73], v[212:215] cbsz:2 blgp:2
	v_cndmask_b32_e64 v158, v134, v204, s[4:5]
	v_fma_mix_f32 v158, v158, v1, v84 op_sel_hi:[0,0,1]
	v_exp_f32_e32 v158, v158
	v_cndmask_b32_e64 v159, v138, v208, s[4:5]
	v_fma_mix_f32 v159, v159, v99, v76 op_sel_hi:[0,0,1]
	v_exp_f32_e32 v159, v159
	v_fma_f32 v158, v158, v186, v186
	v_rcp_f32_e32 v158, v158
	v_add_f32_e32 v159, 1.0, v159
	v_rcp_f32_e32 v159, v159
	v_cndmask_b32_e64 v160, v142, v212, s[4:5]
	v_fma_mix_f32 v161, v158, v160, v80 op_sel_hi:[0,0,1]
	v_exp_f32_e32 v161, v161
	s_add_u32 s48, s48, s40
	v_add_f32_e32 v161, 1.0, v161
	v_rcp_f32_e32 v161, v161
	s_addc_u32 s49, s49, s41
	v_fma_f32 v162, v161, -2.0, 1.0
	v_sub_f32_e32 v163, v176, v162
	v_fma_f32 v176, v159, v163, v162
	v_fma_f32 v164, |v176|, s16, v117
	v_fma_f32 v165, |v176|, s17, v118
	v_fma_f32 v166, |v176|, s18, v119
	v_lshrrev_b32_e32 v167, 26, v176
	v_min3_u32 v164, v164, v165, v166
	v_bfi_b32 v168, 31, v164, v167
	global_store_short_d16_hi v185, v176, s[48:49]
	s_nop 0
	v_mul_u32_u24_dpp v170, v168, v180 quad_perm:[1,2,3,3] row_mask:0xf bank_mask:0xf bound_ctrl:1
	v_mad_u32_u24 v171, v168, v181, v170
	ds_write_b8_d16_hi v184, v171 offset:416
	s_barrier
	s_waitcnt lgkmcnt(0)
	s_barrier
	ds_read_b64 v[122:123], v106 offset:416
	ds_read_b64 v[124:125], v106 offset:424
	ds_read_b64 v[126:127], v106 offset:432
	ds_read_b64 v[128:129], v106 offset:512
	ds_read_b64 v[130:131], v106 offset:520
	ds_read_b64 v[132:133], v106 offset:528
	s_waitcnt lgkmcnt(3)
	v_mfma_f32_16x16x128_f8f6f4 v[134:137], v[122:127], v[2:7], 0 cbsz:2 blgp:2
	v_mfma_f32_16x16x128_f8f6f4 v[138:141], v[122:127], v[14:19], 0 cbsz:2 blgp:2
	v_mfma_f32_16x16x128_f8f6f4 v[142:145], v[122:127], v[26:31], v[188:191] cbsz:2 blgp:2
	v_mfma_f32_16x16x128_f8f6f4 v[204:207], v[122:127], v[38:43], 0 cbsz:2 blgp:2
	v_mfma_f32_16x16x128_f8f6f4 v[208:211], v[122:127], v[50:55], 0 cbsz:2 blgp:2
	v_mfma_f32_16x16x128_f8f6f4 v[212:215], v[122:127], v[62:67], v[188:191] cbsz:2 blgp:2
	s_waitcnt lgkmcnt(0)
	v_mfma_f32_16x16x128_f8f6f4 v[134:137], v[128:133], v[8:13], v[134:137] cbsz:2 blgp:2
	v_mfma_f32_16x16x128_f8f6f4 v[204:207], v[128:133], v[44:49], v[204:207] cbsz:2 blgp:2
	v_mfma_f32_16x16x128_f8f6f4 v[138:141], v[128:133], v[20:25], v[138:141] cbsz:2 blgp:2
	v_mfma_f32_16x16x128_f8f6f4 v[208:211], v[128:133], v[56:61], v[208:211] cbsz:2 blgp:2
	v_mfma_f32_16x16x128_f8f6f4 v[142:145], v[128:133], v[32:37], v[142:145] cbsz:2 blgp:2
	v_mfma_f32_16x16x128_f8f6f4 v[212:215], v[128:133], v[68:73], v[212:215] cbsz:2 blgp:2
	v_cndmask_b32_e64 v158, v134, v204, s[4:5]
	v_fma_mix_f32 v158, v158, v1, v84 op_sel:[0,0,1] op_sel_hi:[0,0,1]
	v_exp_f32_e32 v158, v158
	v_cndmask_b32_e64 v159, v138, v208, s[4:5]
	v_fma_mix_f32 v159, v159, v99, v76 op_sel:[0,0,1] op_sel_hi:[0,0,1]
	v_exp_f32_e32 v159, v159
	v_fma_f32 v158, v158, v186, v186
	v_rcp_f32_e32 v158, v158
	v_add_f32_e32 v159, 1.0, v159
	v_rcp_f32_e32 v159, v159
	v_cndmask_b32_e64 v160, v142, v212, s[4:5]
	v_fma_mix_f32 v161, v158, v160, v80 op_sel:[0,0,1] op_sel_hi:[0,0,1]
	v_exp_f32_e32 v161, v161
	s_add_u32 s48, s48, s40
	v_add_f32_e32 v161, 1.0, v161
	v_rcp_f32_e32 v161, v161
	s_addc_u32 s49, s49, s41
	v_fma_f32 v162, v161, -2.0, 1.0
	v_sub_f32_e32 v163, v176, v162
	v_fma_f32 v176, v159, v163, v162
	v_fma_f32 v164, |v176|, s16, v117
	v_fma_f32 v165, |v176|, s17, v118
	v_fma_f32 v166, |v176|, s18, v119
	v_lshrrev_b32_e32 v167, 26, v176
	v_min3_u32 v164, v164, v165, v166
	v_bfi_b32 v168, 31, v164, v167
	global_store_short_d16_hi v185, v176, s[48:49]
	s_nop 0
	v_mul_u32_u24_dpp v170, v168, v180 quad_perm:[1,2,3,3] row_mask:0xf bank_mask:0xf bound_ctrl:1
	v_mad_u32_u24 v171, v168, v181, v170
	ds_write_b8_d16_hi v184, v171
	s_barrier
	s_waitcnt lgkmcnt(0)
	s_barrier
	ds_read_b64 v[122:123], v106 offset:0
	ds_read_b64 v[124:125], v106 offset:8
	ds_read_b64 v[126:127], v106 offset:16
	ds_read_b64 v[128:129], v106 offset:96
	ds_read_b64 v[130:131], v106 offset:104
	ds_read_b64 v[132:133], v106 offset:112
	s_waitcnt lgkmcnt(3)
	v_mfma_f32_16x16x128_f8f6f4 v[134:137], v[122:127], v[2:7], 0 cbsz:2 blgp:2
	v_mfma_f32_16x16x128_f8f6f4 v[138:141], v[122:127], v[14:19], 0 cbsz:2 blgp:2
	v_mfma_f32_16x16x128_f8f6f4 v[142:145], v[122:127], v[26:31], v[188:191] cbsz:2 blgp:2
	v_mfma_f32_16x16x128_f8f6f4 v[204:207], v[122:127], v[38:43], 0 cbsz:2 blgp:2
	v_mfma_f32_16x16x128_f8f6f4 v[208:211], v[122:127], v[50:55], 0 cbsz:2 blgp:2
	v_mfma_f32_16x16x128_f8f6f4 v[212:215], v[122:127], v[62:67], v[188:191] cbsz:2 blgp:2
	s_waitcnt lgkmcnt(0)
	v_mfma_f32_16x16x128_f8f6f4 v[134:137], v[128:133], v[8:13], v[134:137] cbsz:2 blgp:2
	v_mfma_f32_16x16x128_f8f6f4 v[204:207], v[128:133], v[44:49], v[204:207] cbsz:2 blgp:2
	v_mfma_f32_16x16x128_f8f6f4 v[138:141], v[128:133], v[20:25], v[138:141] cbsz:2 blgp:2
	v_mfma_f32_16x16x128_f8f6f4 v[208:211], v[128:133], v[56:61], v[208:211] cbsz:2 blgp:2
	v_mfma_f32_16x16x128_f8f6f4 v[142:145], v[128:133], v[32:37], v[142:145] cbsz:2 blgp:2
	v_mfma_f32_16x16x128_f8f6f4 v[212:215], v[128:133], v[68:73], v[212:215] cbsz:2 blgp:2
	v_cndmask_b32_e64 v158, v134, v204, s[4:5]
	v_fma_mix_f32 v158, v158, v1, v85 op_sel_hi:[0,0,1]
	v_exp_f32_e32 v158, v158
	v_cndmask_b32_e64 v159, v138, v208, s[4:5]
	v_fma_mix_f32 v159, v159, v99, v77 op_sel_hi:[0,0,1]
	v_exp_f32_e32 v159, v159
	v_fma_f32 v158, v158, v186, v186
	v_rcp_f32_e32 v158, v158
	v_add_f32_e32 v159, 1.0, v159
	v_rcp_f32_e32 v159, v159
	v_cndmask_b32_e64 v160, v142, v212, s[4:5]
	v_fma_mix_f32 v161, v158, v160, v81 op_sel_hi:[0,0,1]
	v_exp_f32_e32 v161, v161
	s_add_u32 s48, s48, s40
	v_add_f32_e32 v161, 1.0, v161
	v_rcp_f32_e32 v161, v161
	s_addc_u32 s49, s49, s41
	v_fma_f32 v162, v161, -2.0, 1.0
	v_sub_f32_e32 v163, v176, v162
	v_fma_f32 v176, v159, v163, v162
	v_fma_f32 v164, |v176|, s16, v117
	v_fma_f32 v165, |v176|, s17, v118
	v_fma_f32 v166, |v176|, s18, v119
	v_lshrrev_b32_e32 v167, 26, v176
	v_min3_u32 v164, v164, v165, v166
	v_bfi_b32 v168, 31, v164, v167
	global_store_short_d16_hi v185, v176, s[48:49]
	s_nop 0
	v_mul_u32_u24_dpp v170, v168, v180 quad_perm:[1,2,3,3] row_mask:0xf bank_mask:0xf bound_ctrl:1
	v_mad_u32_u24 v171, v168, v181, v170
	ds_write_b8_d16_hi v184, v171 offset:416
	s_barrier
	s_waitcnt lgkmcnt(0)
	s_barrier
	ds_read_b64 v[122:123], v106 offset:416
	ds_read_b64 v[124:125], v106 offset:424
	ds_read_b64 v[126:127], v106 offset:432
	ds_read_b64 v[128:129], v106 offset:512
	ds_read_b64 v[130:131], v106 offset:520
	ds_read_b64 v[132:133], v106 offset:528
	s_waitcnt lgkmcnt(3)
	v_mfma_f32_16x16x128_f8f6f4 v[134:137], v[122:127], v[2:7], 0 cbsz:2 blgp:2
	v_mfma_f32_16x16x128_f8f6f4 v[138:141], v[122:127], v[14:19], 0 cbsz:2 blgp:2
	v_mfma_f32_16x16x128_f8f6f4 v[142:145], v[122:127], v[26:31], v[188:191] cbsz:2 blgp:2
	v_mfma_f32_16x16x128_f8f6f4 v[204:207], v[122:127], v[38:43], 0 cbsz:2 blgp:2
	v_mfma_f32_16x16x128_f8f6f4 v[208:211], v[122:127], v[50:55], 0 cbsz:2 blgp:2
	v_mfma_f32_16x16x128_f8f6f4 v[212:215], v[122:127], v[62:67], v[188:191] cbsz:2 blgp:2
	s_waitcnt lgkmcnt(0)
	v_mfma_f32_16x16x128_f8f6f4 v[134:137], v[128:133], v[8:13], v[134:137] cbsz:2 blgp:2
	v_mfma_f32_16x16x128_f8f6f4 v[204:207], v[128:133], v[44:49], v[204:207] cbsz:2 blgp:2
	v_mfma_f32_16x16x128_f8f6f4 v[138:141], v[128:133], v[20:25], v[138:141] cbsz:2 blgp:2
	v_mfma_f32_16x16x128_f8f6f4 v[208:211], v[128:133], v[56:61], v[208:211] cbsz:2 blgp:2
	v_mfma_f32_16x16x128_f8f6f4 v[142:145], v[128:133], v[32:37], v[142:145] cbsz:2 blgp:2
	v_mfma_f32_16x16x128_f8f6f4 v[212:215], v[128:133], v[68:73], v[212:215] cbsz:2 blgp:2
	v_cndmask_b32_e64 v158, v134, v204, s[4:5]
	v_fma_mix_f32 v158, v158, v1, v85 op_sel:[0,0,1] op_sel_hi:[0,0,1]
	v_exp_f32_e32 v158, v158
	v_cndmask_b32_e64 v159, v138, v208, s[4:5]
	v_fma_mix_f32 v159, v159, v99, v77 op_sel:[0,0,1] op_sel_hi:[0,0,1]
	v_exp_f32_e32 v159, v159
	v_fma_f32 v158, v158, v186, v186
	v_rcp_f32_e32 v158, v158
	v_add_f32_e32 v159, 1.0, v159
	v_rcp_f32_e32 v159, v159
	v_cndmask_b32_e64 v160, v142, v212, s[4:5]
	v_fma_mix_f32 v161, v158, v160, v81 op_sel:[0,0,1] op_sel_hi:[0,0,1]
	v_exp_f32_e32 v161, v161
	s_add_u32 s48, s48, s40
	v_add_f32_e32 v161, 1.0, v161
	v_rcp_f32_e32 v161, v161
	s_addc_u32 s49, s49, s41
	v_fma_f32 v162, v161, -2.0, 1.0
	v_sub_f32_e32 v163, v176, v162
	v_fma_f32 v176, v159, v163, v162
	v_fma_f32 v164, |v176|, s16, v117
	v_fma_f32 v165, |v176|, s17, v118
	v_fma_f32 v166, |v176|, s18, v119
	v_lshrrev_b32_e32 v167, 26, v176
	v_min3_u32 v164, v164, v165, v166
	v_bfi_b32 v168, 31, v164, v167
	global_store_short_d16_hi v185, v176, s[48:49]
	s_nop 0
	v_mul_u32_u24_dpp v170, v168, v180 quad_perm:[1,2,3,3] row_mask:0xf bank_mask:0xf bound_ctrl:1
	v_mad_u32_u24 v171, v168, v181, v170
	ds_write_b8_d16_hi v184, v171
	s_barrier
	s_waitcnt lgkmcnt(0)
	s_barrier
	ds_read_b64 v[122:123], v106 offset:0
	ds_read_b64 v[124:125], v106 offset:8
	ds_read_b64 v[126:127], v106 offset:16
	ds_read_b64 v[128:129], v106 offset:96
	ds_read_b64 v[130:131], v106 offset:104
	ds_read_b64 v[132:133], v106 offset:112
	s_waitcnt vmcnt(8)
	global_load_dwordx4 v[82:85], v[196:197], off
	global_load_dwordx4 v[74:77], v[196:197], off offset:512
	global_load_dwordx4 v[78:81], v[196:197], off offset:1024
	v_lshl_add_u64 v[196:197], v[196:197], 0, s[42:43]
	s_waitcnt lgkmcnt(3)
	v_mfma_f32_16x16x128_f8f6f4 v[134:137], v[122:127], v[2:7], 0 cbsz:2 blgp:2
	v_mfma_f32_16x16x128_f8f6f4 v[138:141], v[122:127], v[14:19], 0 cbsz:2 blgp:2
	v_mfma_f32_16x16x128_f8f6f4 v[142:145], v[122:127], v[26:31], v[188:191] cbsz:2 blgp:2
	v_mfma_f32_16x16x128_f8f6f4 v[204:207], v[122:127], v[38:43], 0 cbsz:2 blgp:2
	v_mfma_f32_16x16x128_f8f6f4 v[208:211], v[122:127], v[50:55], 0 cbsz:2 blgp:2
	v_mfma_f32_16x16x128_f8f6f4 v[212:215], v[122:127], v[62:67], v[188:191] cbsz:2 blgp:2
	s_waitcnt lgkmcnt(0)
	v_mfma_f32_16x16x128_f8f6f4 v[134:137], v[128:133], v[8:13], v[134:137] cbsz:2 blgp:2
	v_mfma_f32_16x16x128_f8f6f4 v[204:207], v[128:133], v[44:49], v[204:207] cbsz:2 blgp:2
	v_mfma_f32_16x16x128_f8f6f4 v[138:141], v[128:133], v[20:25], v[138:141] cbsz:2 blgp:2
	v_mfma_f32_16x16x128_f8f6f4 v[208:211], v[128:133], v[56:61], v[208:211] cbsz:2 blgp:2
	v_mfma_f32_16x16x128_f8f6f4 v[142:145], v[128:133], v[32:37], v[142:145] cbsz:2 blgp:2
	v_mfma_f32_16x16x128_f8f6f4 v[212:215], v[128:133], v[68:73], v[212:215] cbsz:2 blgp:2
	v_cndmask_b32_e64 v158, v134, v204, s[4:5]
	v_fma_mix_f32 v158, v158, v1, v146 op_sel_hi:[0,0,1]
	v_exp_f32_e32 v158, v158
	v_cndmask_b32_e64 v159, v138, v208, s[4:5]
	v_fma_mix_f32 v159, v159, v99, v150 op_sel_hi:[0,0,1]
	v_exp_f32_e32 v159, v159
	v_fma_f32 v158, v158, v186, v186
	v_rcp_f32_e32 v158, v158
	v_add_f32_e32 v159, 1.0, v159
	v_rcp_f32_e32 v159, v159
	v_cndmask_b32_e64 v160, v142, v212, s[4:5]
	v_fma_mix_f32 v161, v158, v160, v154 op_sel_hi:[0,0,1]
	v_exp_f32_e32 v161, v161
	s_add_u32 s48, s48, s40
	v_add_f32_e32 v161, 1.0, v161
	v_rcp_f32_e32 v161, v161
	s_addc_u32 s49, s49, s41
	v_fma_f32 v162, v161, -2.0, 1.0
	v_sub_f32_e32 v163, v176, v162
	v_fma_f32 v176, v159, v163, v162
	v_fma_f32 v164, |v176|, s16, v117
	v_fma_f32 v165, |v176|, s17, v118
	v_fma_f32 v166, |v176|, s18, v119
	v_lshrrev_b32_e32 v167, 26, v176
	v_min3_u32 v164, v164, v165, v166
	v_bfi_b32 v168, 31, v164, v167
	global_store_short_d16_hi v185, v176, s[48:49]
	s_nop 0
	v_mul_u32_u24_dpp v170, v168, v180 quad_perm:[1,2,3,3] row_mask:0xf bank_mask:0xf bound_ctrl:1
	v_mad_u32_u24 v171, v168, v181, v170
	ds_write_b8_d16_hi v184, v171 offset:416
	s_barrier
	s_waitcnt lgkmcnt(0)
	s_barrier
	ds_read_b64 v[122:123], v106 offset:416
	ds_read_b64 v[124:125], v106 offset:424
	ds_read_b64 v[126:127], v106 offset:432
	ds_read_b64 v[128:129], v106 offset:512
	ds_read_b64 v[130:131], v106 offset:520
	ds_read_b64 v[132:133], v106 offset:528
	s_waitcnt lgkmcnt(3)
	v_mfma_f32_16x16x128_f8f6f4 v[134:137], v[122:127], v[2:7], 0 cbsz:2 blgp:2
	v_mfma_f32_16x16x128_f8f6f4 v[138:141], v[122:127], v[14:19], 0 cbsz:2 blgp:2
	v_mfma_f32_16x16x128_f8f6f4 v[142:145], v[122:127], v[26:31], v[188:191] cbsz:2 blgp:2
	v_mfma_f32_16x16x128_f8f6f4 v[204:207], v[122:127], v[38:43], 0 cbsz:2 blgp:2
	v_mfma_f32_16x16x128_f8f6f4 v[208:211], v[122:127], v[50:55], 0 cbsz:2 blgp:2
	v_mfma_f32_16x16x128_f8f6f4 v[212:215], v[122:127], v[62:67], v[188:191] cbsz:2 blgp:2
	s_waitcnt lgkmcnt(0)
	v_mfma_f32_16x16x128_f8f6f4 v[134:137], v[128:133], v[8:13], v[134:137] cbsz:2 blgp:2
	v_mfma_f32_16x16x128_f8f6f4 v[204:207], v[128:133], v[44:49], v[204:207] cbsz:2 blgp:2
	v_mfma_f32_16x16x128_f8f6f4 v[138:141], v[128:133], v[20:25], v[138:141] cbsz:2 blgp:2
	v_mfma_f32_16x16x128_f8f6f4 v[208:211], v[128:133], v[56:61], v[208:211] cbsz:2 blgp:2
	v_mfma_f32_16x16x128_f8f6f4 v[142:145], v[128:133], v[32:37], v[142:145] cbsz:2 blgp:2
	v_mfma_f32_16x16x128_f8f6f4 v[212:215], v[128:133], v[68:73], v[212:215] cbsz:2 blgp:2
	v_cndmask_b32_e64 v158, v134, v204, s[4:5]
	v_fma_mix_f32 v158, v158, v1, v146 op_sel:[0,0,1] op_sel_hi:[0,0,1]
	v_exp_f32_e32 v158, v158
	v_cndmask_b32_e64 v159, v138, v208, s[4:5]
	v_fma_mix_f32 v159, v159, v99, v150 op_sel:[0,0,1] op_sel_hi:[0,0,1]
	v_exp_f32_e32 v159, v159
	v_fma_f32 v158, v158, v186, v186
	v_rcp_f32_e32 v158, v158
	v_add_f32_e32 v159, 1.0, v159
	v_rcp_f32_e32 v159, v159
	v_cndmask_b32_e64 v160, v142, v212, s[4:5]
	v_fma_mix_f32 v161, v158, v160, v154 op_sel:[0,0,1] op_sel_hi:[0,0,1]
	v_exp_f32_e32 v161, v161
	s_add_u32 s48, s48, s40
	v_add_f32_e32 v161, 1.0, v161
	v_rcp_f32_e32 v161, v161
	s_addc_u32 s49, s49, s41
	v_fma_f32 v162, v161, -2.0, 1.0
	v_sub_f32_e32 v163, v176, v162
	v_fma_f32 v176, v159, v163, v162
	v_fma_f32 v164, |v176|, s16, v117
	v_fma_f32 v165, |v176|, s17, v118
	v_fma_f32 v166, |v176|, s18, v119
	v_lshrrev_b32_e32 v167, 26, v176
	v_min3_u32 v164, v164, v165, v166
	v_bfi_b32 v168, 31, v164, v167
	global_store_short_d16_hi v185, v176, s[48:49]
	s_nop 0
	v_mul_u32_u24_dpp v170, v168, v180 quad_perm:[1,2,3,3] row_mask:0xf bank_mask:0xf bound_ctrl:1
	v_mad_u32_u24 v171, v168, v181, v170
	ds_write_b8_d16_hi v184, v171
	s_barrier
	s_waitcnt lgkmcnt(0)
	s_barrier
	ds_read_b64 v[122:123], v106 offset:0
	ds_read_b64 v[124:125], v106 offset:8
	ds_read_b64 v[126:127], v106 offset:16
	ds_read_b64 v[128:129], v106 offset:96
	ds_read_b64 v[130:131], v106 offset:104
	ds_read_b64 v[132:133], v106 offset:112
	s_waitcnt lgkmcnt(3)
	v_mfma_f32_16x16x128_f8f6f4 v[134:137], v[122:127], v[2:7], 0 cbsz:2 blgp:2
	v_mfma_f32_16x16x128_f8f6f4 v[138:141], v[122:127], v[14:19], 0 cbsz:2 blgp:2
	v_mfma_f32_16x16x128_f8f6f4 v[142:145], v[122:127], v[26:31], v[188:191] cbsz:2 blgp:2
	v_mfma_f32_16x16x128_f8f6f4 v[204:207], v[122:127], v[38:43], 0 cbsz:2 blgp:2
	v_mfma_f32_16x16x128_f8f6f4 v[208:211], v[122:127], v[50:55], 0 cbsz:2 blgp:2
	v_mfma_f32_16x16x128_f8f6f4 v[212:215], v[122:127], v[62:67], v[188:191] cbsz:2 blgp:2
	s_waitcnt lgkmcnt(0)
	v_mfma_f32_16x16x128_f8f6f4 v[134:137], v[128:133], v[8:13], v[134:137] cbsz:2 blgp:2
	v_mfma_f32_16x16x128_f8f6f4 v[204:207], v[128:133], v[44:49], v[204:207] cbsz:2 blgp:2
	v_mfma_f32_16x16x128_f8f6f4 v[138:141], v[128:133], v[20:25], v[138:141] cbsz:2 blgp:2
	v_mfma_f32_16x16x128_f8f6f4 v[208:211], v[128:133], v[56:61], v[208:211] cbsz:2 blgp:2
	v_mfma_f32_16x16x128_f8f6f4 v[142:145], v[128:133], v[32:37], v[142:145] cbsz:2 blgp:2
	v_mfma_f32_16x16x128_f8f6f4 v[212:215], v[128:133], v[68:73], v[212:215] cbsz:2 blgp:2
	v_cndmask_b32_e64 v158, v134, v204, s[4:5]
	v_fma_mix_f32 v158, v158, v1, v147 op_sel_hi:[0,0,1]
	v_exp_f32_e32 v158, v158
	v_cndmask_b32_e64 v159, v138, v208, s[4:5]
	v_fma_mix_f32 v159, v159, v99, v151 op_sel_hi:[0,0,1]
	v_exp_f32_e32 v159, v159
	v_fma_f32 v158, v158, v186, v186
	v_rcp_f32_e32 v158, v158
	v_add_f32_e32 v159, 1.0, v159
	v_rcp_f32_e32 v159, v159
	v_cndmask_b32_e64 v160, v142, v212, s[4:5]
	v_fma_mix_f32 v161, v158, v160, v155 op_sel_hi:[0,0,1]
	v_exp_f32_e32 v161, v161
	s_add_u32 s48, s48, s40
	v_add_f32_e32 v161, 1.0, v161
	v_rcp_f32_e32 v161, v161
	s_addc_u32 s49, s49, s41
	v_fma_f32 v162, v161, -2.0, 1.0
	v_sub_f32_e32 v163, v176, v162
	v_fma_f32 v176, v159, v163, v162
	v_fma_f32 v164, |v176|, s16, v117
	v_fma_f32 v165, |v176|, s17, v118
	v_fma_f32 v166, |v176|, s18, v119
	v_lshrrev_b32_e32 v167, 26, v176
	v_min3_u32 v164, v164, v165, v166
	v_bfi_b32 v168, 31, v164, v167
	global_store_short_d16_hi v185, v176, s[48:49]
	s_nop 0
	v_mul_u32_u24_dpp v170, v168, v180 quad_perm:[1,2,3,3] row_mask:0xf bank_mask:0xf bound_ctrl:1
	v_mad_u32_u24 v171, v168, v181, v170
	ds_write_b8_d16_hi v184, v171 offset:416
	s_barrier
	s_waitcnt lgkmcnt(0)
	s_barrier
	ds_read_b64 v[122:123], v106 offset:416
	ds_read_b64 v[124:125], v106 offset:424
	ds_read_b64 v[126:127], v106 offset:432
	ds_read_b64 v[128:129], v106 offset:512
	ds_read_b64 v[130:131], v106 offset:520
	ds_read_b64 v[132:133], v106 offset:528
	s_waitcnt lgkmcnt(3)
	v_mfma_f32_16x16x128_f8f6f4 v[134:137], v[122:127], v[2:7], 0 cbsz:2 blgp:2
	v_mfma_f32_16x16x128_f8f6f4 v[138:141], v[122:127], v[14:19], 0 cbsz:2 blgp:2
	v_mfma_f32_16x16x128_f8f6f4 v[142:145], v[122:127], v[26:31], v[188:191] cbsz:2 blgp:2
	v_mfma_f32_16x16x128_f8f6f4 v[204:207], v[122:127], v[38:43], 0 cbsz:2 blgp:2
	v_mfma_f32_16x16x128_f8f6f4 v[208:211], v[122:127], v[50:55], 0 cbsz:2 blgp:2
	v_mfma_f32_16x16x128_f8f6f4 v[212:215], v[122:127], v[62:67], v[188:191] cbsz:2 blgp:2
	s_waitcnt lgkmcnt(0)
	v_mfma_f32_16x16x128_f8f6f4 v[134:137], v[128:133], v[8:13], v[134:137] cbsz:2 blgp:2
	v_mfma_f32_16x16x128_f8f6f4 v[204:207], v[128:133], v[44:49], v[204:207] cbsz:2 blgp:2
	v_mfma_f32_16x16x128_f8f6f4 v[138:141], v[128:133], v[20:25], v[138:141] cbsz:2 blgp:2
	v_mfma_f32_16x16x128_f8f6f4 v[208:211], v[128:133], v[56:61], v[208:211] cbsz:2 blgp:2
	v_mfma_f32_16x16x128_f8f6f4 v[142:145], v[128:133], v[32:37], v[142:145] cbsz:2 blgp:2
	v_mfma_f32_16x16x128_f8f6f4 v[212:215], v[128:133], v[68:73], v[212:215] cbsz:2 blgp:2
	v_cndmask_b32_e64 v158, v134, v204, s[4:5]
	v_fma_mix_f32 v158, v158, v1, v147 op_sel:[0,0,1] op_sel_hi:[0,0,1]
	v_exp_f32_e32 v158, v158
	v_cndmask_b32_e64 v159, v138, v208, s[4:5]
	v_fma_mix_f32 v159, v159, v99, v151 op_sel:[0,0,1] op_sel_hi:[0,0,1]
	v_exp_f32_e32 v159, v159
	v_fma_f32 v158, v158, v186, v186
	v_rcp_f32_e32 v158, v158
	v_add_f32_e32 v159, 1.0, v159
	v_rcp_f32_e32 v159, v159
	v_cndmask_b32_e64 v160, v142, v212, s[4:5]
	v_fma_mix_f32 v161, v158, v160, v155 op_sel:[0,0,1] op_sel_hi:[0,0,1]
	v_exp_f32_e32 v161, v161
	s_add_u32 s48, s48, s40
	v_add_f32_e32 v161, 1.0, v161
	v_rcp_f32_e32 v161, v161
	s_addc_u32 s49, s49, s41
	v_fma_f32 v162, v161, -2.0, 1.0
	v_sub_f32_e32 v163, v176, v162
	v_fma_f32 v176, v159, v163, v162
	v_fma_f32 v164, |v176|, s16, v117
	v_fma_f32 v165, |v176|, s17, v118
	v_fma_f32 v166, |v176|, s18, v119
	v_lshrrev_b32_e32 v167, 26, v176
	v_min3_u32 v164, v164, v165, v166
	v_bfi_b32 v168, 31, v164, v167
	global_store_short_d16_hi v185, v176, s[48:49]
	s_nop 0
	v_mul_u32_u24_dpp v170, v168, v180 quad_perm:[1,2,3,3] row_mask:0xf bank_mask:0xf bound_ctrl:1
	v_mad_u32_u24 v171, v168, v181, v170
	ds_write_b8_d16_hi v184, v171
	s_barrier
	s_waitcnt lgkmcnt(0)
	s_barrier
	ds_read_b64 v[122:123], v106 offset:0
	ds_read_b64 v[124:125], v106 offset:8
	ds_read_b64 v[126:127], v106 offset:16
	ds_read_b64 v[128:129], v106 offset:96
	ds_read_b64 v[130:131], v106 offset:104
	ds_read_b64 v[132:133], v106 offset:112
	s_waitcnt lgkmcnt(3)
	v_mfma_f32_16x16x128_f8f6f4 v[134:137], v[122:127], v[2:7], 0 cbsz:2 blgp:2
	v_mfma_f32_16x16x128_f8f6f4 v[138:141], v[122:127], v[14:19], 0 cbsz:2 blgp:2
	v_mfma_f32_16x16x128_f8f6f4 v[142:145], v[122:127], v[26:31], v[188:191] cbsz:2 blgp:2
	v_mfma_f32_16x16x128_f8f6f4 v[204:207], v[122:127], v[38:43], 0 cbsz:2 blgp:2
	v_mfma_f32_16x16x128_f8f6f4 v[208:211], v[122:127], v[50:55], 0 cbsz:2 blgp:2
	v_mfma_f32_16x16x128_f8f6f4 v[212:215], v[122:127], v[62:67], v[188:191] cbsz:2 blgp:2
	s_waitcnt lgkmcnt(0)
	v_mfma_f32_16x16x128_f8f6f4 v[134:137], v[128:133], v[8:13], v[134:137] cbsz:2 blgp:2
	v_mfma_f32_16x16x128_f8f6f4 v[204:207], v[128:133], v[44:49], v[204:207] cbsz:2 blgp:2
	v_mfma_f32_16x16x128_f8f6f4 v[138:141], v[128:133], v[20:25], v[138:141] cbsz:2 blgp:2
	v_mfma_f32_16x16x128_f8f6f4 v[208:211], v[128:133], v[56:61], v[208:211] cbsz:2 blgp:2
	v_mfma_f32_16x16x128_f8f6f4 v[142:145], v[128:133], v[32:37], v[142:145] cbsz:2 blgp:2
	v_mfma_f32_16x16x128_f8f6f4 v[212:215], v[128:133], v[68:73], v[212:215] cbsz:2 blgp:2
	v_cndmask_b32_e64 v158, v134, v204, s[4:5]
	v_fma_mix_f32 v158, v158, v1, v148 op_sel_hi:[0,0,1]
	v_exp_f32_e32 v158, v158
	v_cndmask_b32_e64 v159, v138, v208, s[4:5]
	v_fma_mix_f32 v159, v159, v99, v152 op_sel_hi:[0,0,1]
	v_exp_f32_e32 v159, v159
	v_fma_f32 v158, v158, v186, v186
	v_rcp_f32_e32 v158, v158
	v_add_f32_e32 v159, 1.0, v159
	v_rcp_f32_e32 v159, v159
	v_cndmask_b32_e64 v160, v142, v212, s[4:5]
	v_fma_mix_f32 v161, v158, v160, v156 op_sel_hi:[0,0,1]
	v_exp_f32_e32 v161, v161
	s_add_u32 s48, s48, s40
	v_add_f32_e32 v161, 1.0, v161
	v_rcp_f32_e32 v161, v161
	s_addc_u32 s49, s49, s41
	v_fma_f32 v162, v161, -2.0, 1.0
	v_sub_f32_e32 v163, v176, v162
	v_fma_f32 v176, v159, v163, v162
	v_fma_f32 v164, |v176|, s16, v117
	v_fma_f32 v165, |v176|, s17, v118
	v_fma_f32 v166, |v176|, s18, v119
	v_lshrrev_b32_e32 v167, 26, v176
	v_min3_u32 v164, v164, v165, v166
	v_bfi_b32 v168, 31, v164, v167
	global_store_short_d16_hi v185, v176, s[48:49]
	s_nop 0
	v_mul_u32_u24_dpp v170, v168, v180 quad_perm:[1,2,3,3] row_mask:0xf bank_mask:0xf bound_ctrl:1
	v_mad_u32_u24 v171, v168, v181, v170
	ds_write_b8_d16_hi v184, v171 offset:416
	s_barrier
	s_waitcnt lgkmcnt(0)
	s_barrier
	ds_read_b64 v[122:123], v106 offset:416
	ds_read_b64 v[124:125], v106 offset:424
	ds_read_b64 v[126:127], v106 offset:432
	ds_read_b64 v[128:129], v106 offset:512
	ds_read_b64 v[130:131], v106 offset:520
	ds_read_b64 v[132:133], v106 offset:528
	s_waitcnt lgkmcnt(3)
	v_mfma_f32_16x16x128_f8f6f4 v[134:137], v[122:127], v[2:7], 0 cbsz:2 blgp:2
	v_mfma_f32_16x16x128_f8f6f4 v[138:141], v[122:127], v[14:19], 0 cbsz:2 blgp:2
	v_mfma_f32_16x16x128_f8f6f4 v[142:145], v[122:127], v[26:31], v[188:191] cbsz:2 blgp:2
	v_mfma_f32_16x16x128_f8f6f4 v[204:207], v[122:127], v[38:43], 0 cbsz:2 blgp:2
	v_mfma_f32_16x16x128_f8f6f4 v[208:211], v[122:127], v[50:55], 0 cbsz:2 blgp:2
	v_mfma_f32_16x16x128_f8f6f4 v[212:215], v[122:127], v[62:67], v[188:191] cbsz:2 blgp:2
	s_waitcnt lgkmcnt(0)
	v_mfma_f32_16x16x128_f8f6f4 v[134:137], v[128:133], v[8:13], v[134:137] cbsz:2 blgp:2
	v_mfma_f32_16x16x128_f8f6f4 v[204:207], v[128:133], v[44:49], v[204:207] cbsz:2 blgp:2
	v_mfma_f32_16x16x128_f8f6f4 v[138:141], v[128:133], v[20:25], v[138:141] cbsz:2 blgp:2
	v_mfma_f32_16x16x128_f8f6f4 v[208:211], v[128:133], v[56:61], v[208:211] cbsz:2 blgp:2
	v_mfma_f32_16x16x128_f8f6f4 v[142:145], v[128:133], v[32:37], v[142:145] cbsz:2 blgp:2
	v_mfma_f32_16x16x128_f8f6f4 v[212:215], v[128:133], v[68:73], v[212:215] cbsz:2 blgp:2
	v_cndmask_b32_e64 v158, v134, v204, s[4:5]
	v_fma_mix_f32 v158, v158, v1, v148 op_sel:[0,0,1] op_sel_hi:[0,0,1]
	v_exp_f32_e32 v158, v158
	v_cndmask_b32_e64 v159, v138, v208, s[4:5]
	v_fma_mix_f32 v159, v159, v99, v152 op_sel:[0,0,1] op_sel_hi:[0,0,1]
	v_exp_f32_e32 v159, v159
	v_fma_f32 v158, v158, v186, v186
	v_rcp_f32_e32 v158, v158
	v_add_f32_e32 v159, 1.0, v159
	v_rcp_f32_e32 v159, v159
	v_cndmask_b32_e64 v160, v142, v212, s[4:5]
	v_fma_mix_f32 v161, v158, v160, v156 op_sel:[0,0,1] op_sel_hi:[0,0,1]
	v_exp_f32_e32 v161, v161
	s_add_u32 s48, s48, s40
	v_add_f32_e32 v161, 1.0, v161
	v_rcp_f32_e32 v161, v161
	s_addc_u32 s49, s49, s41
	v_fma_f32 v162, v161, -2.0, 1.0
	v_sub_f32_e32 v163, v176, v162
	v_fma_f32 v176, v159, v163, v162
	v_fma_f32 v164, |v176|, s16, v117
	v_fma_f32 v165, |v176|, s17, v118
	v_fma_f32 v166, |v176|, s18, v119
	v_lshrrev_b32_e32 v167, 26, v176
	v_min3_u32 v164, v164, v165, v166
	v_bfi_b32 v168, 31, v164, v167
	global_store_short_d16_hi v185, v176, s[48:49]
	s_nop 0
	v_mul_u32_u24_dpp v170, v168, v180 quad_perm:[1,2,3,3] row_mask:0xf bank_mask:0xf bound_ctrl:1
	v_mad_u32_u24 v171, v168, v181, v170
	ds_write_b8_d16_hi v184, v171
	s_barrier
	s_waitcnt lgkmcnt(0)
	s_barrier
	ds_read_b64 v[122:123], v106 offset:0
	ds_read_b64 v[124:125], v106 offset:8
	ds_read_b64 v[126:127], v106 offset:16
	ds_read_b64 v[128:129], v106 offset:96
	ds_read_b64 v[130:131], v106 offset:104
	ds_read_b64 v[132:133], v106 offset:112
	s_waitcnt lgkmcnt(3)
	v_mfma_f32_16x16x128_f8f6f4 v[134:137], v[122:127], v[2:7], 0 cbsz:2 blgp:2
	v_mfma_f32_16x16x128_f8f6f4 v[138:141], v[122:127], v[14:19], 0 cbsz:2 blgp:2
	v_mfma_f32_16x16x128_f8f6f4 v[142:145], v[122:127], v[26:31], v[188:191] cbsz:2 blgp:2
	v_mfma_f32_16x16x128_f8f6f4 v[204:207], v[122:127], v[38:43], 0 cbsz:2 blgp:2
	v_mfma_f32_16x16x128_f8f6f4 v[208:211], v[122:127], v[50:55], 0 cbsz:2 blgp:2
	v_mfma_f32_16x16x128_f8f6f4 v[212:215], v[122:127], v[62:67], v[188:191] cbsz:2 blgp:2
	s_waitcnt lgkmcnt(0)
	v_mfma_f32_16x16x128_f8f6f4 v[134:137], v[128:133], v[8:13], v[134:137] cbsz:2 blgp:2
	v_mfma_f32_16x16x128_f8f6f4 v[204:207], v[128:133], v[44:49], v[204:207] cbsz:2 blgp:2
	v_mfma_f32_16x16x128_f8f6f4 v[138:141], v[128:133], v[20:25], v[138:141] cbsz:2 blgp:2
	v_mfma_f32_16x16x128_f8f6f4 v[208:211], v[128:133], v[56:61], v[208:211] cbsz:2 blgp:2
	v_mfma_f32_16x16x128_f8f6f4 v[142:145], v[128:133], v[32:37], v[142:145] cbsz:2 blgp:2
	v_mfma_f32_16x16x128_f8f6f4 v[212:215], v[128:133], v[68:73], v[212:215] cbsz:2 blgp:2
	v_cndmask_b32_e64 v158, v134, v204, s[4:5]
	v_fma_mix_f32 v158, v158, v1, v149 op_sel_hi:[0,0,1]
	v_exp_f32_e32 v158, v158
	v_cndmask_b32_e64 v159, v138, v208, s[4:5]
	v_fma_mix_f32 v159, v159, v99, v153 op_sel_hi:[0,0,1]
	v_exp_f32_e32 v159, v159
	v_fma_f32 v158, v158, v186, v186
	v_rcp_f32_e32 v158, v158
	v_add_f32_e32 v159, 1.0, v159
	v_rcp_f32_e32 v159, v159
	v_cndmask_b32_e64 v160, v142, v212, s[4:5]
	v_fma_mix_f32 v161, v158, v160, v157 op_sel_hi:[0,0,1]
	v_exp_f32_e32 v161, v161
	s_add_u32 s48, s48, s40
	v_add_f32_e32 v161, 1.0, v161
	v_rcp_f32_e32 v161, v161
	s_addc_u32 s49, s49, s41
	v_fma_f32 v162, v161, -2.0, 1.0
	v_sub_f32_e32 v163, v176, v162
	v_fma_f32 v176, v159, v163, v162
	v_fma_f32 v164, |v176|, s16, v117
	v_fma_f32 v165, |v176|, s17, v118
	v_fma_f32 v166, |v176|, s18, v119
	v_lshrrev_b32_e32 v167, 26, v176
	v_min3_u32 v164, v164, v165, v166
	v_bfi_b32 v168, 31, v164, v167
	global_store_short_d16_hi v185, v176, s[48:49]
	s_nop 0
	v_mul_u32_u24_dpp v170, v168, v180 quad_perm:[1,2,3,3] row_mask:0xf bank_mask:0xf bound_ctrl:1
	v_mad_u32_u24 v171, v168, v181, v170
	ds_write_b8_d16_hi v184, v171 offset:416
	s_barrier
	s_waitcnt lgkmcnt(0)
	s_barrier
	ds_read_b64 v[122:123], v106 offset:416
	ds_read_b64 v[124:125], v106 offset:424
	ds_read_b64 v[126:127], v106 offset:432
	ds_read_b64 v[128:129], v106 offset:512
	ds_read_b64 v[130:131], v106 offset:520
	ds_read_b64 v[132:133], v106 offset:528
	s_add_i32 s44, s44, 16
	s_waitcnt lgkmcnt(3)
	v_mfma_f32_16x16x128_f8f6f4 v[134:137], v[122:127], v[2:7], 0 cbsz:2 blgp:2
	v_mfma_f32_16x16x128_f8f6f4 v[138:141], v[122:127], v[14:19], 0 cbsz:2 blgp:2
	v_mfma_f32_16x16x128_f8f6f4 v[142:145], v[122:127], v[26:31], v[188:191] cbsz:2 blgp:2
	v_mfma_f32_16x16x128_f8f6f4 v[204:207], v[122:127], v[38:43], 0 cbsz:2 blgp:2
	v_mfma_f32_16x16x128_f8f6f4 v[208:211], v[122:127], v[50:55], 0 cbsz:2 blgp:2
	v_mfma_f32_16x16x128_f8f6f4 v[212:215], v[122:127], v[62:67], v[188:191] cbsz:2 blgp:2
	s_waitcnt lgkmcnt(0)
	v_mfma_f32_16x16x128_f8f6f4 v[134:137], v[128:133], v[8:13], v[134:137] cbsz:2 blgp:2
	v_mfma_f32_16x16x128_f8f6f4 v[204:207], v[128:133], v[44:49], v[204:207] cbsz:2 blgp:2
	v_mfma_f32_16x16x128_f8f6f4 v[138:141], v[128:133], v[20:25], v[138:141] cbsz:2 blgp:2
	v_mfma_f32_16x16x128_f8f6f4 v[208:211], v[128:133], v[56:61], v[208:211] cbsz:2 blgp:2
	v_mfma_f32_16x16x128_f8f6f4 v[142:145], v[128:133], v[32:37], v[142:145] cbsz:2 blgp:2
	v_mfma_f32_16x16x128_f8f6f4 v[212:215], v[128:133], v[68:73], v[212:215] cbsz:2 blgp:2
	v_cndmask_b32_e64 v158, v134, v204, s[4:5]
	v_fma_mix_f32 v158, v158, v1, v149 op_sel:[0,0,1] op_sel_hi:[0,0,1]
	v_exp_f32_e32 v158, v158
	v_cndmask_b32_e64 v159, v138, v208, s[4:5]
	v_fma_mix_f32 v159, v159, v99, v153 op_sel:[0,0,1] op_sel_hi:[0,0,1]
	v_exp_f32_e32 v159, v159
	v_fma_f32 v158, v158, v186, v186
	v_rcp_f32_e32 v158, v158
	v_add_f32_e32 v159, 1.0, v159
	v_rcp_f32_e32 v159, v159
	v_cndmask_b32_e64 v160, v142, v212, s[4:5]
	v_fma_mix_f32 v161, v158, v160, v157 op_sel:[0,0,1] op_sel_hi:[0,0,1]
	v_exp_f32_e32 v161, v161
	s_add_u32 s48, s48, s40
	v_add_f32_e32 v161, 1.0, v161
	v_rcp_f32_e32 v161, v161
	s_addc_u32 s49, s49, s41
	v_fma_f32 v162, v161, -2.0, 1.0
	v_sub_f32_e32 v163, v176, v162
	v_fma_f32 v176, v159, v163, v162
	v_fma_f32 v164, |v176|, s16, v117
	v_fma_f32 v165, |v176|, s17, v118
	v_fma_f32 v166, |v176|, s18, v119
	v_lshrrev_b32_e32 v167, 26, v176
	v_min3_u32 v164, v164, v165, v166
	v_bfi_b32 v168, 31, v164, v167
	global_store_short_d16_hi v185, v176, s[48:49]
	s_nop 0
	v_mul_u32_u24_dpp v170, v168, v180 quad_perm:[1,2,3,3] row_mask:0xf bank_mask:0xf bound_ctrl:1
	v_mad_u32_u24 v171, v168, v181, v170
	ds_write_b8_d16_hi v184, v171
	s_barrier
	s_cmp_lt_i32 s44, s45
	s_waitcnt lgkmcnt(0)
	s_barrier
	s_cbranch_scc1 .Lscan_loop_b_st

.LBB2_12:
	s_or_b64 exec, exec, s[0:1]
	v_and_b32_e32 v97, 1, v74
	v_mov_b32_e32 v74, s8
	v_mov_b32_e32 v75, s9
	v_lshl_or_b32 v76, s2, 9, v0
	v_mov_b32_e32 v77, v87
	v_lshl_add_u64 v[74:75], v[76:77], 2, v[74:75]
	s_waitcnt lgkmcnt(0)
	s_barrier
	global_load_dword v118, v[74:75], off
	v_and_b32_e32 v74, 4, v90
	v_mov_b32_e32 v75, 0xd0
	v_cmp_ne_u32_e32 vcc, 0, v74
	v_and_b32_e32 v110, 3, v0
	v_cmp_gt_u32_e64 s[0:1], 12, v90
	v_cndmask_b32_e32 v74, 0, v75, vcc
	v_cmp_eq_u32_e32 vcc, 0, v110
	s_and_b64 s[4:5], vcc, s[0:1]
	s_lshl_b32 s1, s2, 21
	v_add_u32_e32 v109, v74, v86
	s_mul_i32 s0, s2, 0x600000
	v_lshl_or_b32 v74, v89, 1, v88
	s_and_b32 s2, s1, 0x1e00000
	v_mul_u32_u24_e32 v74, 0x60, v74
	v_lshlrev_b32_e32 v75, 1, v90
	s_add_u32 s0, s14, s0
	s_addc_u32 s1, s15, 0
	v_or3_b32 v86, v74, v75, v97
	v_lshl_add_u64 v[98:99], v[86:87], 4, s[0:1]
	s_mov_b64 s[0:1], 0x5a0000
	v_lshl_add_u64 v[100:101], v[98:99], 0, s[0:1]
	s_mov_b32 s0, 0x5a0000
	v_add_co_u32_e32 v102, vcc, s0, v98
	s_waitcnt vmcnt(4)
	v_mul_f32_e32 v86, 0xbfb8aa3b, v95
	v_addc_co_u32_e32 v103, vcc, 0, v99, vcc
	global_load_dwordx4 v[82:85], v[102:103], off
	global_load_dwordx4 v[74:77], v[100:101], off offset:512
	global_load_dwordx4 v[78:81], v[100:101], off offset:1024
	v_mul_f32_e32 v100, 0x3c91a2b4, v86
	s_waitcnt vmcnt(6)
	v_mul_f32_e32 v86, 0xbfb8aa3b, v94
	v_mul_f32_e32 v101, 0x3c91a2b4, v86
	s_waitcnt vmcnt(5)
	v_mul_f32_e32 v86, 0x4038aa3b, v93
	v_and_b32_e32 v0, 12, v0
	v_mul_f32_e32 v102, 0x3c91a2b4, v86
	v_lshrrev_b32_e32 v86, 2, v90
	v_mul_u32_u24_e32 v90, 0xd0, v97
	v_mad_u32_u24 v0, v89, 24, v0
	v_mul_u32_u24_e32 v88, 12, v88
	v_add3_u32 v93, v0, v90, v88
	v_or_b32_e32 v0, s2, v1
	v_lshlrev_b32_e32 v104, 3, v86
	v_lshlrev_b32_e32 v89, 20, v97
	v_lshl_add_u32 v0, s22, 8, v0
	v_sub_u32_e32 v86, 0, v104
	v_or3_b32 v0, v0, v89, v92
	v_and_b32_e32 v111, 24, v86
	v_lshlrev_b32_e32 v86, 1, v0
	s_mov_b64 s[6:7], 0x5a6000
	v_lshl_add_u64 v[0:1], s[12:13], 0, v[86:87]
	v_lshl_add_u64 v[86:87], v[98:99], 0, s[6:7]
	s_mov_b64 s[6:7], 0x5a6200
	v_lshl_add_u64 v[88:89], v[98:99], 0, s[6:7]
	s_mov_b64 s[6:7], 0x5a6400
	v_cmp_lt_u32_e64 s[0:1], 1, v91
	s_waitcnt vmcnt(4)
	v_mul_f32_e32 v103, 0x4038aa3b, v96
	s_mov_b32 s3, 0
	v_or_b32_e32 v105, 0x1c400, v109
	v_add_u32_e32 v106, 0x1c410, v109
	v_add_u32_e32 v107, 0x1c470, v109
	v_add_u32_e32 v108, 0x1c5b0, v109
	v_add_u32_e32 v109, 0x1c610, v109
	v_mul_u32_u24_e32 v110, 6, v110
	v_lshl_add_u64 v[90:91], v[98:99], 0, s[6:7]
	s_movk_i32 s22, 0x780
	s_movk_i32 s14, 0x7f
	s_movk_i32 s15, 0xf0
	v_mov_b32_e32 v112, 0x7f7f7f7f
	s_mov_b32 s17, 0x42700000
	s_mov_b32 s18, 0x41f00000
	s_mov_b32 s19, 0x41700000
	s_mov_b64 s[6:7], 0x12000
	s_mov_b64 s[8:9], 0x12200
	s_mov_b64 s[10:11], 0x12400
	v_mov_b32_e32 v113, 0x4b400000
	v_mov_b32_e32 v114, 0x4b400008
	v_mov_b32_e32 v115, 0x4b400010
	v_add_u32_e32 v116, 0x1c5a0, v93
	v_add_u32_e32 v117, 0x1c400, v93
	v_mbcnt_lo_u32_b32 v200, -1, 0
	v_mbcnt_hi_u32_b32 v200, -1, v200
	v_and_b32_e32 v201, 3, v200
	v_and_b32_e32 v202, 15, v200
	v_cmp_gt_u32_e32 vcc, 8, v202
	s_nop 1
	v_cndmask_b32_e64 v178, 0, v112, vcc
	v_cndmask_b32_e64 v179, v112, 0, vcc
	v_lshlrev_b32_e32 v181, 1, v201
	v_sub_u32_e32 v202, 22, v181
	v_lshlrev_b32_e64 v180, v202, 1
	v_sub_u32_e32 v202, 16, v181
	v_lshlrev_b32_e64 v181, v202, 1
	v_lshrrev_b32_e32 v202, 3, v104
	v_sub_u32_e32 v184, v117, v202
	v_add_u32_e32 v184, v184, v201
	v_add_u32_e32 v202, 0x1c4c0, v202
	v_cmp_eq_u32_e32 vcc, 3, v201
	s_nop 1
	v_cndmask_b32_e32 v184, v184, v202, vcc
	v_subrev_u32_e32 v185, s12, v0
	s_movk_i32 s44, 0x780
	s_movk_i32 s45, 0x800
	s_lshr_b32 s46, s44, 3
	s_add_i32 s46, s46, 1
	s_mul_i32 s46, s46, 0x6000
	s_mov_b32 s47, 0
	v_lshl_add_u64 v[196:197], v[98:99], 0, s[46:47]
	s_mov_b32 s42, 0x6000
	s_mov_b32 s43, 0
	s_sub_i32 s46, s44, 1
	s_sub_i32 s47, 0x800, s44
	s_and_b64 s[40:41], s[20:21], exec
	s_cselect_b32 s46, s46, s47
	s_cselect_b32 s41, 0, -1
	s_xor_b32 s40, s41, 0x400
	s_sub_i32 s40, s40, s41
	s_ashr_i32 s47, s46, 31
	s_lshl_b64 s[46:47], s[46:47], 10
	s_add_u32 s48, s12, s46
	s_addc_u32 s49, s13, s47
	v_readfirstlane_b32 s51, v117
	s_waitcnt vmcnt(0) lgkmcnt(0)
	v_mov_b32_e32 v176, v118
	v_rcp_f32_e32 v186, v102
	s_nop 1
	v_mul_f32_e32 v188, v103, v186
	v_mov_b32_e32 v189, 0
	v_mov_b32_e32 v190, 0
	v_mov_b32_e32 v191, 0
	s_nop 1
	s_sub_u32 s51, s51, 0x1c400
	s_cmp_lt_i32 s44, s45
	s_cbranch_scc0 .Lscan_exit_f2
	ds_read_b64 v[122:123], v105 offset:0
	ds_read_b64 v[124:125], v105 offset:8
	ds_read_b64 v[126:127], v105 offset:16
	s_waitcnt lgkmcnt(0)
	s_cmp_lt_u32 s51, 96
	s_cbranch_scc0 .Lscan_loop_b_f2
.Lscan_loop_a_f2:
	ds_read_b64 v[128:129], v105 offset:96
	ds_read_b64 v[130:131], v105 offset:104
	ds_read_b64 v[132:133], v105 offset:112
	s_waitcnt vmcnt(8)
	global_load_dwordx4 v[146:149], v[196:197], off
	global_load_dwordx4 v[150:153], v[196:197], off offset:512
	global_load_dwordx4 v[154:157], v[196:197], off offset:1024
	v_lshl_add_u64 v[196:197], v[196:197], 0, s[42:43]
	s_waitcnt lgkmcnt(3)
	v_mfma_f32_16x16x128_f8f6f4 v[134:137], v[122:127], v[2:7], 0 cbsz:2 blgp:2
	v_mfma_f32_16x16x128_f8f6f4 v[138:141], v[122:127], v[14:19], 0 cbsz:2 blgp:2
	v_mfma_f32_16x16x128_f8f6f4 v[142:145], v[122:127], v[26:31], v[188:191] cbsz:2 blgp:2
	v_mfma_f32_16x16x128_f8f6f4 v[204:207], v[122:127], v[38:43], 0 cbsz:2 blgp:2
	v_mfma_f32_16x16x128_f8f6f4 v[208:211], v[122:127], v[50:55], 0 cbsz:2 blgp:2
	v_mfma_f32_16x16x128_f8f6f4 v[212:215], v[122:127], v[62:67], v[188:191] cbsz:2 blgp:2
	s_waitcnt lgkmcnt(0)
	v_mfma_f32_16x16x128_f8f6f4 v[134:137], v[128:133], v[8:13], v[134:137] cbsz:2 blgp:2
	v_mfma_f32_16x16x128_f8f6f4 v[204:207], v[128:133], v[44:49], v[204:207] cbsz:2 blgp:2
	v_mfma_f32_16x16x128_f8f6f4 v[138:141], v[128:133], v[20:25], v[138:141] cbsz:2 blgp:2
	v_mfma_f32_16x16x128_f8f6f4 v[208:211], v[128:133], v[56:61], v[208:211] cbsz:2 blgp:2
	v_mfma_f32_16x16x128_f8f6f4 v[142:145], v[128:133], v[32:37], v[142:145] cbsz:2 blgp:2
	v_mfma_f32_16x16x128_f8f6f4 v[212:215], v[128:133], v[68:73], v[212:215] cbsz:2 blgp:2
	v_cndmask_b32_e64 v158, v134, v204, s[0:1]
	v_fma_mix_f32 v158, v158, v100, v82 op_sel_hi:[0,0,1]
	v_exp_f32_e32 v158, v158
	v_cndmask_b32_e64 v159, v138, v208, s[0:1]
	v_fma_mix_f32 v159, v159, v101, v74 op_sel_hi:[0,0,1]
	v_exp_f32_e32 v159, v159
	v_fma_f32 v158, v158, v186, v186
	v_rcp_f32_e32 v158, v158
	v_add_f32_e32 v159, 1.0, v159
	v_rcp_f32_e32 v159, v159
	v_cndmask_b32_e64 v160, v142, v212, s[0:1]
	v_fma_mix_f32 v161, v158, v160, v78 op_sel_hi:[0,0,1]
	v_exp_f32_e32 v161, v161
	s_add_u32 s48, s48, s40
	v_add_f32_e32 v161, 1.0, v161
	v_rcp_f32_e32 v161, v161
	s_addc_u32 s49, s49, s41
	v_fma_f32 v162, v161, -2.0, 1.0
	v_sub_f32_e32 v163, v176, v162
	v_fma_f32 v176, v159, v163, v162
	v_fma_f32 v164, |v176|, s17, v113
	v_fma_f32 v165, |v176|, s18, v114
	v_fma_f32 v166, |v176|, s19, v115
	v_lshrrev_b32_e32 v167, 26, v176
	v_min3_u32 v164, v164, v165, v166
	v_bfi_b32 v168, 31, v164, v167
	global_store_short_d16_hi v185, v176, s[48:49]
	s_nop 0
	v_mul_u32_u24_dpp v170, v168, v180 quad_perm:[1,2,3,3] row_mask:0xf bank_mask:0xf bound_ctrl:1
	v_mad_u32_u24 v171, v168, v181, v170
	ds_write_b8_d16_hi v184, v171 offset:416
	s_waitcnt lgkmcnt(0)
	s_barrier
	ds_read_b64 v[122:123], v105 offset:416
	ds_read_b64 v[124:125], v105 offset:424
	ds_read_b64 v[126:127], v105 offset:432
	s_barrier
	ds_read_b64 v[128:129], v105 offset:512
	ds_read_b64 v[130:131], v105 offset:520
	ds_read_b64 v[132:133], v105 offset:528
	s_waitcnt lgkmcnt(3)
	v_mfma_f32_16x16x128_f8f6f4 v[134:137], v[122:127], v[2:7], 0 cbsz:2 blgp:2
	v_mfma_f32_16x16x128_f8f6f4 v[138:141], v[122:127], v[14:19], 0 cbsz:2 blgp:2
	v_mfma_f32_16x16x128_f8f6f4 v[142:145], v[122:127], v[26:31], v[188:191] cbsz:2 blgp:2
	v_mfma_f32_16x16x128_f8f6f4 v[204:207], v[122:127], v[38:43], 0 cbsz:2 blgp:2
	v_mfma_f32_16x16x128_f8f6f4 v[208:211], v[122:127], v[50:55], 0 cbsz:2 blgp:2
	v_mfma_f32_16x16x128_f8f6f4 v[212:215], v[122:127], v[62:67], v[188:191] cbsz:2 blgp:2
	s_waitcnt lgkmcnt(0)
	v_mfma_f32_16x16x128_f8f6f4 v[134:137], v[128:133], v[8:13], v[134:137] cbsz:2 blgp:2
	v_mfma_f32_16x16x128_f8f6f4 v[204:207], v[128:133], v[44:49], v[204:207] cbsz:2 blgp:2
	v_mfma_f32_16x16x128_f8f6f4 v[138:141], v[128:133], v[20:25], v[138:141] cbsz:2 blgp:2
	v_mfma_f32_16x16x128_f8f6f4 v[208:211], v[128:133], v[56:61], v[208:211] cbsz:2 blgp:2
	v_mfma_f32_16x16x128_f8f6f4 v[142:145], v[128:133], v[32:37], v[142:145] cbsz:2 blgp:2
	v_mfma_f32_16x16x128_f8f6f4 v[212:215], v[128:133], v[68:73], v[212:215] cbsz:2 blgp:2
	v_cndmask_b32_e64 v158, v134, v204, s[0:1]
	v_fma_mix_f32 v158, v158, v100, v82 op_sel:[0,0,1] op_sel_hi:[0,0,1]
	v_exp_f32_e32 v158, v158
	v_cndmask_b32_e64 v159, v138, v208, s[0:1]
	v_fma_mix_f32 v159, v159, v101, v74 op_sel:[0,0,1] op_sel_hi:[0,0,1]
	v_exp_f32_e32 v159, v159
	v_fma_f32 v158, v158, v186, v186
	v_rcp_f32_e32 v158, v158
	v_add_f32_e32 v159, 1.0, v159
	v_rcp_f32_e32 v159, v159
	v_cndmask_b32_e64 v160, v142, v212, s[0:1]
	v_fma_mix_f32 v161, v158, v160, v78 op_sel:[0,0,1] op_sel_hi:[0,0,1]
	v_exp_f32_e32 v161, v161
	s_add_u32 s48, s48, s40
	v_add_f32_e32 v161, 1.0, v161
	v_rcp_f32_e32 v161, v161
	s_addc_u32 s49, s49, s41
	v_fma_f32 v162, v161, -2.0, 1.0
	v_sub_f32_e32 v163, v176, v162
	v_fma_f32 v176, v159, v163, v162
	v_fma_f32 v164, |v176|, s17, v113
	v_fma_f32 v165, |v176|, s18, v114
	v_fma_f32 v166, |v176|, s19, v115
	v_lshrrev_b32_e32 v167, 26, v176
	v_min3_u32 v164, v164, v165, v166
	v_bfi_b32 v168, 31, v164, v167
	global_store_short_d16_hi v185, v176, s[48:49]
	s_nop 0
	v_mul_u32_u24_dpp v170, v168, v180 quad_perm:[1,2,3,3] row_mask:0xf bank_mask:0xf bound_ctrl:1
	v_mad_u32_u24 v171, v168, v181, v170
	ds_write_b8_d16_hi v184, v171
	s_waitcnt lgkmcnt(0)
	s_barrier
	ds_read_b64 v[122:123], v105 offset:0
	ds_read_b64 v[124:125], v105 offset:8
	ds_read_b64 v[126:127], v105 offset:16
	s_barrier
	ds_read_b64 v[128:129], v105 offset:96
	ds_read_b64 v[130:131], v105 offset:104
	ds_read_b64 v[132:133], v105 offset:112
	s_waitcnt lgkmcnt(3)
	v_mfma_f32_16x16x128_f8f6f4 v[134:137], v[122:127], v[2:7], 0 cbsz:2 blgp:2
	v_mfma_f32_16x16x128_f8f6f4 v[138:141], v[122:127], v[14:19], 0 cbsz:2 blgp:2
	v_mfma_f32_16x16x128_f8f6f4 v[142:145], v[122:127], v[26:31], v[188:191] cbsz:2 blgp:2
	v_mfma_f32_16x16x128_f8f6f4 v[204:207], v[122:127], v[38:43], 0 cbsz:2 blgp:2
	v_mfma_f32_16x16x128_f8f6f4 v[208:211], v[122:127], v[50:55], 0 cbsz:2 blgp:2
	v_mfma_f32_16x16x128_f8f6f4 v[212:215], v[122:127], v[62:67], v[188:191] cbsz:2 blgp:2
	s_waitcnt lgkmcnt(0)
	v_mfma_f32_16x16x128_f8f6f4 v[134:137], v[128:133], v[8:13], v[134:137] cbsz:2 blgp:2
	v_mfma_f32_16x16x128_f8f6f4 v[204:207], v[128:133], v[44:49], v[204:207] cbsz:2 blgp:2
	v_mfma_f32_16x16x128_f8f6f4 v[138:141], v[128:133], v[20:25], v[138:141] cbsz:2 blgp:2
	v_mfma_f32_16x16x128_f8f6f4 v[208:211], v[128:133], v[56:61], v[208:211] cbsz:2 blgp:2
	v_mfma_f32_16x16x128_f8f6f4 v[142:145], v[128:133], v[32:37], v[142:145] cbsz:2 blgp:2
	v_mfma_f32_16x16x128_f8f6f4 v[212:215], v[128:133], v[68:73], v[212:215] cbsz:2 blgp:2
	v_cndmask_b32_e64 v158, v134, v204, s[0:1]
	v_fma_mix_f32 v158, v158, v100, v83 op_sel_hi:[0,0,1]
	v_exp_f32_e32 v158, v158
	v_cndmask_b32_e64 v159, v138, v208, s[0:1]
	v_fma_mix_f32 v159, v159, v101, v75 op_sel_hi:[0,0,1]
	v_exp_f32_e32 v159, v159
	v_fma_f32 v158, v158, v186, v186
	v_rcp_f32_e32 v158, v158
	v_add_f32_e32 v159, 1.0, v159
	v_rcp_f32_e32 v159, v159
	v_cndmask_b32_e64 v160, v142, v212, s[0:1]
	v_fma_mix_f32 v161, v158, v160, v79 op_sel_hi:[0,0,1]
	v_exp_f32_e32 v161, v161
	s_add_u32 s48, s48, s40
	v_add_f32_e32 v161, 1.0, v161
	v_rcp_f32_e32 v161, v161
	s_addc_u32 s49, s49, s41
	v_fma_f32 v162, v161, -2.0, 1.0
	v_sub_f32_e32 v163, v176, v162
	v_fma_f32 v176, v159, v163, v162
	v_fma_f32 v164, |v176|, s17, v113
	v_fma_f32 v165, |v176|, s18, v114
	v_fma_f32 v166, |v176|, s19, v115
	v_lshrrev_b32_e32 v167, 26, v176
	v_min3_u32 v164, v164, v165, v166
	v_bfi_b32 v168, 31, v164, v167
	global_store_short_d16_hi v185, v176, s[48:49]
	s_nop 0
	v_mul_u32_u24_dpp v170, v168, v180 quad_perm:[1,2,3,3] row_mask:0xf bank_mask:0xf bound_ctrl:1
	v_mad_u32_u24 v171, v168, v181, v170
	ds_write_b8_d16_hi v184, v171 offset:416
	s_waitcnt lgkmcnt(0)
	s_barrier
	ds_read_b64 v[122:123], v105 offset:416
	ds_read_b64 v[124:125], v105 offset:424
	ds_read_b64 v[126:127], v105 offset:432
	s_barrier
	ds_read_b64 v[128:129], v105 offset:512
	ds_read_b64 v[130:131], v105 offset:520
	ds_read_b64 v[132:133], v105 offset:528
	s_waitcnt lgkmcnt(3)
	v_mfma_f32_16x16x128_f8f6f4 v[134:137], v[122:127], v[2:7], 0 cbsz:2 blgp:2
	v_mfma_f32_16x16x128_f8f6f4 v[138:141], v[122:127], v[14:19], 0 cbsz:2 blgp:2
	v_mfma_f32_16x16x128_f8f6f4 v[142:145], v[122:127], v[26:31], v[188:191] cbsz:2 blgp:2
	v_mfma_f32_16x16x128_f8f6f4 v[204:207], v[122:127], v[38:43], 0 cbsz:2 blgp:2
	v_mfma_f32_16x16x128_f8f6f4 v[208:211], v[122:127], v[50:55], 0 cbsz:2 blgp:2
	v_mfma_f32_16x16x128_f8f6f4 v[212:215], v[122:127], v[62:67], v[188:191] cbsz:2 blgp:2
	s_waitcnt lgkmcnt(0)
	v_mfma_f32_16x16x128_f8f6f4 v[134:137], v[128:133], v[8:13], v[134:137] cbsz:2 blgp:2
	v_mfma_f32_16x16x128_f8f6f4 v[204:207], v[128:133], v[44:49], v[204:207] cbsz:2 blgp:2
	v_mfma_f32_16x16x128_f8f6f4 v[138:141], v[128:133], v[20:25], v[138:141] cbsz:2 blgp:2
	v_mfma_f32_16x16x128_f8f6f4 v[208:211], v[128:133], v[56:61], v[208:211] cbsz:2 blgp:2
	v_mfma_f32_16x16x128_f8f6f4 v[142:145], v[128:133], v[32:37], v[142:145] cbsz:2 blgp:2
	v_mfma_f32_16x16x128_f8f6f4 v[212:215], v[128:133], v[68:73], v[212:215] cbsz:2 blgp:2
	v_cndmask_b32_e64 v158, v134, v204, s[0:1]
	v_fma_mix_f32 v158, v158, v100, v83 op_sel:[0,0,1] op_sel_hi:[0,0,1]
	v_exp_f32_e32 v158, v158
	v_cndmask_b32_e64 v159, v138, v208, s[0:1]
	v_fma_mix_f32 v159, v159, v101, v75 op_sel:[0,0,1] op_sel_hi:[0,0,1]
	v_exp_f32_e32 v159, v159
	v_fma_f32 v158, v158, v186, v186
	v_rcp_f32_e32 v158, v158
	v_add_f32_e32 v159, 1.0, v159
	v_rcp_f32_e32 v159, v159
	v_cndmask_b32_e64 v160, v142, v212, s[0:1]
	v_fma_mix_f32 v161, v158, v160, v79 op_sel:[0,0,1] op_sel_hi:[0,0,1]
	v_exp_f32_e32 v161, v161
	s_add_u32 s48, s48, s40
	v_add_f32_e32 v161, 1.0, v161
	v_rcp_f32_e32 v161, v161
	s_addc_u32 s49, s49, s41
	v_fma_f32 v162, v161, -2.0, 1.0
	v_sub_f32_e32 v163, v176, v162
	v_fma_f32 v176, v159, v163, v162
	v_fma_f32 v164, |v176|, s17, v113
	v_fma_f32 v165, |v176|, s18, v114
	v_fma_f32 v166, |v176|, s19, v115
	v_lshrrev_b32_e32 v167, 26, v176
	v_min3_u32 v164, v164, v165, v166
	v_bfi_b32 v168, 31, v164, v167
	global_store_short_d16_hi v185, v176, s[48:49]
	s_nop 0
	v_mul_u32_u24_dpp v170, v168, v180 quad_perm:[1,2,3,3] row_mask:0xf bank_mask:0xf bound_ctrl:1
	v_mad_u32_u24 v171, v168, v181, v170
	ds_write_b8_d16_hi v184, v171
	s_waitcnt lgkmcnt(0)
	s_barrier
	ds_read_b64 v[122:123], v105 offset:0
	ds_read_b64 v[124:125], v105 offset:8
	ds_read_b64 v[126:127], v105 offset:16
	s_barrier
	ds_read_b64 v[128:129], v105 offset:96
	ds_read_b64 v[130:131], v105 offset:104
	ds_read_b64 v[132:133], v105 offset:112
	s_waitcnt lgkmcnt(3)
	v_mfma_f32_16x16x128_f8f6f4 v[134:137], v[122:127], v[2:7], 0 cbsz:2 blgp:2
	v_mfma_f32_16x16x128_f8f6f4 v[138:141], v[122:127], v[14:19], 0 cbsz:2 blgp:2
	v_mfma_f32_16x16x128_f8f6f4 v[142:145], v[122:127], v[26:31], v[188:191] cbsz:2 blgp:2
	v_mfma_f32_16x16x128_f8f6f4 v[204:207], v[122:127], v[38:43], 0 cbsz:2 blgp:2
	v_mfma_f32_16x16x128_f8f6f4 v[208:211], v[122:127], v[50:55], 0 cbsz:2 blgp:2
	v_mfma_f32_16x16x128_f8f6f4 v[212:215], v[122:127], v[62:67], v[188:191] cbsz:2 blgp:2
	s_waitcnt lgkmcnt(0)
	v_mfma_f32_16x16x128_f8f6f4 v[134:137], v[128:133], v[8:13], v[134:137] cbsz:2 blgp:2
	v_mfma_f32_16x16x128_f8f6f4 v[204:207], v[128:133], v[44:49], v[204:207] cbsz:2 blgp:2
	v_mfma_f32_16x16x128_f8f6f4 v[138:141], v[128:133], v[20:25], v[138:141] cbsz:2 blgp:2
	v_mfma_f32_16x16x128_f8f6f4 v[208:211], v[128:133], v[56:61], v[208:211] cbsz:2 blgp:2
	v_mfma_f32_16x16x128_f8f6f4 v[142:145], v[128:133], v[32:37], v[142:145] cbsz:2 blgp:2
	v_mfma_f32_16x16x128_f8f6f4 v[212:215], v[128:133], v[68:73], v[212:215] cbsz:2 blgp:2
	v_cndmask_b32_e64 v158, v134, v204, s[0:1]
	v_fma_mix_f32 v158, v158, v100, v84 op_sel_hi:[0,0,1]
	v_exp_f32_e32 v158, v158
	v_cndmask_b32_e64 v159, v138, v208, s[0:1]
	v_fma_mix_f32 v159, v159, v101, v76 op_sel_hi:[0,0,1]
	v_exp_f32_e32 v159, v159
	v_fma_f32 v158, v158, v186, v186
	v_rcp_f32_e32 v158, v158
	v_add_f32_e32 v159, 1.0, v159
	v_rcp_f32_e32 v159, v159
	v_cndmask_b32_e64 v160, v142, v212, s[0:1]
	v_fma_mix_f32 v161, v158, v160, v80 op_sel_hi:[0,0,1]
	v_exp_f32_e32 v161, v161
	s_add_u32 s48, s48, s40
	v_add_f32_e32 v161, 1.0, v161
	v_rcp_f32_e32 v161, v161
	s_addc_u32 s49, s49, s41
	v_fma_f32 v162, v161, -2.0, 1.0
	v_sub_f32_e32 v163, v176, v162
	v_fma_f32 v176, v159, v163, v162
	v_fma_f32 v164, |v176|, s17, v113
	v_fma_f32 v165, |v176|, s18, v114
	v_fma_f32 v166, |v176|, s19, v115
	v_lshrrev_b32_e32 v167, 26, v176
	v_min3_u32 v164, v164, v165, v166
	v_bfi_b32 v168, 31, v164, v167
	global_store_short_d16_hi v185, v176, s[48:49]
	s_nop 0
	v_mul_u32_u24_dpp v170, v168, v180 quad_perm:[1,2,3,3] row_mask:0xf bank_mask:0xf bound_ctrl:1
	v_mad_u32_u24 v171, v168, v181, v170
	ds_write_b8_d16_hi v184, v171 offset:416
	s_waitcnt lgkmcnt(0)
	s_barrier
	ds_read_b64 v[122:123], v105 offset:416
	ds_read_b64 v[124:125], v105 offset:424
	ds_read_b64 v[126:127], v105 offset:432
	s_barrier
	ds_read_b64 v[128:129], v105 offset:512
	ds_read_b64 v[130:131], v105 offset:520
	ds_read_b64 v[132:133], v105 offset:528
	s_waitcnt lgkmcnt(3)
	v_mfma_f32_16x16x128_f8f6f4 v[134:137], v[122:127], v[2:7], 0 cbsz:2 blgp:2
	v_mfma_f32_16x16x128_f8f6f4 v[138:141], v[122:127], v[14:19], 0 cbsz:2 blgp:2
	v_mfma_f32_16x16x128_f8f6f4 v[142:145], v[122:127], v[26:31], v[188:191] cbsz:2 blgp:2
	v_mfma_f32_16x16x128_f8f6f4 v[204:207], v[122:127], v[38:43], 0 cbsz:2 blgp:2
	v_mfma_f32_16x16x128_f8f6f4 v[208:211], v[122:127], v[50:55], 0 cbsz:2 blgp:2
	v_mfma_f32_16x16x128_f8f6f4 v[212:215], v[122:127], v[62:67], v[188:191] cbsz:2 blgp:2
	s_waitcnt lgkmcnt(0)
	v_mfma_f32_16x16x128_f8f6f4 v[134:137], v[128:133], v[8:13], v[134:137] cbsz:2 blgp:2
	v_mfma_f32_16x16x128_f8f6f4 v[204:207], v[128:133], v[44:49], v[204:207] cbsz:2 blgp:2
	v_mfma_f32_16x16x128_f8f6f4 v[138:141], v[128:133], v[20:25], v[138:141] cbsz:2 blgp:2
	v_mfma_f32_16x16x128_f8f6f4 v[208:211], v[128:133], v[56:61], v[208:211] cbsz:2 blgp:2
	v_mfma_f32_16x16x128_f8f6f4 v[142:145], v[128:133], v[32:37], v[142:145] cbsz:2 blgp:2
	v_mfma_f32_16x16x128_f8f6f4 v[212:215], v[128:133], v[68:73], v[212:215] cbsz:2 blgp:2
	v_cndmask_b32_e64 v158, v134, v204, s[0:1]
	v_fma_mix_f32 v158, v158, v100, v84 op_sel:[0,0,1] op_sel_hi:[0,0,1]
	v_exp_f32_e32 v158, v158
	v_cndmask_b32_e64 v159, v138, v208, s[0:1]
	v_fma_mix_f32 v159, v159, v101, v76 op_sel:[0,0,1] op_sel_hi:[0,0,1]
	v_exp_f32_e32 v159, v159
	v_fma_f32 v158, v158, v186, v186
	v_rcp_f32_e32 v158, v158
	v_add_f32_e32 v159, 1.0, v159
	v_rcp_f32_e32 v159, v159
	v_cndmask_b32_e64 v160, v142, v212, s[0:1]
	v_fma_mix_f32 v161, v158, v160, v80 op_sel:[0,0,1] op_sel_hi:[0,0,1]
	v_exp_f32_e32 v161, v161
	s_add_u32 s48, s48, s40
	v_add_f32_e32 v161, 1.0, v161
	v_rcp_f32_e32 v161, v161
	s_addc_u32 s49, s49, s41
	v_fma_f32 v162, v161, -2.0, 1.0
	v_sub_f32_e32 v163, v176, v162
	v_fma_f32 v176, v159, v163, v162
	v_fma_f32 v164, |v176|, s17, v113
	v_fma_f32 v165, |v176|, s18, v114
	v_fma_f32 v166, |v176|, s19, v115
	v_lshrrev_b32_e32 v167, 26, v176
	v_min3_u32 v164, v164, v165, v166
	v_bfi_b32 v168, 31, v164, v167
	global_store_short_d16_hi v185, v176, s[48:49]
	s_nop 0
	v_mul_u32_u24_dpp v170, v168, v180 quad_perm:[1,2,3,3] row_mask:0xf bank_mask:0xf bound_ctrl:1
	v_mad_u32_u24 v171, v168, v181, v170
	ds_write_b8_d16_hi v184, v171
	s_waitcnt lgkmcnt(0)
	s_barrier
	ds_read_b64 v[122:123], v105 offset:0
	ds_read_b64 v[124:125], v105 offset:8
	ds_read_b64 v[126:127], v105 offset:16
	s_barrier
	ds_read_b64 v[128:129], v105 offset:96
	ds_read_b64 v[130:131], v105 offset:104
	ds_read_b64 v[132:133], v105 offset:112
	s_waitcnt lgkmcnt(3)
	v_mfma_f32_16x16x128_f8f6f4 v[134:137], v[122:127], v[2:7], 0 cbsz:2 blgp:2
	v_mfma_f32_16x16x128_f8f6f4 v[138:141], v[122:127], v[14:19], 0 cbsz:2 blgp:2
	v_mfma_f32_16x16x128_f8f6f4 v[142:145], v[122:127], v[26:31], v[188:191] cbsz:2 blgp:2
	v_mfma_f32_16x16x128_f8f6f4 v[204:207], v[122:127], v[38:43], 0 cbsz:2 blgp:2
	v_mfma_f32_16x16x128_f8f6f4 v[208:211], v[122:127], v[50:55], 0 cbsz:2 blgp:2
	v_mfma_f32_16x16x128_f8f6f4 v[212:215], v[122:127], v[62:67], v[188:191] cbsz:2 blgp:2
	s_waitcnt lgkmcnt(0)
	v_mfma_f32_16x16x128_f8f6f4 v[134:137], v[128:133], v[8:13], v[134:137] cbsz:2 blgp:2
	v_mfma_f32_16x16x128_f8f6f4 v[204:207], v[128:133], v[44:49], v[204:207] cbsz:2 blgp:2
	v_mfma_f32_16x16x128_f8f6f4 v[138:141], v[128:133], v[20:25], v[138:141] cbsz:2 blgp:2
	v_mfma_f32_16x16x128_f8f6f4 v[208:211], v[128:133], v[56:61], v[208:211] cbsz:2 blgp:2
	v_mfma_f32_16x16x128_f8f6f4 v[142:145], v[128:133], v[32:37], v[142:145] cbsz:2 blgp:2
	v_mfma_f32_16x16x128_f8f6f4 v[212:215], v[128:133], v[68:73], v[212:215] cbsz:2 blgp:2
	v_cndmask_b32_e64 v158, v134, v204, s[0:1]
	v_fma_mix_f32 v158, v158, v100, v85 op_sel_hi:[0,0,1]
	v_exp_f32_e32 v158, v158
	v_cndmask_b32_e64 v159, v138, v208, s[0:1]
	v_fma_mix_f32 v159, v159, v101, v77 op_sel_hi:[0,0,1]
	v_exp_f32_e32 v159, v159
	v_fma_f32 v158, v158, v186, v186
	v_rcp_f32_e32 v158, v158
	v_add_f32_e32 v159, 1.0, v159
	v_rcp_f32_e32 v159, v159
	v_cndmask_b32_e64 v160, v142, v212, s[0:1]
	v_fma_mix_f32 v161, v158, v160, v81 op_sel_hi:[0,0,1]
	v_exp_f32_e32 v161, v161
	s_add_u32 s48, s48, s40
	v_add_f32_e32 v161, 1.0, v161
	v_rcp_f32_e32 v161, v161
	s_addc_u32 s49, s49, s41
	v_fma_f32 v162, v161, -2.0, 1.0
	v_sub_f32_e32 v163, v176, v162
	v_fma_f32 v176, v159, v163, v162
	v_fma_f32 v164, |v176|, s17, v113
	v_fma_f32 v165, |v176|, s18, v114
	v_fma_f32 v166, |v176|, s19, v115
	v_lshrrev_b32_e32 v167, 26, v176
	v_min3_u32 v164, v164, v165, v166
	v_bfi_b32 v168, 31, v164, v167
	global_store_short_d16_hi v185, v176, s[48:49]
	s_nop 0
	v_mul_u32_u24_dpp v170, v168, v180 quad_perm:[1,2,3,3] row_mask:0xf bank_mask:0xf bound_ctrl:1
	v_mad_u32_u24 v171, v168, v181, v170
	ds_write_b8_d16_hi v184, v171 offset:416
	s_waitcnt lgkmcnt(0)
	s_barrier
	ds_read_b64 v[122:123], v105 offset:416
	ds_read_b64 v[124:125], v105 offset:424
	ds_read_b64 v[126:127], v105 offset:432
	s_barrier
	ds_read_b64 v[128:129], v105 offset:512
	ds_read_b64 v[130:131], v105 offset:520
	ds_read_b64 v[132:133], v105 offset:528
	s_waitcnt lgkmcnt(3)
	v_mfma_f32_16x16x128_f8f6f4 v[134:137], v[122:127], v[2:7], 0 cbsz:2 blgp:2
	v_mfma_f32_16x16x128_f8f6f4 v[138:141], v[122:127], v[14:19], 0 cbsz:2 blgp:2
	v_mfma_f32_16x16x128_f8f6f4 v[142:145], v[122:127], v[26:31], v[188:191] cbsz:2 blgp:2
	v_mfma_f32_16x16x128_f8f6f4 v[204:207], v[122:127], v[38:43], 0 cbsz:2 blgp:2
	v_mfma_f32_16x16x128_f8f6f4 v[208:211], v[122:127], v[50:55], 0 cbsz:2 blgp:2
	v_mfma_f32_16x16x128_f8f6f4 v[212:215], v[122:127], v[62:67], v[188:191] cbsz:2 blgp:2
	s_waitcnt lgkmcnt(0)
	v_mfma_f32_16x16x128_f8f6f4 v[134:137], v[128:133], v[8:13], v[134:137] cbsz:2 blgp:2
	v_mfma_f32_16x16x128_f8f6f4 v[204:207], v[128:133], v[44:49], v[204:207] cbsz:2 blgp:2
	v_mfma_f32_16x16x128_f8f6f4 v[138:141], v[128:133], v[20:25], v[138:141] cbsz:2 blgp:2
	v_mfma_f32_16x16x128_f8f6f4 v[208:211], v[128:133], v[56:61], v[208:211] cbsz:2 blgp:2
	v_mfma_f32_16x16x128_f8f6f4 v[142:145], v[128:133], v[32:37], v[142:145] cbsz:2 blgp:2
	v_mfma_f32_16x16x128_f8f6f4 v[212:215], v[128:133], v[68:73], v[212:215] cbsz:2 blgp:2
	v_cndmask_b32_e64 v158, v134, v204, s[0:1]
	v_fma_mix_f32 v158, v158, v100, v85 op_sel:[0,0,1] op_sel_hi:[0,0,1]
	v_exp_f32_e32 v158, v158
	v_cndmask_b32_e64 v159, v138, v208, s[0:1]
	v_fma_mix_f32 v159, v159, v101, v77 op_sel:[0,0,1] op_sel_hi:[0,0,1]
	v_exp_f32_e32 v159, v159
	v_fma_f32 v158, v158, v186, v186
	v_rcp_f32_e32 v158, v158
	v_add_f32_e32 v159, 1.0, v159
	v_rcp_f32_e32 v159, v159
	v_cndmask_b32_e64 v160, v142, v212, s[0:1]
	v_fma_mix_f32 v161, v158, v160, v81 op_sel:[0,0,1] op_sel_hi:[0,0,1]
	v_exp_f32_e32 v161, v161
	s_add_u32 s48, s48, s40
	v_add_f32_e32 v161, 1.0, v161
	v_rcp_f32_e32 v161, v161
	s_addc_u32 s49, s49, s41
	v_fma_f32 v162, v161, -2.0, 1.0
	v_sub_f32_e32 v163, v176, v162
	v_fma_f32 v176, v159, v163, v162
	v_fma_f32 v164, |v176|, s17, v113
	v_fma_f32 v165, |v176|, s18, v114
	v_fma_f32 v166, |v176|, s19, v115
	v_lshrrev_b32_e32 v167, 26, v176
	v_min3_u32 v164, v164, v165, v166
	v_bfi_b32 v168, 31, v164, v167
	global_store_short_d16_hi v185, v176, s[48:49]
	s_nop 0
	v_mul_u32_u24_dpp v170, v168, v180 quad_perm:[1,2,3,3] row_mask:0xf bank_mask:0xf bound_ctrl:1
	v_mad_u32_u24 v171, v168, v181, v170
	ds_write_b8_d16_hi v184, v171
	s_waitcnt lgkmcnt(0)
	s_barrier
	ds_read_b64 v[122:123], v105 offset:0
	ds_read_b64 v[124:125], v105 offset:8
	ds_read_b64 v[126:127], v105 offset:16
	s_barrier
	ds_read_b64 v[128:129], v105 offset:96
	ds_read_b64 v[130:131], v105 offset:104
	ds_read_b64 v[132:133], v105 offset:112
	s_waitcnt vmcnt(8)
	global_load_dwordx4 v[82:85], v[196:197], off
	global_load_dwordx4 v[74:77], v[196:197], off offset:512
	global_load_dwordx4 v[78:81], v[196:197], off offset:1024
	v_lshl_add_u64 v[196:197], v[196:197], 0, s[42:43]
	s_waitcnt lgkmcnt(3)
	v_mfma_f32_16x16x128_f8f6f4 v[134:137], v[122:127], v[2:7], 0 cbsz:2 blgp:2
	v_mfma_f32_16x16x128_f8f6f4 v[138:141], v[122:127], v[14:19], 0 cbsz:2 blgp:2
	v_mfma_f32_16x16x128_f8f6f4 v[142:145], v[122:127], v[26:31], v[188:191] cbsz:2 blgp:2
	v_mfma_f32_16x16x128_f8f6f4 v[204:207], v[122:127], v[38:43], 0 cbsz:2 blgp:2
	v_mfma_f32_16x16x128_f8f6f4 v[208:211], v[122:127], v[50:55], 0 cbsz:2 blgp:2
	v_mfma_f32_16x16x128_f8f6f4 v[212:215], v[122:127], v[62:67], v[188:191] cbsz:2 blgp:2
	s_waitcnt lgkmcnt(0)
	v_mfma_f32_16x16x128_f8f6f4 v[134:137], v[128:133], v[8:13], v[134:137] cbsz:2 blgp:2
	v_mfma_f32_16x16x128_f8f6f4 v[204:207], v[128:133], v[44:49], v[204:207] cbsz:2 blgp:2
	v_mfma_f32_16x16x128_f8f6f4 v[138:141], v[128:133], v[20:25], v[138:141] cbsz:2 blgp:2
	v_mfma_f32_16x16x128_f8f6f4 v[208:211], v[128:133], v[56:61], v[208:211] cbsz:2 blgp:2
	v_mfma_f32_16x16x128_f8f6f4 v[142:145], v[128:133], v[32:37], v[142:145] cbsz:2 blgp:2
	v_mfma_f32_16x16x128_f8f6f4 v[212:215], v[128:133], v[68:73], v[212:215] cbsz:2 blgp:2
	v_cndmask_b32_e64 v158, v134, v204, s[0:1]
	v_fma_mix_f32 v158, v158, v100, v146 op_sel_hi:[0,0,1]
	v_exp_f32_e32 v158, v158
	v_cndmask_b32_e64 v159, v138, v208, s[0:1]
	v_fma_mix_f32 v159, v159, v101, v150 op_sel_hi:[0,0,1]
	v_exp_f32_e32 v159, v159
	v_fma_f32 v158, v158, v186, v186
	v_rcp_f32_e32 v158, v158
	v_add_f32_e32 v159, 1.0, v159
	v_rcp_f32_e32 v159, v159
	v_cndmask_b32_e64 v160, v142, v212, s[0:1]
	v_fma_mix_f32 v161, v158, v160, v154 op_sel_hi:[0,0,1]
	v_exp_f32_e32 v161, v161
	s_add_u32 s48, s48, s40
	v_add_f32_e32 v161, 1.0, v161
	v_rcp_f32_e32 v161, v161
	s_addc_u32 s49, s49, s41
	v_fma_f32 v162, v161, -2.0, 1.0
	v_sub_f32_e32 v163, v176, v162
	v_fma_f32 v176, v159, v163, v162
	v_fma_f32 v164, |v176|, s17, v113
	v_fma_f32 v165, |v176|, s18, v114
	v_fma_f32 v166, |v176|, s19, v115
	v_lshrrev_b32_e32 v167, 26, v176
	v_min3_u32 v164, v164, v165, v166
	v_bfi_b32 v168, 31, v164, v167
	global_store_short_d16_hi v185, v176, s[48:49]
	s_nop 0
	v_mul_u32_u24_dpp v170, v168, v180 quad_perm:[1,2,3,3] row_mask:0xf bank_mask:0xf bound_ctrl:1
	v_mad_u32_u24 v171, v168, v181, v170
	ds_write_b8_d16_hi v184, v171 offset:416
	s_waitcnt lgkmcnt(0)
	s_barrier
	ds_read_b64 v[122:123], v105 offset:416
	ds_read_b64 v[124:125], v105 offset:424
	ds_read_b64 v[126:127], v105 offset:432
	s_barrier
	ds_read_b64 v[128:129], v105 offset:512
	ds_read_b64 v[130:131], v105 offset:520
	ds_read_b64 v[132:133], v105 offset:528
	s_waitcnt lgkmcnt(3)
	v_mfma_f32_16x16x128_f8f6f4 v[134:137], v[122:127], v[2:7], 0 cbsz:2 blgp:2
	v_mfma_f32_16x16x128_f8f6f4 v[138:141], v[122:127], v[14:19], 0 cbsz:2 blgp:2
	v_mfma_f32_16x16x128_f8f6f4 v[142:145], v[122:127], v[26:31], v[188:191] cbsz:2 blgp:2
	v_mfma_f32_16x16x128_f8f6f4 v[204:207], v[122:127], v[38:43], 0 cbsz:2 blgp:2
	v_mfma_f32_16x16x128_f8f6f4 v[208:211], v[122:127], v[50:55], 0 cbsz:2 blgp:2
	v_mfma_f32_16x16x128_f8f6f4 v[212:215], v[122:127], v[62:67], v[188:191] cbsz:2 blgp:2
	s_waitcnt lgkmcnt(0)
	v_mfma_f32_16x16x128_f8f6f4 v[134:137], v[128:133], v[8:13], v[134:137] cbsz:2 blgp:2
	v_mfma_f32_16x16x128_f8f6f4 v[204:207], v[128:133], v[44:49], v[204:207] cbsz:2 blgp:2
	v_mfma_f32_16x16x128_f8f6f4 v[138:141], v[128:133], v[20:25], v[138:141] cbsz:2 blgp:2
	v_mfma_f32_16x16x128_f8f6f4 v[208:211], v[128:133], v[56:61], v[208:211] cbsz:2 blgp:2
	v_mfma_f32_16x16x128_f8f6f4 v[142:145], v[128:133], v[32:37], v[142:145] cbsz:2 blgp:2
	v_mfma_f32_16x16x128_f8f6f4 v[212:215], v[128:133], v[68:73], v[212:215] cbsz:2 blgp:2
	v_cndmask_b32_e64 v158, v134, v204, s[0:1]
	v_fma_mix_f32 v158, v158, v100, v146 op_sel:[0,0,1] op_sel_hi:[0,0,1]
	v_exp_f32_e32 v158, v158
	v_cndmask_b32_e64 v159, v138, v208, s[0:1]
	v_fma_mix_f32 v159, v159, v101, v150 op_sel:[0,0,1] op_sel_hi:[0,0,1]
	v_exp_f32_e32 v159, v159
	v_fma_f32 v158, v158, v186, v186
	v_rcp_f32_e32 v158, v158
	v_add_f32_e32 v159, 1.0, v159
	v_rcp_f32_e32 v159, v159
	v_cndmask_b32_e64 v160, v142, v212, s[0:1]
	v_fma_mix_f32 v161, v158, v160, v154 op_sel:[0,0,1] op_sel_hi:[0,0,1]
	v_exp_f32_e32 v161, v161
	s_add_u32 s48, s48, s40
	v_add_f32_e32 v161, 1.0, v161
	v_rcp_f32_e32 v161, v161
	s_addc_u32 s49, s49, s41
	v_fma_f32 v162, v161, -2.0, 1.0
	v_sub_f32_e32 v163, v176, v162
	v_fma_f32 v176, v159, v163, v162
	v_fma_f32 v164, |v176|, s17, v113
	v_fma_f32 v165, |v176|, s18, v114
	v_fma_f32 v166, |v176|, s19, v115
	v_lshrrev_b32_e32 v167, 26, v176
	v_min3_u32 v164, v164, v165, v166
	v_bfi_b32 v168, 31, v164, v167
	global_store_short_d16_hi v185, v176, s[48:49]
	s_nop 0
	v_mul_u32_u24_dpp v170, v168, v180 quad_perm:[1,2,3,3] row_mask:0xf bank_mask:0xf bound_ctrl:1
	v_mad_u32_u24 v171, v168, v181, v170
	ds_write_b8_d16_hi v184, v171
	s_waitcnt lgkmcnt(0)
	s_barrier
	ds_read_b64 v[122:123], v105 offset:0
	ds_read_b64 v[124:125], v105 offset:8
	ds_read_b64 v[126:127], v105 offset:16
	s_barrier
	ds_read_b64 v[128:129], v105 offset:96
	ds_read_b64 v[130:131], v105 offset:104
	ds_read_b64 v[132:133], v105 offset:112
	s_waitcnt lgkmcnt(3)
	v_mfma_f32_16x16x128_f8f6f4 v[134:137], v[122:127], v[2:7], 0 cbsz:2 blgp:2
	v_mfma_f32_16x16x128_f8f6f4 v[138:141], v[122:127], v[14:19], 0 cbsz:2 blgp:2
	v_mfma_f32_16x16x128_f8f6f4 v[142:145], v[122:127], v[26:31], v[188:191] cbsz:2 blgp:2
	v_mfma_f32_16x16x128_f8f6f4 v[204:207], v[122:127], v[38:43], 0 cbsz:2 blgp:2
	v_mfma_f32_16x16x128_f8f6f4 v[208:211], v[122:127], v[50:55], 0 cbsz:2 blgp:2
	v_mfma_f32_16x16x128_f8f6f4 v[212:215], v[122:127], v[62:67], v[188:191] cbsz:2 blgp:2
	s_waitcnt lgkmcnt(0)
	v_mfma_f32_16x16x128_f8f6f4 v[134:137], v[128:133], v[8:13], v[134:137] cbsz:2 blgp:2
	v_mfma_f32_16x16x128_f8f6f4 v[204:207], v[128:133], v[44:49], v[204:207] cbsz:2 blgp:2
	v_mfma_f32_16x16x128_f8f6f4 v[138:141], v[128:133], v[20:25], v[138:141] cbsz:2 blgp:2
	v_mfma_f32_16x16x128_f8f6f4 v[208:211], v[128:133], v[56:61], v[208:211] cbsz:2 blgp:2
	v_mfma_f32_16x16x128_f8f6f4 v[142:145], v[128:133], v[32:37], v[142:145] cbsz:2 blgp:2
	v_mfma_f32_16x16x128_f8f6f4 v[212:215], v[128:133], v[68:73], v[212:215] cbsz:2 blgp:2
	v_cndmask_b32_e64 v158, v134, v204, s[0:1]
	v_fma_mix_f32 v158, v158, v100, v147 op_sel_hi:[0,0,1]
	v_exp_f32_e32 v158, v158
	v_cndmask_b32_e64 v159, v138, v208, s[0:1]
	v_fma_mix_f32 v159, v159, v101, v151 op_sel_hi:[0,0,1]
	v_exp_f32_e32 v159, v159
	v_fma_f32 v158, v158, v186, v186
	v_rcp_f32_e32 v158, v158
	v_add_f32_e32 v159, 1.0, v159
	v_rcp_f32_e32 v159, v159
	v_cndmask_b32_e64 v160, v142, v212, s[0:1]
	v_fma_mix_f32 v161, v158, v160, v155 op_sel_hi:[0,0,1]
	v_exp_f32_e32 v161, v161
	s_add_u32 s48, s48, s40
	v_add_f32_e32 v161, 1.0, v161
	v_rcp_f32_e32 v161, v161
	s_addc_u32 s49, s49, s41
	v_fma_f32 v162, v161, -2.0, 1.0
	v_sub_f32_e32 v163, v176, v162
	v_fma_f32 v176, v159, v163, v162
	v_fma_f32 v164, |v176|, s17, v113
	v_fma_f32 v165, |v176|, s18, v114
	v_fma_f32 v166, |v176|, s19, v115
	v_lshrrev_b32_e32 v167, 26, v176
	v_min3_u32 v164, v164, v165, v166
	v_bfi_b32 v168, 31, v164, v167
	global_store_short_d16_hi v185, v176, s[48:49]
	s_nop 0
	v_mul_u32_u24_dpp v170, v168, v180 quad_perm:[1,2,3,3] row_mask:0xf bank_mask:0xf bound_ctrl:1
	v_mad_u32_u24 v171, v168, v181, v170
	ds_write_b8_d16_hi v184, v171 offset:416
	s_waitcnt lgkmcnt(0)
	s_barrier
	ds_read_b64 v[122:123], v105 offset:416
	ds_read_b64 v[124:125], v105 offset:424
	ds_read_b64 v[126:127], v105 offset:432
	s_barrier
	ds_read_b64 v[128:129], v105 offset:512
	ds_read_b64 v[130:131], v105 offset:520
	ds_read_b64 v[132:133], v105 offset:528
	s_waitcnt lgkmcnt(3)
	v_mfma_f32_16x16x128_f8f6f4 v[134:137], v[122:127], v[2:7], 0 cbsz:2 blgp:2
	v_mfma_f32_16x16x128_f8f6f4 v[138:141], v[122:127], v[14:19], 0 cbsz:2 blgp:2
	v_mfma_f32_16x16x128_f8f6f4 v[142:145], v[122:127], v[26:31], v[188:191] cbsz:2 blgp:2
	v_mfma_f32_16x16x128_f8f6f4 v[204:207], v[122:127], v[38:43], 0 cbsz:2 blgp:2
	v_mfma_f32_16x16x128_f8f6f4 v[208:211], v[122:127], v[50:55], 0 cbsz:2 blgp:2
	v_mfma_f32_16x16x128_f8f6f4 v[212:215], v[122:127], v[62:67], v[188:191] cbsz:2 blgp:2
	s_waitcnt lgkmcnt(0)
	v_mfma_f32_16x16x128_f8f6f4 v[134:137], v[128:133], v[8:13], v[134:137] cbsz:2 blgp:2
	v_mfma_f32_16x16x128_f8f6f4 v[204:207], v[128:133], v[44:49], v[204:207] cbsz:2 blgp:2
	v_mfma_f32_16x16x128_f8f6f4 v[138:141], v[128:133], v[20:25], v[138:141] cbsz:2 blgp:2
	v_mfma_f32_16x16x128_f8f6f4 v[208:211], v[128:133], v[56:61], v[208:211] cbsz:2 blgp:2
	v_mfma_f32_16x16x128_f8f6f4 v[142:145], v[128:133], v[32:37], v[142:145] cbsz:2 blgp:2
	v_mfma_f32_16x16x128_f8f6f4 v[212:215], v[128:133], v[68:73], v[212:215] cbsz:2 blgp:2
	v_cndmask_b32_e64 v158, v134, v204, s[0:1]
	v_fma_mix_f32 v158, v158, v100, v147 op_sel:[0,0,1] op_sel_hi:[0,0,1]
	v_exp_f32_e32 v158, v158
	v_cndmask_b32_e64 v159, v138, v208, s[0:1]
	v_fma_mix_f32 v159, v159, v101, v151 op_sel:[0,0,1] op_sel_hi:[0,0,1]
	v_exp_f32_e32 v159, v159
	v_fma_f32 v158, v158, v186, v186
	v_rcp_f32_e32 v158, v158
	v_add_f32_e32 v159, 1.0, v159
	v_rcp_f32_e32 v159, v159
	v_cndmask_b32_e64 v160, v142, v212, s[0:1]
	v_fma_mix_f32 v161, v158, v160, v155 op_sel:[0,0,1] op_sel_hi:[0,0,1]
	v_exp_f32_e32 v161, v161
	s_add_u32 s48, s48, s40
	v_add_f32_e32 v161, 1.0, v161
	v_rcp_f32_e32 v161, v161
	s_addc_u32 s49, s49, s41
	v_fma_f32 v162, v161, -2.0, 1.0
	v_sub_f32_e32 v163, v176, v162
	v_fma_f32 v176, v159, v163, v162
	v_fma_f32 v164, |v176|, s17, v113
	v_fma_f32 v165, |v176|, s18, v114
	v_fma_f32 v166, |v176|, s19, v115
	v_lshrrev_b32_e32 v167, 26, v176
	v_min3_u32 v164, v164, v165, v166
	v_bfi_b32 v168, 31, v164, v167
	global_store_short_d16_hi v185, v176, s[48:49]
	s_nop 0
	v_mul_u32_u24_dpp v170, v168, v180 quad_perm:[1,2,3,3] row_mask:0xf bank_mask:0xf bound_ctrl:1
	v_mad_u32_u24 v171, v168, v181, v170
	ds_write_b8_d16_hi v184, v171
	s_waitcnt lgkmcnt(0)
	s_barrier
	ds_read_b64 v[122:123], v105 offset:0
	ds_read_b64 v[124:125], v105 offset:8
	ds_read_b64 v[126:127], v105 offset:16
	s_barrier
	ds_read_b64 v[128:129], v105 offset:96
	ds_read_b64 v[130:131], v105 offset:104
	ds_read_b64 v[132:133], v105 offset:112
	s_waitcnt lgkmcnt(3)
	v_mfma_f32_16x16x128_f8f6f4 v[134:137], v[122:127], v[2:7], 0 cbsz:2 blgp:2
	v_mfma_f32_16x16x128_f8f6f4 v[138:141], v[122:127], v[14:19], 0 cbsz:2 blgp:2
	v_mfma_f32_16x16x128_f8f6f4 v[142:145], v[122:127], v[26:31], v[188:191] cbsz:2 blgp:2
	v_mfma_f32_16x16x128_f8f6f4 v[204:207], v[122:127], v[38:43], 0 cbsz:2 blgp:2
	v_mfma_f32_16x16x128_f8f6f4 v[208:211], v[122:127], v[50:55], 0 cbsz:2 blgp:2
	v_mfma_f32_16x16x128_f8f6f4 v[212:215], v[122:127], v[62:67], v[188:191] cbsz:2 blgp:2
	s_waitcnt lgkmcnt(0)
	v_mfma_f32_16x16x128_f8f6f4 v[134:137], v[128:133], v[8:13], v[134:137] cbsz:2 blgp:2
	v_mfma_f32_16x16x128_f8f6f4 v[204:207], v[128:133], v[44:49], v[204:207] cbsz:2 blgp:2
	v_mfma_f32_16x16x128_f8f6f4 v[138:141], v[128:133], v[20:25], v[138:141] cbsz:2 blgp:2
	v_mfma_f32_16x16x128_f8f6f4 v[208:211], v[128:133], v[56:61], v[208:211] cbsz:2 blgp:2
	v_mfma_f32_16x16x128_f8f6f4 v[142:145], v[128:133], v[32:37], v[142:145] cbsz:2 blgp:2
	v_mfma_f32_16x16x128_f8f6f4 v[212:215], v[128:133], v[68:73], v[212:215] cbsz:2 blgp:2
	v_cndmask_b32_e64 v158, v134, v204, s[0:1]
	v_fma_mix_f32 v158, v158, v100, v148 op_sel_hi:[0,0,1]
	v_exp_f32_e32 v158, v158
	v_cndmask_b32_e64 v159, v138, v208, s[0:1]
	v_fma_mix_f32 v159, v159, v101, v152 op_sel_hi:[0,0,1]
	v_exp_f32_e32 v159, v159
	v_fma_f32 v158, v158, v186, v186
	v_rcp_f32_e32 v158, v158
	v_add_f32_e32 v159, 1.0, v159
	v_rcp_f32_e32 v159, v159
	v_cndmask_b32_e64 v160, v142, v212, s[0:1]
	v_fma_mix_f32 v161, v158, v160, v156 op_sel_hi:[0,0,1]
	v_exp_f32_e32 v161, v161
	s_add_u32 s48, s48, s40
	v_add_f32_e32 v161, 1.0, v161
	v_rcp_f32_e32 v161, v161
	s_addc_u32 s49, s49, s41
	v_fma_f32 v162, v161, -2.0, 1.0
	v_sub_f32_e32 v163, v176, v162
	v_fma_f32 v176, v159, v163, v162
	v_fma_f32 v164, |v176|, s17, v113
	v_fma_f32 v165, |v176|, s18, v114
	v_fma_f32 v166, |v176|, s19, v115
	v_lshrrev_b32_e32 v167, 26, v176
	v_min3_u32 v164, v164, v165, v166
	v_bfi_b32 v168, 31, v164, v167
	global_store_short_d16_hi v185, v176, s[48:49]
	s_nop 0
	v_mul_u32_u24_dpp v170, v168, v180 quad_perm:[1,2,3,3] row_mask:0xf bank_mask:0xf bound_ctrl:1
	v_mad_u32_u24 v171, v168, v181, v170
	ds_write_b8_d16_hi v184, v171 offset:416
	s_waitcnt lgkmcnt(0)
	s_barrier
	ds_read_b64 v[122:123], v105 offset:416
	ds_read_b64 v[124:125], v105 offset:424
	ds_read_b64 v[126:127], v105 offset:432
	s_barrier
	ds_read_b64 v[128:129], v105 offset:512
	ds_read_b64 v[130:131], v105 offset:520
	ds_read_b64 v[132:133], v105 offset:528
	s_waitcnt lgkmcnt(3)
	v_mfma_f32_16x16x128_f8f6f4 v[134:137], v[122:127], v[2:7], 0 cbsz:2 blgp:2
	v_mfma_f32_16x16x128_f8f6f4 v[138:141], v[122:127], v[14:19], 0 cbsz:2 blgp:2
	v_mfma_f32_16x16x128_f8f6f4 v[142:145], v[122:127], v[26:31], v[188:191] cbsz:2 blgp:2
	v_mfma_f32_16x16x128_f8f6f4 v[204:207], v[122:127], v[38:43], 0 cbsz:2 blgp:2
	v_mfma_f32_16x16x128_f8f6f4 v[208:211], v[122:127], v[50:55], 0 cbsz:2 blgp:2
	v_mfma_f32_16x16x128_f8f6f4 v[212:215], v[122:127], v[62:67], v[188:191] cbsz:2 blgp:2
	s_waitcnt lgkmcnt(0)
	v_mfma_f32_16x16x128_f8f6f4 v[134:137], v[128:133], v[8:13], v[134:137] cbsz:2 blgp:2
	v_mfma_f32_16x16x128_f8f6f4 v[204:207], v[128:133], v[44:49], v[204:207] cbsz:2 blgp:2
	v_mfma_f32_16x16x128_f8f6f4 v[138:141], v[128:133], v[20:25], v[138:141] cbsz:2 blgp:2
	v_mfma_f32_16x16x128_f8f6f4 v[208:211], v[128:133], v[56:61], v[208:211] cbsz:2 blgp:2
	v_mfma_f32_16x16x128_f8f6f4 v[142:145], v[128:133], v[32:37], v[142:145] cbsz:2 blgp:2
	v_mfma_f32_16x16x128_f8f6f4 v[212:215], v[128:133], v[68:73], v[212:215] cbsz:2 blgp:2
	v_cndmask_b32_e64 v158, v134, v204, s[0:1]
	v_fma_mix_f32 v158, v158, v100, v148 op_sel:[0,0,1] op_sel_hi:[0,0,1]
	v_exp_f32_e32 v158, v158
	v_cndmask_b32_e64 v159, v138, v208, s[0:1]
	v_fma_mix_f32 v159, v159, v101, v152 op_sel:[0,0,1] op_sel_hi:[0,0,1]
	v_exp_f32_e32 v159, v159
	v_fma_f32 v158, v158, v186, v186
	v_rcp_f32_e32 v158, v158
	v_add_f32_e32 v159, 1.0, v159
	v_rcp_f32_e32 v159, v159
	v_cndmask_b32_e64 v160, v142, v212, s[0:1]
	v_fma_mix_f32 v161, v158, v160, v156 op_sel:[0,0,1] op_sel_hi:[0,0,1]
	v_exp_f32_e32 v161, v161
	s_add_u32 s48, s48, s40
	v_add_f32_e32 v161, 1.0, v161
	v_rcp_f32_e32 v161, v161
	s_addc_u32 s49, s49, s41
	v_fma_f32 v162, v161, -2.0, 1.0
	v_sub_f32_e32 v163, v176, v162
	v_fma_f32 v176, v159, v163, v162
	v_fma_f32 v164, |v176|, s17, v113
	v_fma_f32 v165, |v176|, s18, v114
	v_fma_f32 v166, |v176|, s19, v115
	v_lshrrev_b32_e32 v167, 26, v176
	v_min3_u32 v164, v164, v165, v166
	v_bfi_b32 v168, 31, v164, v167
	global_store_short_d16_hi v185, v176, s[48:49]
	s_nop 0
	v_mul_u32_u24_dpp v170, v168, v180 quad_perm:[1,2,3,3] row_mask:0xf bank_mask:0xf bound_ctrl:1
	v_mad_u32_u24 v171, v168, v181, v170
	ds_write_b8_d16_hi v184, v171
	s_waitcnt lgkmcnt(0)
	s_barrier
	ds_read_b64 v[122:123], v105 offset:0
	ds_read_b64 v[124:125], v105 offset:8
	ds_read_b64 v[126:127], v105 offset:16
	s_barrier
	ds_read_b64 v[128:129], v105 offset:96
	ds_read_b64 v[130:131], v105 offset:104
	ds_read_b64 v[132:133], v105 offset:112
	s_waitcnt lgkmcnt(3)
	v_mfma_f32_16x16x128_f8f6f4 v[134:137], v[122:127], v[2:7], 0 cbsz:2 blgp:2
	v_mfma_f32_16x16x128_f8f6f4 v[138:141], v[122:127], v[14:19], 0 cbsz:2 blgp:2
	v_mfma_f32_16x16x128_f8f6f4 v[142:145], v[122:127], v[26:31], v[188:191] cbsz:2 blgp:2
	v_mfma_f32_16x16x128_f8f6f4 v[204:207], v[122:127], v[38:43], 0 cbsz:2 blgp:2
	v_mfma_f32_16x16x128_f8f6f4 v[208:211], v[122:127], v[50:55], 0 cbsz:2 blgp:2
	v_mfma_f32_16x16x128_f8f6f4 v[212:215], v[122:127], v[62:67], v[188:191] cbsz:2 blgp:2
	s_waitcnt lgkmcnt(0)
	v_mfma_f32_16x16x128_f8f6f4 v[134:137], v[128:133], v[8:13], v[134:137] cbsz:2 blgp:2
	v_mfma_f32_16x16x128_f8f6f4 v[204:207], v[128:133], v[44:49], v[204:207] cbsz:2 blgp:2
	v_mfma_f32_16x16x128_f8f6f4 v[138:141], v[128:133], v[20:25], v[138:141] cbsz:2 blgp:2
	v_mfma_f32_16x16x128_f8f6f4 v[208:211], v[128:133], v[56:61], v[208:211] cbsz:2 blgp:2
	v_mfma_f32_16x16x128_f8f6f4 v[142:145], v[128:133], v[32:37], v[142:145] cbsz:2 blgp:2
	v_mfma_f32_16x16x128_f8f6f4 v[212:215], v[128:133], v[68:73], v[212:215] cbsz:2 blgp:2
	v_cndmask_b32_e64 v158, v134, v204, s[0:1]
	v_fma_mix_f32 v158, v158, v100, v149 op_sel_hi:[0,0,1]
	v_exp_f32_e32 v158, v158
	v_cndmask_b32_e64 v159, v138, v208, s[0:1]
	v_fma_mix_f32 v159, v159, v101, v153 op_sel_hi:[0,0,1]
	v_exp_f32_e32 v159, v159
	v_fma_f32 v158, v158, v186, v186
	v_rcp_f32_e32 v158, v158
	v_add_f32_e32 v159, 1.0, v159
	v_rcp_f32_e32 v159, v159
	v_cndmask_b32_e64 v160, v142, v212, s[0:1]
	v_fma_mix_f32 v161, v158, v160, v157 op_sel_hi:[0,0,1]
	v_exp_f32_e32 v161, v161
	s_add_u32 s48, s48, s40
	v_add_f32_e32 v161, 1.0, v161
	v_rcp_f32_e32 v161, v161
	s_addc_u32 s49, s49, s41
	v_fma_f32 v162, v161, -2.0, 1.0
	v_sub_f32_e32 v163, v176, v162
	v_fma_f32 v176, v159, v163, v162
	v_fma_f32 v164, |v176|, s17, v113
	v_fma_f32 v165, |v176|, s18, v114
	v_fma_f32 v166, |v176|, s19, v115
	v_lshrrev_b32_e32 v167, 26, v176
	v_min3_u32 v164, v164, v165, v166
	v_bfi_b32 v168, 31, v164, v167
	global_store_short_d16_hi v185, v176, s[48:49]
	s_nop 0
	v_mul_u32_u24_dpp v170, v168, v180 quad_perm:[1,2,3,3] row_mask:0xf bank_mask:0xf bound_ctrl:1
	v_mad_u32_u24 v171, v168, v181, v170
	ds_write_b8_d16_hi v184, v171 offset:416
	s_waitcnt lgkmcnt(0)
	s_barrier
	ds_read_b64 v[122:123], v105 offset:416
	ds_read_b64 v[124:125], v105 offset:424
	ds_read_b64 v[126:127], v105 offset:432
	s_barrier
	ds_read_b64 v[128:129], v105 offset:512
	ds_read_b64 v[130:131], v105 offset:520
	ds_read_b64 v[132:133], v105 offset:528
	s_add_i32 s44, s44, 16
	s_waitcnt lgkmcnt(3)
	v_mfma_f32_16x16x128_f8f6f4 v[134:137], v[122:127], v[2:7], 0 cbsz:2 blgp:2
	v_mfma_f32_16x16x128_f8f6f4 v[138:141], v[122:127], v[14:19], 0 cbsz:2 blgp:2
	v_mfma_f32_16x16x128_f8f6f4 v[142:145], v[122:127], v[26:31], v[188:191] cbsz:2 blgp:2
	v_mfma_f32_16x16x128_f8f6f4 v[204:207], v[122:127], v[38:43], 0 cbsz:2 blgp:2
	v_mfma_f32_16x16x128_f8f6f4 v[208:211], v[122:127], v[50:55], 0 cbsz:2 blgp:2
	v_mfma_f32_16x16x128_f8f6f4 v[212:215], v[122:127], v[62:67], v[188:191] cbsz:2 blgp:2
	s_waitcnt lgkmcnt(0)
	v_mfma_f32_16x16x128_f8f6f4 v[134:137], v[128:133], v[8:13], v[134:137] cbsz:2 blgp:2
	v_mfma_f32_16x16x128_f8f6f4 v[204:207], v[128:133], v[44:49], v[204:207] cbsz:2 blgp:2
	v_mfma_f32_16x16x128_f8f6f4 v[138:141], v[128:133], v[20:25], v[138:141] cbsz:2 blgp:2
	v_mfma_f32_16x16x128_f8f6f4 v[208:211], v[128:133], v[56:61], v[208:211] cbsz:2 blgp:2
	v_mfma_f32_16x16x128_f8f6f4 v[142:145], v[128:133], v[32:37], v[142:145] cbsz:2 blgp:2
	v_mfma_f32_16x16x128_f8f6f4 v[212:215], v[128:133], v[68:73], v[212:215] cbsz:2 blgp:2
	v_cndmask_b32_e64 v158, v134, v204, s[0:1]
	v_fma_mix_f32 v158, v158, v100, v149 op_sel:[0,0,1] op_sel_hi:[0,0,1]
	v_exp_f32_e32 v158, v158
	v_cndmask_b32_e64 v159, v138, v208, s[0:1]
	v_fma_mix_f32 v159, v159, v101, v153 op_sel:[0,0,1] op_sel_hi:[0,0,1]
	v_exp_f32_e32 v159, v159
	v_fma_f32 v158, v158, v186, v186
	v_rcp_f32_e32 v158, v158
	v_add_f32_e32 v159, 1.0, v159
	v_rcp_f32_e32 v159, v159
	v_cndmask_b32_e64 v160, v142, v212, s[0:1]
	v_fma_mix_f32 v161, v158, v160, v157 op_sel:[0,0,1] op_sel_hi:[0,0,1]
	v_exp_f32_e32 v161, v161
	s_add_u32 s48, s48, s40
	v_add_f32_e32 v161, 1.0, v161
	v_rcp_f32_e32 v161, v161
	s_addc_u32 s49, s49, s41
	v_fma_f32 v162, v161, -2.0, 1.0
	v_sub_f32_e32 v163, v176, v162
	v_fma_f32 v176, v159, v163, v162
	v_fma_f32 v164, |v176|, s17, v113
	v_fma_f32 v165, |v176|, s18, v114
	v_fma_f32 v166, |v176|, s19, v115
	v_lshrrev_b32_e32 v167, 26, v176
	v_min3_u32 v164, v164, v165, v166
	v_bfi_b32 v168, 31, v164, v167
	global_store_short_d16_hi v185, v176, s[48:49]
	s_nop 0
	v_mul_u32_u24_dpp v170, v168, v180 quad_perm:[1,2,3,3] row_mask:0xf bank_mask:0xf bound_ctrl:1
	v_mad_u32_u24 v171, v168, v181, v170
	ds_write_b8_d16_hi v184, v171
	s_waitcnt lgkmcnt(0)
	s_barrier
	ds_read_b64 v[122:123], v105 offset:0
	ds_read_b64 v[124:125], v105 offset:8
	ds_read_b64 v[126:127], v105 offset:16
	s_cmp_lt_i32 s44, s45
	s_barrier
	s_cbranch_scc1 .Lscan_loop_a_f2
	s_branch .Lscan_exit_f2
.Lscan_loop_b_f2:
	ds_read_b64 v[122:123], v105 offset:0
	ds_read_b64 v[124:125], v105 offset:8
	ds_read_b64 v[126:127], v105 offset:16
	ds_read_b64 v[128:129], v105 offset:96
	ds_read_b64 v[130:131], v105 offset:104
	ds_read_b64 v[132:133], v105 offset:112
	s_waitcnt vmcnt(8)
	global_load_dwordx4 v[146:149], v[196:197], off
	global_load_dwordx4 v[150:153], v[196:197], off offset:512
	global_load_dwordx4 v[154:157], v[196:197], off offset:1024
	v_lshl_add_u64 v[196:197], v[196:197], 0, s[42:43]
	s_waitcnt lgkmcnt(3)
	v_mfma_f32_16x16x128_f8f6f4 v[134:137], v[122:127], v[2:7], 0 cbsz:2 blgp:2
	v_mfma_f32_16x16x128_f8f6f4 v[138:141], v[122:127], v[14:19], 0 cbsz:2 blgp:2
	v_mfma_f32_16x16x128_f8f6f4 v[142:145], v[122:127], v[26:31], v[188:191] cbsz:2 blgp:2
	v_mfma_f32_16x16x128_f8f6f4 v[204:207], v[122:127], v[38:43], 0 cbsz:2 blgp:2
	v_mfma_f32_16x16x128_f8f6f4 v[208:211], v[122:127], v[50:55], 0 cbsz:2 blgp:2
	v_mfma_f32_16x16x128_f8f6f4 v[212:215], v[122:127], v[62:67], v[188:191] cbsz:2 blgp:2
	s_waitcnt lgkmcnt(0)
	v_mfma_f32_16x16x128_f8f6f4 v[134:137], v[128:133], v[8:13], v[134:137] cbsz:2 blgp:2
	v_mfma_f32_16x16x128_f8f6f4 v[204:207], v[128:133], v[44:49], v[204:207] cbsz:2 blgp:2
	v_mfma_f32_16x16x128_f8f6f4 v[138:141], v[128:133], v[20:25], v[138:141] cbsz:2 blgp:2
	v_mfma_f32_16x16x128_f8f6f4 v[208:211], v[128:133], v[56:61], v[208:211] cbsz:2 blgp:2
	v_mfma_f32_16x16x128_f8f6f4 v[142:145], v[128:133], v[32:37], v[142:145] cbsz:2 blgp:2
	v_mfma_f32_16x16x128_f8f6f4 v[212:215], v[128:133], v[68:73], v[212:215] cbsz:2 blgp:2
	v_cndmask_b32_e64 v158, v134, v204, s[0:1]
	v_fma_mix_f32 v158, v158, v100, v82 op_sel_hi:[0,0,1]
	v_exp_f32_e32 v158, v158
	v_cndmask_b32_e64 v159, v138, v208, s[0:1]
	v_fma_mix_f32 v159, v159, v101, v74 op_sel_hi:[0,0,1]
	v_exp_f32_e32 v159, v159
	v_fma_f32 v158, v158, v186, v186
	v_rcp_f32_e32 v158, v158
	v_add_f32_e32 v159, 1.0, v159
	v_rcp_f32_e32 v159, v159
	v_cndmask_b32_e64 v160, v142, v212, s[0:1]
	v_fma_mix_f32 v161, v158, v160, v78 op_sel_hi:[0,0,1]
	v_exp_f32_e32 v161, v161
	s_add_u32 s48, s48, s40
	v_add_f32_e32 v161, 1.0, v161
	v_rcp_f32_e32 v161, v161
	s_addc_u32 s49, s49, s41
	v_fma_f32 v162, v161, -2.0, 1.0
	v_sub_f32_e32 v163, v176, v162
	v_fma_f32 v176, v159, v163, v162
	v_fma_f32 v164, |v176|, s17, v113
	v_fma_f32 v165, |v176|, s18, v114
	v_fma_f32 v166, |v176|, s19, v115
	v_lshrrev_b32_e32 v167, 26, v176
	v_min3_u32 v164, v164, v165, v166
	v_bfi_b32 v168, 31, v164, v167
	global_store_short_d16_hi v185, v176, s[48:49]
	s_nop 0
	v_mul_u32_u24_dpp v170, v168, v180 quad_perm:[1,2,3,3] row_mask:0xf bank_mask:0xf bound_ctrl:1
	v_mad_u32_u24 v171, v168, v181, v170
	ds_write_b8_d16_hi v184, v171 offset:416
	s_barrier
	s_waitcnt lgkmcnt(0)
	s_barrier
	ds_read_b64 v[122:123], v105 offset:416
	ds_read_b64 v[124:125], v105 offset:424
	ds_read_b64 v[126:127], v105 offset:432
	ds_read_b64 v[128:129], v105 offset:512
	ds_read_b64 v[130:131], v105 offset:520
	ds_read_b64 v[132:133], v105 offset:528
	s_waitcnt lgkmcnt(3)
	v_mfma_f32_16x16x128_f8f6f4 v[134:137], v[122:127], v[2:7], 0 cbsz:2 blgp:2
	v_mfma_f32_16x16x128_f8f6f4 v[138:141], v[122:127], v[14:19], 0 cbsz:2 blgp:2
	v_mfma_f32_16x16x128_f8f6f4 v[142:145], v[122:127], v[26:31], v[188:191] cbsz:2 blgp:2
	v_mfma_f32_16x16x128_f8f6f4 v[204:207], v[122:127], v[38:43], 0 cbsz:2 blgp:2
	v_mfma_f32_16x16x128_f8f6f4 v[208:211], v[122:127], v[50:55], 0 cbsz:2 blgp:2
	v_mfma_f32_16x16x128_f8f6f4 v[212:215], v[122:127], v[62:67], v[188:191] cbsz:2 blgp:2
	s_waitcnt lgkmcnt(0)
	v_mfma_f32_16x16x128_f8f6f4 v[134:137], v[128:133], v[8:13], v[134:137] cbsz:2 blgp:2
	v_mfma_f32_16x16x128_f8f6f4 v[204:207], v[128:133], v[44:49], v[204:207] cbsz:2 blgp:2
	v_mfma_f32_16x16x128_f8f6f4 v[138:141], v[128:133], v[20:25], v[138:141] cbsz:2 blgp:2
	v_mfma_f32_16x16x128_f8f6f4 v[208:211], v[128:133], v[56:61], v[208:211] cbsz:2 blgp:2
	v_mfma_f32_16x16x128_f8f6f4 v[142:145], v[128:133], v[32:37], v[142:145] cbsz:2 blgp:2
	v_mfma_f32_16x16x128_f8f6f4 v[212:215], v[128:133], v[68:73], v[212:215] cbsz:2 blgp:2
	v_cndmask_b32_e64 v158, v134, v204, s[0:1]
	v_fma_mix_f32 v158, v158, v100, v82 op_sel:[0,0,1] op_sel_hi:[0,0,1]
	v_exp_f32_e32 v158, v158
	v_cndmask_b32_e64 v159, v138, v208, s[0:1]
	v_fma_mix_f32 v159, v159, v101, v74 op_sel:[0,0,1] op_sel_hi:[0,0,1]
	v_exp_f32_e32 v159, v159
	v_fma_f32 v158, v158, v186, v186
	v_rcp_f32_e32 v158, v158
	v_add_f32_e32 v159, 1.0, v159
	v_rcp_f32_e32 v159, v159
	v_cndmask_b32_e64 v160, v142, v212, s[0:1]
	v_fma_mix_f32 v161, v158, v160, v78 op_sel:[0,0,1] op_sel_hi:[0,0,1]
	v_exp_f32_e32 v161, v161
	s_add_u32 s48, s48, s40
	v_add_f32_e32 v161, 1.0, v161
	v_rcp_f32_e32 v161, v161
	s_addc_u32 s49, s49, s41
	v_fma_f32 v162, v161, -2.0, 1.0
	v_sub_f32_e32 v163, v176, v162
	v_fma_f32 v176, v159, v163, v162
	v_fma_f32 v164, |v176|, s17, v113
	v_fma_f32 v165, |v176|, s18, v114
	v_fma_f32 v166, |v176|, s19, v115
	v_lshrrev_b32_e32 v167, 26, v176
	v_min3_u32 v164, v164, v165, v166
	v_bfi_b32 v168, 31, v164, v167
	global_store_short_d16_hi v185, v176, s[48:49]
	s_nop 0
	v_mul_u32_u24_dpp v170, v168, v180 quad_perm:[1,2,3,3] row_mask:0xf bank_mask:0xf bound_ctrl:1
	v_mad_u32_u24 v171, v168, v181, v170
	ds_write_b8_d16_hi v184, v171
	s_barrier
	s_waitcnt lgkmcnt(0)
	s_barrier
	ds_read_b64 v[122:123], v105 offset:0
	ds_read_b64 v[124:125], v105 offset:8
	ds_read_b64 v[126:127], v105 offset:16
	ds_read_b64 v[128:129], v105 offset:96
	ds_read_b64 v[130:131], v105 offset:104
	ds_read_b64 v[132:133], v105 offset:112
	s_waitcnt lgkmcnt(3)
	v_mfma_f32_16x16x128_f8f6f4 v[134:137], v[122:127], v[2:7], 0 cbsz:2 blgp:2
	v_mfma_f32_16x16x128_f8f6f4 v[138:141], v[122:127], v[14:19], 0 cbsz:2 blgp:2
	v_mfma_f32_16x16x128_f8f6f4 v[142:145], v[122:127], v[26:31], v[188:191] cbsz:2 blgp:2
	v_mfma_f32_16x16x128_f8f6f4 v[204:207], v[122:127], v[38:43], 0 cbsz:2 blgp:2
	v_mfma_f32_16x16x128_f8f6f4 v[208:211], v[122:127], v[50:55], 0 cbsz:2 blgp:2
	v_mfma_f32_16x16x128_f8f6f4 v[212:215], v[122:127], v[62:67], v[188:191] cbsz:2 blgp:2
	s_waitcnt lgkmcnt(0)
	v_mfma_f32_16x16x128_f8f6f4 v[134:137], v[128:133], v[8:13], v[134:137] cbsz:2 blgp:2
	v_mfma_f32_16x16x128_f8f6f4 v[204:207], v[128:133], v[44:49], v[204:207] cbsz:2 blgp:2
	v_mfma_f32_16x16x128_f8f6f4 v[138:141], v[128:133], v[20:25], v[138:141] cbsz:2 blgp:2
	v_mfma_f32_16x16x128_f8f6f4 v[208:211], v[128:133], v[56:61], v[208:211] cbsz:2 blgp:2
	v_mfma_f32_16x16x128_f8f6f4 v[142:145], v[128:133], v[32:37], v[142:145] cbsz:2 blgp:2
	v_mfma_f32_16x16x128_f8f6f4 v[212:215], v[128:133], v[68:73], v[212:215] cbsz:2 blgp:2
	v_cndmask_b32_e64 v158, v134, v204, s[0:1]
	v_fma_mix_f32 v158, v158, v100, v83 op_sel_hi:[0,0,1]
	v_exp_f32_e32 v158, v158
	v_cndmask_b32_e64 v159, v138, v208, s[0:1]
	v_fma_mix_f32 v159, v159, v101, v75 op_sel_hi:[0,0,1]
	v_exp_f32_e32 v159, v159
	v_fma_f32 v158, v158, v186, v186
	v_rcp_f32_e32 v158, v158
	v_add_f32_e32 v159, 1.0, v159
	v_rcp_f32_e32 v159, v159
	v_cndmask_b32_e64 v160, v142, v212, s[0:1]
	v_fma_mix_f32 v161, v158, v160, v79 op_sel_hi:[0,0,1]
	v_exp_f32_e32 v161, v161
	s_add_u32 s48, s48, s40
	v_add_f32_e32 v161, 1.0, v161
	v_rcp_f32_e32 v161, v161
	s_addc_u32 s49, s49, s41
	v_fma_f32 v162, v161, -2.0, 1.0
	v_sub_f32_e32 v163, v176, v162
	v_fma_f32 v176, v159, v163, v162
	v_fma_f32 v164, |v176|, s17, v113
	v_fma_f32 v165, |v176|, s18, v114
	v_fma_f32 v166, |v176|, s19, v115
	v_lshrrev_b32_e32 v167, 26, v176
	v_min3_u32 v164, v164, v165, v166
	v_bfi_b32 v168, 31, v164, v167
	global_store_short_d16_hi v185, v176, s[48:49]
	s_nop 0
	v_mul_u32_u24_dpp v170, v168, v180 quad_perm:[1,2,3,3] row_mask:0xf bank_mask:0xf bound_ctrl:1
	v_mad_u32_u24 v171, v168, v181, v170
	ds_write_b8_d16_hi v184, v171 offset:416
	s_barrier
	s_waitcnt lgkmcnt(0)
	s_barrier
	ds_read_b64 v[122:123], v105 offset:416
	ds_read_b64 v[124:125], v105 offset:424
	ds_read_b64 v[126:127], v105 offset:432
	ds_read_b64 v[128:129], v105 offset:512
	ds_read_b64 v[130:131], v105 offset:520
	ds_read_b64 v[132:133], v105 offset:528
	s_waitcnt lgkmcnt(3)
	v_mfma_f32_16x16x128_f8f6f4 v[134:137], v[122:127], v[2:7], 0 cbsz:2 blgp:2
	v_mfma_f32_16x16x128_f8f6f4 v[138:141], v[122:127], v[14:19], 0 cbsz:2 blgp:2
	v_mfma_f32_16x16x128_f8f6f4 v[142:145], v[122:127], v[26:31], v[188:191] cbsz:2 blgp:2
	v_mfma_f32_16x16x128_f8f6f4 v[204:207], v[122:127], v[38:43], 0 cbsz:2 blgp:2
	v_mfma_f32_16x16x128_f8f6f4 v[208:211], v[122:127], v[50:55], 0 cbsz:2 blgp:2
	v_mfma_f32_16x16x128_f8f6f4 v[212:215], v[122:127], v[62:67], v[188:191] cbsz:2 blgp:2
	s_waitcnt lgkmcnt(0)
	v_mfma_f32_16x16x128_f8f6f4 v[134:137], v[128:133], v[8:13], v[134:137] cbsz:2 blgp:2
	v_mfma_f32_16x16x128_f8f6f4 v[204:207], v[128:133], v[44:49], v[204:207] cbsz:2 blgp:2
	v_mfma_f32_16x16x128_f8f6f4 v[138:141], v[128:133], v[20:25], v[138:141] cbsz:2 blgp:2
	v_mfma_f32_16x16x128_f8f6f4 v[208:211], v[128:133], v[56:61], v[208:211] cbsz:2 blgp:2
	v_mfma_f32_16x16x128_f8f6f4 v[142:145], v[128:133], v[32:37], v[142:145] cbsz:2 blgp:2
	v_mfma_f32_16x16x128_f8f6f4 v[212:215], v[128:133], v[68:73], v[212:215] cbsz:2 blgp:2
	v_cndmask_b32_e64 v158, v134, v204, s[0:1]
	v_fma_mix_f32 v158, v158, v100, v83 op_sel:[0,0,1] op_sel_hi:[0,0,1]
	v_exp_f32_e32 v158, v158
	v_cndmask_b32_e64 v159, v138, v208, s[0:1]
	v_fma_mix_f32 v159, v159, v101, v75 op_sel:[0,0,1] op_sel_hi:[0,0,1]
	v_exp_f32_e32 v159, v159
	v_fma_f32 v158, v158, v186, v186
	v_rcp_f32_e32 v158, v158
	v_add_f32_e32 v159, 1.0, v159
	v_rcp_f32_e32 v159, v159
	v_cndmask_b32_e64 v160, v142, v212, s[0:1]
	v_fma_mix_f32 v161, v158, v160, v79 op_sel:[0,0,1] op_sel_hi:[0,0,1]
	v_exp_f32_e32 v161, v161
	s_add_u32 s48, s48, s40
	v_add_f32_e32 v161, 1.0, v161
	v_rcp_f32_e32 v161, v161
	s_addc_u32 s49, s49, s41
	v_fma_f32 v162, v161, -2.0, 1.0
	v_sub_f32_e32 v163, v176, v162
	v_fma_f32 v176, v159, v163, v162
	v_fma_f32 v164, |v176|, s17, v113
	v_fma_f32 v165, |v176|, s18, v114
	v_fma_f32 v166, |v176|, s19, v115
	v_lshrrev_b32_e32 v167, 26, v176
	v_min3_u32 v164, v164, v165, v166
	v_bfi_b32 v168, 31, v164, v167
	global_store_short_d16_hi v185, v176, s[48:49]
	s_nop 0
	v_mul_u32_u24_dpp v170, v168, v180 quad_perm:[1,2,3,3] row_mask:0xf bank_mask:0xf bound_ctrl:1
	v_mad_u32_u24 v171, v168, v181, v170
	ds_write_b8_d16_hi v184, v171
	s_barrier
	s_waitcnt lgkmcnt(0)
	s_barrier
	ds_read_b64 v[122:123], v105 offset:0
	ds_read_b64 v[124:125], v105 offset:8
	ds_read_b64 v[126:127], v105 offset:16
	ds_read_b64 v[128:129], v105 offset:96
	ds_read_b64 v[130:131], v105 offset:104
	ds_read_b64 v[132:133], v105 offset:112
	s_waitcnt lgkmcnt(3)
	v_mfma_f32_16x16x128_f8f6f4 v[134:137], v[122:127], v[2:7], 0 cbsz:2 blgp:2
	v_mfma_f32_16x16x128_f8f6f4 v[138:141], v[122:127], v[14:19], 0 cbsz:2 blgp:2
	v_mfma_f32_16x16x128_f8f6f4 v[142:145], v[122:127], v[26:31], v[188:191] cbsz:2 blgp:2
	v_mfma_f32_16x16x128_f8f6f4 v[204:207], v[122:127], v[38:43], 0 cbsz:2 blgp:2
	v_mfma_f32_16x16x128_f8f6f4 v[208:211], v[122:127], v[50:55], 0 cbsz:2 blgp:2
	v_mfma_f32_16x16x128_f8f6f4 v[212:215], v[122:127], v[62:67], v[188:191] cbsz:2 blgp:2
	s_waitcnt lgkmcnt(0)
	v_mfma_f32_16x16x128_f8f6f4 v[134:137], v[128:133], v[8:13], v[134:137] cbsz:2 blgp:2
	v_mfma_f32_16x16x128_f8f6f4 v[204:207], v[128:133], v[44:49], v[204:207] cbsz:2 blgp:2
	v_mfma_f32_16x16x128_f8f6f4 v[138:141], v[128:133], v[20:25], v[138:141] cbsz:2 blgp:2
	v_mfma_f32_16x16x128_f8f6f4 v[208:211], v[128:133], v[56:61], v[208:211] cbsz:2 blgp:2
	v_mfma_f32_16x16x128_f8f6f4 v[142:145], v[128:133], v[32:37], v[142:145] cbsz:2 blgp:2
	v_mfma_f32_16x16x128_f8f6f4 v[212:215], v[128:133], v[68:73], v[212:215] cbsz:2 blgp:2
	v_cndmask_b32_e64 v158, v134, v204, s[0:1]
	v_fma_mix_f32 v158, v158, v100, v84 op_sel_hi:[0,0,1]
	v_exp_f32_e32 v158, v158
	v_cndmask_b32_e64 v159, v138, v208, s[0:1]
	v_fma_mix_f32 v159, v159, v101, v76 op_sel_hi:[0,0,1]
	v_exp_f32_e32 v159, v159
	v_fma_f32 v158, v158, v186, v186
	v_rcp_f32_e32 v158, v158
	v_add_f32_e32 v159, 1.0, v159
	v_rcp_f32_e32 v159, v159
	v_cndmask_b32_e64 v160, v142, v212, s[0:1]
	v_fma_mix_f32 v161, v158, v160, v80 op_sel_hi:[0,0,1]
	v_exp_f32_e32 v161, v161
	s_add_u32 s48, s48, s40
	v_add_f32_e32 v161, 1.0, v161
	v_rcp_f32_e32 v161, v161
	s_addc_u32 s49, s49, s41
	v_fma_f32 v162, v161, -2.0, 1.0
	v_sub_f32_e32 v163, v176, v162
	v_fma_f32 v176, v159, v163, v162
	v_fma_f32 v164, |v176|, s17, v113
	v_fma_f32 v165, |v176|, s18, v114
	v_fma_f32 v166, |v176|, s19, v115
	v_lshrrev_b32_e32 v167, 26, v176
	v_min3_u32 v164, v164, v165, v166
	v_bfi_b32 v168, 31, v164, v167
	global_store_short_d16_hi v185, v176, s[48:49]
	s_nop 0
	v_mul_u32_u24_dpp v170, v168, v180 quad_perm:[1,2,3,3] row_mask:0xf bank_mask:0xf bound_ctrl:1
	v_mad_u32_u24 v171, v168, v181, v170
	ds_write_b8_d16_hi v184, v171 offset:416
	s_barrier
	s_waitcnt lgkmcnt(0)
	s_barrier
	ds_read_b64 v[122:123], v105 offset:416
	ds_read_b64 v[124:125], v105 offset:424
	ds_read_b64 v[126:127], v105 offset:432
	ds_read_b64 v[128:129], v105 offset:512
	ds_read_b64 v[130:131], v105 offset:520
	ds_read_b64 v[132:133], v105 offset:528
	s_waitcnt lgkmcnt(3)
	v_mfma_f32_16x16x128_f8f6f4 v[134:137], v[122:127], v[2:7], 0 cbsz:2 blgp:2
	v_mfma_f32_16x16x128_f8f6f4 v[138:141], v[122:127], v[14:19], 0 cbsz:2 blgp:2
	v_mfma_f32_16x16x128_f8f6f4 v[142:145], v[122:127], v[26:31], v[188:191] cbsz:2 blgp:2
	v_mfma_f32_16x16x128_f8f6f4 v[204:207], v[122:127], v[38:43], 0 cbsz:2 blgp:2
	v_mfma_f32_16x16x128_f8f6f4 v[208:211], v[122:127], v[50:55], 0 cbsz:2 blgp:2
	v_mfma_f32_16x16x128_f8f6f4 v[212:215], v[122:127], v[62:67], v[188:191] cbsz:2 blgp:2
	s_waitcnt lgkmcnt(0)
	v_mfma_f32_16x16x128_f8f6f4 v[134:137], v[128:133], v[8:13], v[134:137] cbsz:2 blgp:2
	v_mfma_f32_16x16x128_f8f6f4 v[204:207], v[128:133], v[44:49], v[204:207] cbsz:2 blgp:2
	v_mfma_f32_16x16x128_f8f6f4 v[138:141], v[128:133], v[20:25], v[138:141] cbsz:2 blgp:2
	v_mfma_f32_16x16x128_f8f6f4 v[208:211], v[128:133], v[56:61], v[208:211] cbsz:2 blgp:2
	v_mfma_f32_16x16x128_f8f6f4 v[142:145], v[128:133], v[32:37], v[142:145] cbsz:2 blgp:2
	v_mfma_f32_16x16x128_f8f6f4 v[212:215], v[128:133], v[68:73], v[212:215] cbsz:2 blgp:2
	v_cndmask_b32_e64 v158, v134, v204, s[0:1]
	v_fma_mix_f32 v158, v158, v100, v84 op_sel:[0,0,1] op_sel_hi:[0,0,1]
	v_exp_f32_e32 v158, v158
	v_cndmask_b32_e64 v159, v138, v208, s[0:1]
	v_fma_mix_f32 v159, v159, v101, v76 op_sel:[0,0,1] op_sel_hi:[0,0,1]
	v_exp_f32_e32 v159, v159
	v_fma_f32 v158, v158, v186, v186
	v_rcp_f32_e32 v158, v158
	v_add_f32_e32 v159, 1.0, v159
	v_rcp_f32_e32 v159, v159
	v_cndmask_b32_e64 v160, v142, v212, s[0:1]
	v_fma_mix_f32 v161, v158, v160, v80 op_sel:[0,0,1] op_sel_hi:[0,0,1]
	v_exp_f32_e32 v161, v161
	s_add_u32 s48, s48, s40
	v_add_f32_e32 v161, 1.0, v161
	v_rcp_f32_e32 v161, v161
	s_addc_u32 s49, s49, s41
	v_fma_f32 v162, v161, -2.0, 1.0
	v_sub_f32_e32 v163, v176, v162
	v_fma_f32 v176, v159, v163, v162
	v_fma_f32 v164, |v176|, s17, v113
	v_fma_f32 v165, |v176|, s18, v114
	v_fma_f32 v166, |v176|, s19, v115
	v_lshrrev_b32_e32 v167, 26, v176
	v_min3_u32 v164, v164, v165, v166
	v_bfi_b32 v168, 31, v164, v167
	global_store_short_d16_hi v185, v176, s[48:49]
	s_nop 0
	v_mul_u32_u24_dpp v170, v168, v180 quad_perm:[1,2,3,3] row_mask:0xf bank_mask:0xf bound_ctrl:1
	v_mad_u32_u24 v171, v168, v181, v170
	ds_write_b8_d16_hi v184, v171
	s_barrier
	s_waitcnt lgkmcnt(0)
	s_barrier
	ds_read_b64 v[122:123], v105 offset:0
	ds_read_b64 v[124:125], v105 offset:8
	ds_read_b64 v[126:127], v105 offset:16
	ds_read_b64 v[128:129], v105 offset:96
	ds_read_b64 v[130:131], v105 offset:104
	ds_read_b64 v[132:133], v105 offset:112
	s_waitcnt lgkmcnt(3)
	v_mfma_f32_16x16x128_f8f6f4 v[134:137], v[122:127], v[2:7], 0 cbsz:2 blgp:2
	v_mfma_f32_16x16x128_f8f6f4 v[138:141], v[122:127], v[14:19], 0 cbsz:2 blgp:2
	v_mfma_f32_16x16x128_f8f6f4 v[142:145], v[122:127], v[26:31], v[188:191] cbsz:2 blgp:2
	v_mfma_f32_16x16x128_f8f6f4 v[204:207], v[122:127], v[38:43], 0 cbsz:2 blgp:2
	v_mfma_f32_16x16x128_f8f6f4 v[208:211], v[122:127], v[50:55], 0 cbsz:2 blgp:2
	v_mfma_f32_16x16x128_f8f6f4 v[212:215], v[122:127], v[62:67], v[188:191] cbsz:2 blgp:2
	s_waitcnt lgkmcnt(0)
	v_mfma_f32_16x16x128_f8f6f4 v[134:137], v[128:133], v[8:13], v[134:137] cbsz:2 blgp:2
	v_mfma_f32_16x16x128_f8f6f4 v[204:207], v[128:133], v[44:49], v[204:207] cbsz:2 blgp:2
	v_mfma_f32_16x16x128_f8f6f4 v[138:141], v[128:133], v[20:25], v[138:141] cbsz:2 blgp:2
	v_mfma_f32_16x16x128_f8f6f4 v[208:211], v[128:133], v[56:61], v[208:211] cbsz:2 blgp:2
	v_mfma_f32_16x16x128_f8f6f4 v[142:145], v[128:133], v[32:37], v[142:145] cbsz:2 blgp:2
	v_mfma_f32_16x16x128_f8f6f4 v[212:215], v[128:133], v[68:73], v[212:215] cbsz:2 blgp:2
	v_cndmask_b32_e64 v158, v134, v204, s[0:1]
	v_fma_mix_f32 v158, v158, v100, v85 op_sel_hi:[0,0,1]
	v_exp_f32_e32 v158, v158
	v_cndmask_b32_e64 v159, v138, v208, s[0:1]
	v_fma_mix_f32 v159, v159, v101, v77 op_sel_hi:[0,0,1]
	v_exp_f32_e32 v159, v159
	v_fma_f32 v158, v158, v186, v186
	v_rcp_f32_e32 v158, v158
	v_add_f32_e32 v159, 1.0, v159
	v_rcp_f32_e32 v159, v159
	v_cndmask_b32_e64 v160, v142, v212, s[0:1]
	v_fma_mix_f32 v161, v158, v160, v81 op_sel_hi:[0,0,1]
	v_exp_f32_e32 v161, v161
	s_add_u32 s48, s48, s40
	v_add_f32_e32 v161, 1.0, v161
	v_rcp_f32_e32 v161, v161
	s_addc_u32 s49, s49, s41
	v_fma_f32 v162, v161, -2.0, 1.0
	v_sub_f32_e32 v163, v176, v162
	v_fma_f32 v176, v159, v163, v162
	v_fma_f32 v164, |v176|, s17, v113
	v_fma_f32 v165, |v176|, s18, v114
	v_fma_f32 v166, |v176|, s19, v115
	v_lshrrev_b32_e32 v167, 26, v176
	v_min3_u32 v164, v164, v165, v166
	v_bfi_b32 v168, 31, v164, v167
	global_store_short_d16_hi v185, v176, s[48:49]
	s_nop 0
	v_mul_u32_u24_dpp v170, v168, v180 quad_perm:[1,2,3,3] row_mask:0xf bank_mask:0xf bound_ctrl:1
	v_mad_u32_u24 v171, v168, v181, v170
	ds_write_b8_d16_hi v184, v171 offset:416
	s_barrier
	s_waitcnt lgkmcnt(0)
	s_barrier
	ds_read_b64 v[122:123], v105 offset:416
	ds_read_b64 v[124:125], v105 offset:424
	ds_read_b64 v[126:127], v105 offset:432
	ds_read_b64 v[128:129], v105 offset:512
	ds_read_b64 v[130:131], v105 offset:520
	ds_read_b64 v[132:133], v105 offset:528
	s_waitcnt lgkmcnt(3)
	v_mfma_f32_16x16x128_f8f6f4 v[134:137], v[122:127], v[2:7], 0 cbsz:2 blgp:2
	v_mfma_f32_16x16x128_f8f6f4 v[138:141], v[122:127], v[14:19], 0 cbsz:2 blgp:2
	v_mfma_f32_16x16x128_f8f6f4 v[142:145], v[122:127], v[26:31], v[188:191] cbsz:2 blgp:2
	v_mfma_f32_16x16x128_f8f6f4 v[204:207], v[122:127], v[38:43], 0 cbsz:2 blgp:2
	v_mfma_f32_16x16x128_f8f6f4 v[208:211], v[122:127], v[50:55], 0 cbsz:2 blgp:2
	v_mfma_f32_16x16x128_f8f6f4 v[212:215], v[122:127], v[62:67], v[188:191] cbsz:2 blgp:2
	s_waitcnt lgkmcnt(0)
	v_mfma_f32_16x16x128_f8f6f4 v[134:137], v[128:133], v[8:13], v[134:137] cbsz:2 blgp:2
	v_mfma_f32_16x16x128_f8f6f4 v[204:207], v[128:133], v[44:49], v[204:207] cbsz:2 blgp:2
	v_mfma_f32_16x16x128_f8f6f4 v[138:141], v[128:133], v[20:25], v[138:141] cbsz:2 blgp:2
	v_mfma_f32_16x16x128_f8f6f4 v[208:211], v[128:133], v[56:61], v[208:211] cbsz:2 blgp:2
	v_mfma_f32_16x16x128_f8f6f4 v[142:145], v[128:133], v[32:37], v[142:145] cbsz:2 blgp:2
	v_mfma_f32_16x16x128_f8f6f4 v[212:215], v[128:133], v[68:73], v[212:215] cbsz:2 blgp:2
	v_cndmask_b32_e64 v158, v134, v204, s[0:1]
	v_fma_mix_f32 v158, v158, v100, v85 op_sel:[0,0,1] op_sel_hi:[0,0,1]
	v_exp_f32_e32 v158, v158
	v_cndmask_b32_e64 v159, v138, v208, s[0:1]
	v_fma_mix_f32 v159, v159, v101, v77 op_sel:[0,0,1] op_sel_hi:[0,0,1]
	v_exp_f32_e32 v159, v159
	v_fma_f32 v158, v158, v186, v186
	v_rcp_f32_e32 v158, v158
	v_add_f32_e32 v159, 1.0, v159
	v_rcp_f32_e32 v159, v159
	v_cndmask_b32_e64 v160, v142, v212, s[0:1]
	v_fma_mix_f32 v161, v158, v160, v81 op_sel:[0,0,1] op_sel_hi:[0,0,1]
	v_exp_f32_e32 v161, v161
	s_add_u32 s48, s48, s40
	v_add_f32_e32 v161, 1.0, v161
	v_rcp_f32_e32 v161, v161
	s_addc_u32 s49, s49, s41
	v_fma_f32 v162, v161, -2.0, 1.0
	v_sub_f32_e32 v163, v176, v162
	v_fma_f32 v176, v159, v163, v162
	v_fma_f32 v164, |v176|, s17, v113
	v_fma_f32 v165, |v176|, s18, v114
	v_fma_f32 v166, |v176|, s19, v115
	v_lshrrev_b32_e32 v167, 26, v176
	v_min3_u32 v164, v164, v165, v166
	v_bfi_b32 v168, 31, v164, v167
	global_store_short_d16_hi v185, v176, s[48:49]
	s_nop 0
	v_mul_u32_u24_dpp v170, v168, v180 quad_perm:[1,2,3,3] row_mask:0xf bank_mask:0xf bound_ctrl:1
	v_mad_u32_u24 v171, v168, v181, v170
	ds_write_b8_d16_hi v184, v171
	s_barrier
	s_waitcnt lgkmcnt(0)
	s_barrier
	ds_read_b64 v[122:123], v105 offset:0
	ds_read_b64 v[124:125], v105 offset:8
	ds_read_b64 v[126:127], v105 offset:16
	ds_read_b64 v[128:129], v105 offset:96
	ds_read_b64 v[130:131], v105 offset:104
	ds_read_b64 v[132:133], v105 offset:112
	s_waitcnt vmcnt(8)
	global_load_dwordx4 v[82:85], v[196:197], off
	global_load_dwordx4 v[74:77], v[196:197], off offset:512
	global_load_dwordx4 v[78:81], v[196:197], off offset:1024
	v_lshl_add_u64 v[196:197], v[196:197], 0, s[42:43]
	s_waitcnt lgkmcnt(3)
	v_mfma_f32_16x16x128_f8f6f4 v[134:137], v[122:127], v[2:7], 0 cbsz:2 blgp:2
	v_mfma_f32_16x16x128_f8f6f4 v[138:141], v[122:127], v[14:19], 0 cbsz:2 blgp:2
	v_mfma_f32_16x16x128_f8f6f4 v[142:145], v[122:127], v[26:31], v[188:191] cbsz:2 blgp:2
	v_mfma_f32_16x16x128_f8f6f4 v[204:207], v[122:127], v[38:43], 0 cbsz:2 blgp:2
	v_mfma_f32_16x16x128_f8f6f4 v[208:211], v[122:127], v[50:55], 0 cbsz:2 blgp:2
	v_mfma_f32_16x16x128_f8f6f4 v[212:215], v[122:127], v[62:67], v[188:191] cbsz:2 blgp:2
	s_waitcnt lgkmcnt(0)
	v_mfma_f32_16x16x128_f8f6f4 v[134:137], v[128:133], v[8:13], v[134:137] cbsz:2 blgp:2
	v_mfma_f32_16x16x128_f8f6f4 v[204:207], v[128:133], v[44:49], v[204:207] cbsz:2 blgp:2
	v_mfma_f32_16x16x128_f8f6f4 v[138:141], v[128:133], v[20:25], v[138:141] cbsz:2 blgp:2
	v_mfma_f32_16x16x128_f8f6f4 v[208:211], v[128:133], v[56:61], v[208:211] cbsz:2 blgp:2
	v_mfma_f32_16x16x128_f8f6f4 v[142:145], v[128:133], v[32:37], v[142:145] cbsz:2 blgp:2
	v_mfma_f32_16x16x128_f8f6f4 v[212:215], v[128:133], v[68:73], v[212:215] cbsz:2 blgp:2
	v_cndmask_b32_e64 v158, v134, v204, s[0:1]
	v_fma_mix_f32 v158, v158, v100, v146 op_sel_hi:[0,0,1]
	v_exp_f32_e32 v158, v158
	v_cndmask_b32_e64 v159, v138, v208, s[0:1]
	v_fma_mix_f32 v159, v159, v101, v150 op_sel_hi:[0,0,1]
	v_exp_f32_e32 v159, v159
	v_fma_f32 v158, v158, v186, v186
	v_rcp_f32_e32 v158, v158
	v_add_f32_e32 v159, 1.0, v159
	v_rcp_f32_e32 v159, v159
	v_cndmask_b32_e64 v160, v142, v212, s[0:1]
	v_fma_mix_f32 v161, v158, v160, v154 op_sel_hi:[0,0,1]
	v_exp_f32_e32 v161, v161
	s_add_u32 s48, s48, s40
	v_add_f32_e32 v161, 1.0, v161
	v_rcp_f32_e32 v161, v161
	s_addc_u32 s49, s49, s41
	v_fma_f32 v162, v161, -2.0, 1.0
	v_sub_f32_e32 v163, v176, v162
	v_fma_f32 v176, v159, v163, v162
	v_fma_f32 v164, |v176|, s17, v113
	v_fma_f32 v165, |v176|, s18, v114
	v_fma_f32 v166, |v176|, s19, v115
	v_lshrrev_b32_e32 v167, 26, v176
	v_min3_u32 v164, v164, v165, v166
	v_bfi_b32 v168, 31, v164, v167
	global_store_short_d16_hi v185, v176, s[48:49]
	s_nop 0
	v_mul_u32_u24_dpp v170, v168, v180 quad_perm:[1,2,3,3] row_mask:0xf bank_mask:0xf bound_ctrl:1
	v_mad_u32_u24 v171, v168, v181, v170
	ds_write_b8_d16_hi v184, v171 offset:416
	s_barrier
	s_waitcnt lgkmcnt(0)
	s_barrier
	ds_read_b64 v[122:123], v105 offset:416
	ds_read_b64 v[124:125], v105 offset:424
	ds_read_b64 v[126:127], v105 offset:432
	ds_read_b64 v[128:129], v105 offset:512
	ds_read_b64 v[130:131], v105 offset:520
	ds_read_b64 v[132:133], v105 offset:528
	s_waitcnt lgkmcnt(3)
	v_mfma_f32_16x16x128_f8f6f4 v[134:137], v[122:127], v[2:7], 0 cbsz:2 blgp:2
	v_mfma_f32_16x16x128_f8f6f4 v[138:141], v[122:127], v[14:19], 0 cbsz:2 blgp:2
	v_mfma_f32_16x16x128_f8f6f4 v[142:145], v[122:127], v[26:31], v[188:191] cbsz:2 blgp:2
	v_mfma_f32_16x16x128_f8f6f4 v[204:207], v[122:127], v[38:43], 0 cbsz:2 blgp:2
	v_mfma_f32_16x16x128_f8f6f4 v[208:211], v[122:127], v[50:55], 0 cbsz:2 blgp:2
	v_mfma_f32_16x16x128_f8f6f4 v[212:215], v[122:127], v[62:67], v[188:191] cbsz:2 blgp:2
	s_waitcnt lgkmcnt(0)
	v_mfma_f32_16x16x128_f8f6f4 v[134:137], v[128:133], v[8:13], v[134:137] cbsz:2 blgp:2
	v_mfma_f32_16x16x128_f8f6f4 v[204:207], v[128:133], v[44:49], v[204:207] cbsz:2 blgp:2
	v_mfma_f32_16x16x128_f8f6f4 v[138:141], v[128:133], v[20:25], v[138:141] cbsz:2 blgp:2
	v_mfma_f32_16x16x128_f8f6f4 v[208:211], v[128:133], v[56:61], v[208:211] cbsz:2 blgp:2
	v_mfma_f32_16x16x128_f8f6f4 v[142:145], v[128:133], v[32:37], v[142:145] cbsz:2 blgp:2
	v_mfma_f32_16x16x128_f8f6f4 v[212:215], v[128:133], v[68:73], v[212:215] cbsz:2 blgp:2
	v_cndmask_b32_e64 v158, v134, v204, s[0:1]
	v_fma_mix_f32 v158, v158, v100, v146 op_sel:[0,0,1] op_sel_hi:[0,0,1]
	v_exp_f32_e32 v158, v158
	v_cndmask_b32_e64 v159, v138, v208, s[0:1]
	v_fma_mix_f32 v159, v159, v101, v150 op_sel:[0,0,1] op_sel_hi:[0,0,1]
	v_exp_f32_e32 v159, v159
	v_fma_f32 v158, v158, v186, v186
	v_rcp_f32_e32 v158, v158
	v_add_f32_e32 v159, 1.0, v159
	v_rcp_f32_e32 v159, v159
	v_cndmask_b32_e64 v160, v142, v212, s[0:1]
	v_fma_mix_f32 v161, v158, v160, v154 op_sel:[0,0,1] op_sel_hi:[0,0,1]
	v_exp_f32_e32 v161, v161
	s_add_u32 s48, s48, s40
	v_add_f32_e32 v161, 1.0, v161
	v_rcp_f32_e32 v161, v161
	s_addc_u32 s49, s49, s41
	v_fma_f32 v162, v161, -2.0, 1.0
	v_sub_f32_e32 v163, v176, v162
	v_fma_f32 v176, v159, v163, v162
	v_fma_f32 v164, |v176|, s17, v113
	v_fma_f32 v165, |v176|, s18, v114
	v_fma_f32 v166, |v176|, s19, v115
	v_lshrrev_b32_e32 v167, 26, v176
	v_min3_u32 v164, v164, v165, v166
	v_bfi_b32 v168, 31, v164, v167
	global_store_short_d16_hi v185, v176, s[48:49]
	s_nop 0
	v_mul_u32_u24_dpp v170, v168, v180 quad_perm:[1,2,3,3] row_mask:0xf bank_mask:0xf bound_ctrl:1
	v_mad_u32_u24 v171, v168, v181, v170
	ds_write_b8_d16_hi v184, v171
	s_barrier
	s_waitcnt lgkmcnt(0)
	s_barrier
	ds_read_b64 v[122:123], v105 offset:0
	ds_read_b64 v[124:125], v105 offset:8
	ds_read_b64 v[126:127], v105 offset:16
	ds_read_b64 v[128:129], v105 offset:96
	ds_read_b64 v[130:131], v105 offset:104
	ds_read_b64 v[132:133], v105 offset:112
	s_waitcnt lgkmcnt(3)
	v_mfma_f32_16x16x128_f8f6f4 v[134:137], v[122:127], v[2:7], 0 cbsz:2 blgp:2
	v_mfma_f32_16x16x128_f8f6f4 v[138:141], v[122:127], v[14:19], 0 cbsz:2 blgp:2
	v_mfma_f32_16x16x128_f8f6f4 v[142:145], v[122:127], v[26:31], v[188:191] cbsz:2 blgp:2
	v_mfma_f32_16x16x128_f8f6f4 v[204:207], v[122:127], v[38:43], 0 cbsz:2 blgp:2
	v_mfma_f32_16x16x128_f8f6f4 v[208:211], v[122:127], v[50:55], 0 cbsz:2 blgp:2
	v_mfma_f32_16x16x128_f8f6f4 v[212:215], v[122:127], v[62:67], v[188:191] cbsz:2 blgp:2
	s_waitcnt lgkmcnt(0)
	v_mfma_f32_16x16x128_f8f6f4 v[134:137], v[128:133], v[8:13], v[134:137] cbsz:2 blgp:2
	v_mfma_f32_16x16x128_f8f6f4 v[204:207], v[128:133], v[44:49], v[204:207] cbsz:2 blgp:2
	v_mfma_f32_16x16x128_f8f6f4 v[138:141], v[128:133], v[20:25], v[138:141] cbsz:2 blgp:2
	v_mfma_f32_16x16x128_f8f6f4 v[208:211], v[128:133], v[56:61], v[208:211] cbsz:2 blgp:2
	v_mfma_f32_16x16x128_f8f6f4 v[142:145], v[128:133], v[32:37], v[142:145] cbsz:2 blgp:2
	v_mfma_f32_16x16x128_f8f6f4 v[212:215], v[128:133], v[68:73], v[212:215] cbsz:2 blgp:2
	v_cndmask_b32_e64 v158, v134, v204, s[0:1]
	v_fma_mix_f32 v158, v158, v100, v147 op_sel_hi:[0,0,1]
	v_exp_f32_e32 v158, v158
	v_cndmask_b32_e64 v159, v138, v208, s[0:1]
	v_fma_mix_f32 v159, v159, v101, v151 op_sel_hi:[0,0,1]
	v_exp_f32_e32 v159, v159
	v_fma_f32 v158, v158, v186, v186
	v_rcp_f32_e32 v158, v158
	v_add_f32_e32 v159, 1.0, v159
	v_rcp_f32_e32 v159, v159
	v_cndmask_b32_e64 v160, v142, v212, s[0:1]
	v_fma_mix_f32 v161, v158, v160, v155 op_sel_hi:[0,0,1]
	v_exp_f32_e32 v161, v161
	s_add_u32 s48, s48, s40
	v_add_f32_e32 v161, 1.0, v161
	v_rcp_f32_e32 v161, v161
	s_addc_u32 s49, s49, s41
	v_fma_f32 v162, v161, -2.0, 1.0
	v_sub_f32_e32 v163, v176, v162
	v_fma_f32 v176, v159, v163, v162
	v_fma_f32 v164, |v176|, s17, v113
	v_fma_f32 v165, |v176|, s18, v114
	v_fma_f32 v166, |v176|, s19, v115
	v_lshrrev_b32_e32 v167, 26, v176
	v_min3_u32 v164, v164, v165, v166
	v_bfi_b32 v168, 31, v164, v167
	global_store_short_d16_hi v185, v176, s[48:49]
	s_nop 0
	v_mul_u32_u24_dpp v170, v168, v180 quad_perm:[1,2,3,3] row_mask:0xf bank_mask:0xf bound_ctrl:1
	v_mad_u32_u24 v171, v168, v181, v170
	ds_write_b8_d16_hi v184, v171 offset:416
	s_barrier
	s_waitcnt lgkmcnt(0)
	s_barrier
	ds_read_b64 v[122:123], v105 offset:416
	ds_read_b64 v[124:125], v105 offset:424
	ds_read_b64 v[126:127], v105 offset:432
	ds_read_b64 v[128:129], v105 offset:512
	ds_read_b64 v[130:131], v105 offset:520
	ds_read_b64 v[132:133], v105 offset:528
	s_waitcnt lgkmcnt(3)
	v_mfma_f32_16x16x128_f8f6f4 v[134:137], v[122:127], v[2:7], 0 cbsz:2 blgp:2
	v_mfma_f32_16x16x128_f8f6f4 v[138:141], v[122:127], v[14:19], 0 cbsz:2 blgp:2
	v_mfma_f32_16x16x128_f8f6f4 v[142:145], v[122:127], v[26:31], v[188:191] cbsz:2 blgp:2
	v_mfma_f32_16x16x128_f8f6f4 v[204:207], v[122:127], v[38:43], 0 cbsz:2 blgp:2
	v_mfma_f32_16x16x128_f8f6f4 v[208:211], v[122:127], v[50:55], 0 cbsz:2 blgp:2
	v_mfma_f32_16x16x128_f8f6f4 v[212:215], v[122:127], v[62:67], v[188:191] cbsz:2 blgp:2
	s_waitcnt lgkmcnt(0)
	v_mfma_f32_16x16x128_f8f6f4 v[134:137], v[128:133], v[8:13], v[134:137] cbsz:2 blgp:2
	v_mfma_f32_16x16x128_f8f6f4 v[204:207], v[128:133], v[44:49], v[204:207] cbsz:2 blgp:2
	v_mfma_f32_16x16x128_f8f6f4 v[138:141], v[128:133], v[20:25], v[138:141] cbsz:2 blgp:2
	v_mfma_f32_16x16x128_f8f6f4 v[208:211], v[128:133], v[56:61], v[208:211] cbsz:2 blgp:2
	v_mfma_f32_16x16x128_f8f6f4 v[142:145], v[128:133], v[32:37], v[142:145] cbsz:2 blgp:2
	v_mfma_f32_16x16x128_f8f6f4 v[212:215], v[128:133], v[68:73], v[212:215] cbsz:2 blgp:2
	v_cndmask_b32_e64 v158, v134, v204, s[0:1]
	v_fma_mix_f32 v158, v158, v100, v147 op_sel:[0,0,1] op_sel_hi:[0,0,1]
	v_exp_f32_e32 v158, v158
	v_cndmask_b32_e64 v159, v138, v208, s[0:1]
	v_fma_mix_f32 v159, v159, v101, v151 op_sel:[0,0,1] op_sel_hi:[0,0,1]
	v_exp_f32_e32 v159, v159
	v_fma_f32 v158, v158, v186, v186
	v_rcp_f32_e32 v158, v158
	v_add_f32_e32 v159, 1.0, v159
	v_rcp_f32_e32 v159, v159
	v_cndmask_b32_e64 v160, v142, v212, s[0:1]
	v_fma_mix_f32 v161, v158, v160, v155 op_sel:[0,0,1] op_sel_hi:[0,0,1]
	v_exp_f32_e32 v161, v161
	s_add_u32 s48, s48, s40
	v_add_f32_e32 v161, 1.0, v161
	v_rcp_f32_e32 v161, v161
	s_addc_u32 s49, s49, s41
	v_fma_f32 v162, v161, -2.0, 1.0
	v_sub_f32_e32 v163, v176, v162
	v_fma_f32 v176, v159, v163, v162
	v_fma_f32 v164, |v176|, s17, v113
	v_fma_f32 v165, |v176|, s18, v114
	v_fma_f32 v166, |v176|, s19, v115
	v_lshrrev_b32_e32 v167, 26, v176
	v_min3_u32 v164, v164, v165, v166
	v_bfi_b32 v168, 31, v164, v167
	global_store_short_d16_hi v185, v176, s[48:49]
	s_nop 0
	v_mul_u32_u24_dpp v170, v168, v180 quad_perm:[1,2,3,3] row_mask:0xf bank_mask:0xf bound_ctrl:1
	v_mad_u32_u24 v171, v168, v181, v170
	ds_write_b8_d16_hi v184, v171
	s_barrier
	s_waitcnt lgkmcnt(0)
	s_barrier
	ds_read_b64 v[122:123], v105 offset:0
	ds_read_b64 v[124:125], v105 offset:8
	ds_read_b64 v[126:127], v105 offset:16
	ds_read_b64 v[128:129], v105 offset:96
	ds_read_b64 v[130:131], v105 offset:104
	ds_read_b64 v[132:133], v105 offset:112
	s_waitcnt lgkmcnt(3)
	v_mfma_f32_16x16x128_f8f6f4 v[134:137], v[122:127], v[2:7], 0 cbsz:2 blgp:2
	v_mfma_f32_16x16x128_f8f6f4 v[138:141], v[122:127], v[14:19], 0 cbsz:2 blgp:2
	v_mfma_f32_16x16x128_f8f6f4 v[142:145], v[122:127], v[26:31], v[188:191] cbsz:2 blgp:2
	v_mfma_f32_16x16x128_f8f6f4 v[204:207], v[122:127], v[38:43], 0 cbsz:2 blgp:2
	v_mfma_f32_16x16x128_f8f6f4 v[208:211], v[122:127], v[50:55], 0 cbsz:2 blgp:2
	v_mfma_f32_16x16x128_f8f6f4 v[212:215], v[122:127], v[62:67], v[188:191] cbsz:2 blgp:2
	s_waitcnt lgkmcnt(0)
	v_mfma_f32_16x16x128_f8f6f4 v[134:137], v[128:133], v[8:13], v[134:137] cbsz:2 blgp:2
	v_mfma_f32_16x16x128_f8f6f4 v[204:207], v[128:133], v[44:49], v[204:207] cbsz:2 blgp:2
	v_mfma_f32_16x16x128_f8f6f4 v[138:141], v[128:133], v[20:25], v[138:141] cbsz:2 blgp:2
	v_mfma_f32_16x16x128_f8f6f4 v[208:211], v[128:133], v[56:61], v[208:211] cbsz:2 blgp:2
	v_mfma_f32_16x16x128_f8f6f4 v[142:145], v[128:133], v[32:37], v[142:145] cbsz:2 blgp:2
	v_mfma_f32_16x16x128_f8f6f4 v[212:215], v[128:133], v[68:73], v[212:215] cbsz:2 blgp:2
	v_cndmask_b32_e64 v158, v134, v204, s[0:1]
	v_fma_mix_f32 v158, v158, v100, v148 op_sel_hi:[0,0,1]
	v_exp_f32_e32 v158, v158
	v_cndmask_b32_e64 v159, v138, v208, s[0:1]
	v_fma_mix_f32 v159, v159, v101, v152 op_sel_hi:[0,0,1]
	v_exp_f32_e32 v159, v159
	v_fma_f32 v158, v158, v186, v186
	v_rcp_f32_e32 v158, v158
	v_add_f32_e32 v159, 1.0, v159
	v_rcp_f32_e32 v159, v159
	v_cndmask_b32_e64 v160, v142, v212, s[0:1]
	v_fma_mix_f32 v161, v158, v160, v156 op_sel_hi:[0,0,1]
	v_exp_f32_e32 v161, v161
	s_add_u32 s48, s48, s40
	v_add_f32_e32 v161, 1.0, v161
	v_rcp_f32_e32 v161, v161
	s_addc_u32 s49, s49, s41
	v_fma_f32 v162, v161, -2.0, 1.0
	v_sub_f32_e32 v163, v176, v162
	v_fma_f32 v176, v159, v163, v162
	v_fma_f32 v164, |v176|, s17, v113
	v_fma_f32 v165, |v176|, s18, v114
	v_fma_f32 v166, |v176|, s19, v115
	v_lshrrev_b32_e32 v167, 26, v176
	v_min3_u32 v164, v164, v165, v166
	v_bfi_b32 v168, 31, v164, v167
	global_store_short_d16_hi v185, v176, s[48:49]
	s_nop 0
	v_mul_u32_u24_dpp v170, v168, v180 quad_perm:[1,2,3,3] row_mask:0xf bank_mask:0xf bound_ctrl:1
	v_mad_u32_u24 v171, v168, v181, v170
	ds_write_b8_d16_hi v184, v171 offset:416
	s_barrier
	s_waitcnt lgkmcnt(0)
	s_barrier
	ds_read_b64 v[122:123], v105 offset:416
	ds_read_b64 v[124:125], v105 offset:424
	ds_read_b64 v[126:127], v105 offset:432
	ds_read_b64 v[128:129], v105 offset:512
	ds_read_b64 v[130:131], v105 offset:520
	ds_read_b64 v[132:133], v105 offset:528
	s_waitcnt lgkmcnt(3)
	v_mfma_f32_16x16x128_f8f6f4 v[134:137], v[122:127], v[2:7], 0 cbsz:2 blgp:2
	v_mfma_f32_16x16x128_f8f6f4 v[138:141], v[122:127], v[14:19], 0 cbsz:2 blgp:2
	v_mfma_f32_16x16x128_f8f6f4 v[142:145], v[122:127], v[26:31], v[188:191] cbsz:2 blgp:2
	v_mfma_f32_16x16x128_f8f6f4 v[204:207], v[122:127], v[38:43], 0 cbsz:2 blgp:2
	v_mfma_f32_16x16x128_f8f6f4 v[208:211], v[122:127], v[50:55], 0 cbsz:2 blgp:2
	v_mfma_f32_16x16x128_f8f6f4 v[212:215], v[122:127], v[62:67], v[188:191] cbsz:2 blgp:2
	s_waitcnt lgkmcnt(0)
	v_mfma_f32_16x16x128_f8f6f4 v[134:137], v[128:133], v[8:13], v[134:137] cbsz:2 blgp:2
	v_mfma_f32_16x16x128_f8f6f4 v[204:207], v[128:133], v[44:49], v[204:207] cbsz:2 blgp:2
	v_mfma_f32_16x16x128_f8f6f4 v[138:141], v[128:133], v[20:25], v[138:141] cbsz:2 blgp:2
	v_mfma_f32_16x16x128_f8f6f4 v[208:211], v[128:133], v[56:61], v[208:211] cbsz:2 blgp:2
	v_mfma_f32_16x16x128_f8f6f4 v[142:145], v[128:133], v[32:37], v[142:145] cbsz:2 blgp:2
	v_mfma_f32_16x16x128_f8f6f4 v[212:215], v[128:133], v[68:73], v[212:215] cbsz:2 blgp:2
	v_cndmask_b32_e64 v158, v134, v204, s[0:1]
	v_fma_mix_f32 v158, v158, v100, v148 op_sel:[0,0,1] op_sel_hi:[0,0,1]
	v_exp_f32_e32 v158, v158
	v_cndmask_b32_e64 v159, v138, v208, s[0:1]
	v_fma_mix_f32 v159, v159, v101, v152 op_sel:[0,0,1] op_sel_hi:[0,0,1]
	v_exp_f32_e32 v159, v159
	v_fma_f32 v158, v158, v186, v186
	v_rcp_f32_e32 v158, v158
	v_add_f32_e32 v159, 1.0, v159
	v_rcp_f32_e32 v159, v159
	v_cndmask_b32_e64 v160, v142, v212, s[0:1]
	v_fma_mix_f32 v161, v158, v160, v156 op_sel:[0,0,1] op_sel_hi:[0,0,1]
	v_exp_f32_e32 v161, v161
	s_add_u32 s48, s48, s40
	v_add_f32_e32 v161, 1.0, v161
	v_rcp_f32_e32 v161, v161
	s_addc_u32 s49, s49, s41
	v_fma_f32 v162, v161, -2.0, 1.0
	v_sub_f32_e32 v163, v176, v162
	v_fma_f32 v176, v159, v163, v162
	v_fma_f32 v164, |v176|, s17, v113
	v_fma_f32 v165, |v176|, s18, v114
	v_fma_f32 v166, |v176|, s19, v115
	v_lshrrev_b32_e32 v167, 26, v176
	v_min3_u32 v164, v164, v165, v166
	v_bfi_b32 v168, 31, v164, v167
	global_store_short_d16_hi v185, v176, s[48:49]
	s_nop 0
	v_mul_u32_u24_dpp v170, v168, v180 quad_perm:[1,2,3,3] row_mask:0xf bank_mask:0xf bound_ctrl:1
	v_mad_u32_u24 v171, v168, v181, v170
	ds_write_b8_d16_hi v184, v171
	s_barrier
	s_waitcnt lgkmcnt(0)
	s_barrier
	ds_read_b64 v[122:123], v105 offset:0
	ds_read_b64 v[124:125], v105 offset:8
	ds_read_b64 v[126:127], v105 offset:16
	ds_read_b64 v[128:129], v105 offset:96
	ds_read_b64 v[130:131], v105 offset:104
	ds_read_b64 v[132:133], v105 offset:112
	s_waitcnt lgkmcnt(3)
	v_mfma_f32_16x16x128_f8f6f4 v[134:137], v[122:127], v[2:7], 0 cbsz:2 blgp:2
	v_mfma_f32_16x16x128_f8f6f4 v[138:141], v[122:127], v[14:19], 0 cbsz:2 blgp:2
	v_mfma_f32_16x16x128_f8f6f4 v[142:145], v[122:127], v[26:31], v[188:191] cbsz:2 blgp:2
	v_mfma_f32_16x16x128_f8f6f4 v[204:207], v[122:127], v[38:43], 0 cbsz:2 blgp:2
	v_mfma_f32_16x16x128_f8f6f4 v[208:211], v[122:127], v[50:55], 0 cbsz:2 blgp:2
	v_mfma_f32_16x16x128_f8f6f4 v[212:215], v[122:127], v[62:67], v[188:191] cbsz:2 blgp:2
	s_waitcnt lgkmcnt(0)
	v_mfma_f32_16x16x128_f8f6f4 v[134:137], v[128:133], v[8:13], v[134:137] cbsz:2 blgp:2
	v_mfma_f32_16x16x128_f8f6f4 v[204:207], v[128:133], v[44:49], v[204:207] cbsz:2 blgp:2
	v_mfma_f32_16x16x128_f8f6f4 v[138:141], v[128:133], v[20:25], v[138:141] cbsz:2 blgp:2
	v_mfma_f32_16x16x128_f8f6f4 v[208:211], v[128:133], v[56:61], v[208:211] cbsz:2 blgp:2
	v_mfma_f32_16x16x128_f8f6f4 v[142:145], v[128:133], v[32:37], v[142:145] cbsz:2 blgp:2
	v_mfma_f32_16x16x128_f8f6f4 v[212:215], v[128:133], v[68:73], v[212:215] cbsz:2 blgp:2
	v_cndmask_b32_e64 v158, v134, v204, s[0:1]
	v_fma_mix_f32 v158, v158, v100, v149 op_sel_hi:[0,0,1]
	v_exp_f32_e32 v158, v158
	v_cndmask_b32_e64 v159, v138, v208, s[0:1]
	v_fma_mix_f32 v159, v159, v101, v153 op_sel_hi:[0,0,1]
	v_exp_f32_e32 v159, v159
	v_fma_f32 v158, v158, v186, v186
	v_rcp_f32_e32 v158, v158
	v_add_f32_e32 v159, 1.0, v159
	v_rcp_f32_e32 v159, v159
	v_cndmask_b32_e64 v160, v142, v212, s[0:1]
	v_fma_mix_f32 v161, v158, v160, v157 op_sel_hi:[0,0,1]
	v_exp_f32_e32 v161, v161
	s_add_u32 s48, s48, s40
	v_add_f32_e32 v161, 1.0, v161
	v_rcp_f32_e32 v161, v161
	s_addc_u32 s49, s49, s41
	v_fma_f32 v162, v161, -2.0, 1.0
	v_sub_f32_e32 v163, v176, v162
	v_fma_f32 v176, v159, v163, v162
	v_fma_f32 v164, |v176|, s17, v113
	v_fma_f32 v165, |v176|, s18, v114
	v_fma_f32 v166, |v176|, s19, v115
	v_lshrrev_b32_e32 v167, 26, v176
	v_min3_u32 v164, v164, v165, v166
	v_bfi_b32 v168, 31, v164, v167
	global_store_short_d16_hi v185, v176, s[48:49]
	s_nop 0
	v_mul_u32_u24_dpp v170, v168, v180 quad_perm:[1,2,3,3] row_mask:0xf bank_mask:0xf bound_ctrl:1
	v_mad_u32_u24 v171, v168, v181, v170
	ds_write_b8_d16_hi v184, v171 offset:416
	s_barrier
	s_waitcnt lgkmcnt(0)
	s_barrier
	ds_read_b64 v[122:123], v105 offset:416
	ds_read_b64 v[124:125], v105 offset:424
	ds_read_b64 v[126:127], v105 offset:432
	ds_read_b64 v[128:129], v105 offset:512
	ds_read_b64 v[130:131], v105 offset:520
	ds_read_b64 v[132:133], v105 offset:528
	s_add_i32 s44, s44, 16
	s_waitcnt lgkmcnt(3)
	v_mfma_f32_16x16x128_f8f6f4 v[134:137], v[122:127], v[2:7], 0 cbsz:2 blgp:2
	v_mfma_f32_16x16x128_f8f6f4 v[138:141], v[122:127], v[14:19], 0 cbsz:2 blgp:2
	v_mfma_f32_16x16x128_f8f6f4 v[142:145], v[122:127], v[26:31], v[188:191] cbsz:2 blgp:2
	v_mfma_f32_16x16x128_f8f6f4 v[204:207], v[122:127], v[38:43], 0 cbsz:2 blgp:2
	v_mfma_f32_16x16x128_f8f6f4 v[208:211], v[122:127], v[50:55], 0 cbsz:2 blgp:2
	v_mfma_f32_16x16x128_f8f6f4 v[212:215], v[122:127], v[62:67], v[188:191] cbsz:2 blgp:2
	s_waitcnt lgkmcnt(0)
	v_mfma_f32_16x16x128_f8f6f4 v[134:137], v[128:133], v[8:13], v[134:137] cbsz:2 blgp:2
	v_mfma_f32_16x16x128_f8f6f4 v[204:207], v[128:133], v[44:49], v[204:207] cbsz:2 blgp:2
	v_mfma_f32_16x16x128_f8f6f4 v[138:141], v[128:133], v[20:25], v[138:141] cbsz:2 blgp:2
	v_mfma_f32_16x16x128_f8f6f4 v[208:211], v[128:133], v[56:61], v[208:211] cbsz:2 blgp:2
	v_mfma_f32_16x16x128_f8f6f4 v[142:145], v[128:133], v[32:37], v[142:145] cbsz:2 blgp:2
	v_mfma_f32_16x16x128_f8f6f4 v[212:215], v[128:133], v[68:73], v[212:215] cbsz:2 blgp:2
	v_cndmask_b32_e64 v158, v134, v204, s[0:1]
	v_fma_mix_f32 v158, v158, v100, v149 op_sel:[0,0,1] op_sel_hi:[0,0,1]
	v_exp_f32_e32 v158, v158
	v_cndmask_b32_e64 v159, v138, v208, s[0:1]
	v_fma_mix_f32 v159, v159, v101, v153 op_sel:[0,0,1] op_sel_hi:[0,0,1]
	v_exp_f32_e32 v159, v159
	v_fma_f32 v158, v158, v186, v186
	v_rcp_f32_e32 v158, v158
	v_add_f32_e32 v159, 1.0, v159
	v_rcp_f32_e32 v159, v159
	v_cndmask_b32_e64 v160, v142, v212, s[0:1]
	v_fma_mix_f32 v161, v158, v160, v157 op_sel:[0,0,1] op_sel_hi:[0,0,1]
	v_exp_f32_e32 v161, v161
	s_add_u32 s48, s48, s40
	v_add_f32_e32 v161, 1.0, v161
	v_rcp_f32_e32 v161, v161
	s_addc_u32 s49, s49, s41
	v_fma_f32 v162, v161, -2.0, 1.0
	v_sub_f32_e32 v163, v176, v162
	v_fma_f32 v176, v159, v163, v162
	v_fma_f32 v164, |v176|, s17, v113
	v_fma_f32 v165, |v176|, s18, v114
	v_fma_f32 v166, |v176|, s19, v115
	v_lshrrev_b32_e32 v167, 26, v176
	v_min3_u32 v164, v164, v165, v166
	v_bfi_b32 v168, 31, v164, v167
	global_store_short_d16_hi v185, v176, s[48:49]
	s_nop 0
	v_mul_u32_u24_dpp v170, v168, v180 quad_perm:[1,2,3,3] row_mask:0xf bank_mask:0xf bound_ctrl:1
	v_mad_u32_u24 v171, v168, v181, v170
	ds_write_b8_d16_hi v184, v171
	s_barrier
	s_cmp_lt_i32 s44, s45
	s_waitcnt lgkmcnt(0)
	s_barrier
	s_cbranch_scc1 .Lscan_loop_b_f2
